# nt cache hint on read-once global loads of P0 P4 P7 (x, o, h1, y rows)
# speedup vs baseline: 1.0068x; 1.0068x over previous
; #define LAS __attribute__((address_space(3)))
; __device__ __forceinline__ float shx(float v, int m, int lane) { return __int_as_float(__builtin_amdgcn_ds_bpermute((lane ^ m) << 2, __float_as_int(v))); }
; __device__ __forceinline__ void meta_task(const Ctx& c, int hs) {
;     ...
;     for (int rr = 0; rr < 2; ++rr) { const int row = 2 * wave + rr; const float* xr = p.meta + (size_t)row * DM; f32x4 v[4]; float s = 0.f;
; #pragma unroll
;         for (int j = 0; j < 4; ++j) { v[j] = ((const f32x4*)xr)[lane + 64 * j]; s += (v[j][0] * v[j][0] + v[j][1] * v[j][1]) + (v[j][2] * v[j][2] + v[j][3] * v[j][3]); }
; #pragma unroll
;         for (int o = 1; o < 64; o <<= 1) s += shx(s, o, lane);
;         const float rs = rsqrtf(s * (1.0f / DM) + EPS);
; #pragma unroll
;         for (int j = 0; j < 4; ++j) { const f32x4 g = ((const f32x4*)p.g_attn)[lane + 64 * j]; ((LAS f32x4*)(xm + row * DM))[lane + 64 * j] = v[j] * rs * g; } }
;     __syncthreads();
;     { float acc[16];
; #pragma unroll
;       for (int r = 0; r < 16; ++r) acc[r] = 0.f;
;       const float* wp = p.w_in + (size_t)(128 * wave) * INW + hc * 64 + lane;
.LBB7_22:
	v_writelane_b32 v254, s13, 42
	v_writelane_b32 v254, s12, 43
	v_writelane_b32 v254, s95, 44
	v_writelane_b32 v254, s92, 45
	s_or_b64 exec, exec, s[0:1]
	s_lshl_b32 s4, s94, 1
	s_mov_b32 s5, 0
	v_readlane_b32 s36, v254, 9
	s_lshl_b64 s[0:1], s[4:5], 12
	v_readlane_b32 s38, v254, 11
	v_readlane_b32 s39, v254, 12
	s_add_u32 s0, s38, s0
	v_ashrrev_i32_e32 v63, 31, v62
	s_addc_u32 s1, s39, s1
	v_lshlrev_b64 v[32:33], 4, v[62:63]
	v_lshl_add_u64 v[12:13], s[0:1], 0, v[32:33]
	global_load_dwordx4 v[0:3], v[12:13], off nt
	global_load_dwordx4 v[4:7], v[12:13], off offset:1024 nt
	global_load_dwordx4 v[8:11], v[12:13], off offset:3072 nt
	s_nop 0
	global_load_dwordx4 v[12:15], v[12:13], off offset:2048 nt
	s_lshl_b32 s0, s94, 13
	s_or_b32 s4, s4, 1
	s_add_i32 s0, s0, 0
	s_lshl_b64 s[6:7], s[4:5], 12
	s_add_u32 s6, s38, s6
	s_addc_u32 s7, s39, s7
	v_lshl_add_u64 v[28:29], s[6:7], 0, v[32:33]
	global_load_dwordx4 v[24:27], v[28:29], off nt
	global_load_dwordx4 v[20:23], v[28:29], off offset:1024 nt
	global_load_dwordx4 v[16:19], v[28:29], off offset:3072 nt
	s_nop 0
	global_load_dwordx4 v[28:31], v[28:29], off offset:2048 nt
	v_readlane_b32 s40, v254, 13
	v_readlane_b32 s41, v254, 14
	v_lshlrev_b32_e32 v61, 2, v62
	v_xor_b32_e32 v69, 4, v61
	v_lshl_add_u64 v[44:45], s[40:41], 0, v[32:33]
	global_load_dwordx4 v[32:35], v[44:45], off nt
	global_load_dwordx4 v[36:39], v[44:45], off offset:1024 nt
	global_load_dwordx4 v[40:43], v[44:45], off offset:2048 nt
	s_nop 0
	global_load_dwordx4 v[44:47], v[44:45], off offset:3072 nt
	s_mov_b32 s2, 0x3a800000
	s_mov_b32 s1, 0x800000
	v_readlane_b32 s42, v254, 15
	v_readlane_b32 s43, v254, 16
	s_mov_b32 s90, s94
	v_readlane_b32 s37, v254, 10
	v_readlane_b32 s44, v254, 17
	v_readlane_b32 s45, v254, 18
	v_readlane_b32 s46, v254, 19
	v_readlane_b32 s47, v254, 20
	v_readlane_b32 s48, v254, 21
	v_readlane_b32 s49, v254, 22
	v_readlane_b32 s50, v254, 23
	v_readlane_b32 s51, v254, 24
	s_waitcnt vmcnt(11)
	v_pk_mul_f32 v[48:49], v[2:3], v[2:3]
	v_pk_mul_f32 v[50:51], v[0:1], v[0:1]
	s_waitcnt vmcnt(10)
	v_pk_mul_f32 v[52:53], v[6:7], v[6:7]
	v_pk_mul_f32 v[54:55], v[4:5], v[4:5]
	s_waitcnt vmcnt(9)
	v_mul_f32_e32 v59, v10, v10
	s_waitcnt vmcnt(8)
	v_mul_f32_e32 v56, v13, v13
	v_mul_f32_e32 v58, v15, v15
	v_mul_f32_e32 v66, v11, v11
	v_pk_mov_b32 v[64:65], v[50:51], v[48:49] op_sel:[1,0]
	v_mov_b32_e32 v51, v49
	v_pk_mov_b32 v[48:49], v[54:55], v[52:53] op_sel:[1,0]
	v_mov_b32_e32 v55, v53
	v_pk_fma_f32 v[52:53], v[12:13], v[12:13], v[56:57] op_sel_hi:[1,1,0]
	v_pk_fma_f32 v[56:57], v[14:15], v[14:15], v[58:59] op_sel_hi:[1,1,0]
	v_pk_add_f32 v[50:51], v[64:65], v[50:51]
	v_pk_add_f32 v[48:49], v[48:49], v[54:55]
	v_mov_b32_e32 v53, v59
	v_mov_b32_e32 v57, v66
	v_mul_f32_e32 v67, v8, v8
	v_mul_f32_e32 v72, v9, v9
	v_pk_add_f32 v[52:53], v[52:53], v[56:57]
	s_waitcnt vmcnt(7)
	v_pk_mul_f32 v[54:55], v[26:27], v[26:27]
	v_pk_mul_f32 v[56:57], v[24:25], v[24:25]
	s_waitcnt vmcnt(6)
	v_pk_mul_f32 v[58:59], v[22:23], v[22:23]
	v_pk_mul_f32 v[64:65], v[20:21], v[20:21]
	v_pk_add_f32 v[50:51], v[50:51], v[50:51] op_sel:[0,1] op_sel_hi:[1,0]
	v_pk_add_f32 v[48:49], v[48:49], v[48:49] op_sel:[0,1] op_sel_hi:[1,0]
	v_pk_mov_b32 v[70:71], v[56:57], v[54:55] op_sel:[1,0]
	v_mov_b32_e32 v57, v55
	v_pk_mov_b32 v[54:55], v[64:65], v[58:59] op_sel:[1,0]
	v_mov_b32_e32 v65, v59
	v_mov_b32_e32 v51, v67
	v_mov_b32_e32 v49, v72
	s_waitcnt vmcnt(4)
	v_mul_f32_e32 v66, v29, v29
	v_mul_f32_e32 v68, v31, v31
	v_pk_add_f32 v[48:49], v[50:51], v[48:49]
	v_pk_add_f32 v[50:51], v[70:71], v[56:57]
	v_pk_add_f32 v[54:55], v[54:55], v[64:65]
	v_mul_f32_e32 v73, v18, v18
	v_mul_f32_e32 v74, v19, v19
	v_mul_f32_e32 v75, v16, v16
	v_mul_f32_e32 v76, v17, v17
	v_pk_fma_f32 v[58:59], v[28:29], v[28:29], v[66:67] op_sel_hi:[1,1,0]
	v_pk_fma_f32 v[66:67], v[30:31], v[30:31], v[68:69] op_sel_hi:[1,1,0]
	v_pk_add_f32 v[50:51], v[50:51], v[50:51] op_sel:[0,1] op_sel_hi:[1,0]
	v_pk_add_f32 v[54:55], v[54:55], v[54:55] op_sel:[0,1] op_sel_hi:[1,0]
	v_mov_b32_e32 v59, v73
	v_mov_b32_e32 v67, v74
	v_mov_b32_e32 v51, v75
	v_mov_b32_e32 v55, v76
	v_pk_add_f32 v[48:49], v[48:49], v[52:53]
	v_pk_add_f32 v[52:53], v[58:59], v[66:67]
	v_pk_add_f32 v[50:51], v[50:51], v[54:55]
	v_mov_b32_e32 v57, v48
	v_pk_add_f32 v[50:51], v[50:51], v[52:53]
	v_xor_b32_e32 v52, 8, v61
	v_mov_b32_e32 v56, v50
	v_mov_b32_e32 v48, v51
	v_pk_add_f32 v[48:49], v[56:57], v[48:49]
	ds_bpermute_b32 v51, v69, v49
	ds_bpermute_b32 v50, v69, v48
	v_lshlrev_b32_e32 v53, 4, v62
	v_add_u32_e32 v54, s0, v53
	s_waitcnt lgkmcnt(0)
; #define LAS __attribute__((address_space(3)))
; __device__ __forceinline__ float shx(float v, int m, int lane) { return __int_as_float(__builtin_amdgcn_ds_bpermute((lane ^ m) << 2, __float_as_int(v))); }
; __device__ __forceinline__ void meta_task(const Ctx& c, int hs) {
;     ...
; #pragma unroll
;         for (int o = 1; o < 64; o <<= 1) s += shx(s, o, lane);
;         const float rs = rsqrtf(s * (1.0f / DM) + EPS);
; #pragma unroll
;         for (int j = 0; j < 4; ++j) { const f32x4 g = ((const f32x4*)p.g_attn)[lane + 64 * j]; ((LAS f32x4*)(xm + row * DM))[lane + 64 * j] = v[j] * rs * g; } }
;     __syncthreads();
;     { float acc[16];
; #pragma unroll
;       for (int r = 0; r < 16; ++r) acc[r] = 0.f;
	v_pk_add_f32 v[48:49], v[48:49], v[50:51]
	ds_bpermute_b32 v51, v52, v49
	ds_bpermute_b32 v50, v52, v48
	v_xor_b32_e32 v52, 16, v61
	s_waitcnt lgkmcnt(0)
	v_pk_add_f32 v[48:49], v[48:49], v[50:51]
	ds_bpermute_b32 v51, v52, v49
	ds_bpermute_b32 v50, v52, v48
	v_xor_b32_e32 v52, 32, v61
	s_waitcnt lgkmcnt(0)
	v_pk_add_f32 v[48:49], v[48:49], v[50:51]
	ds_bpermute_b32 v51, v52, v49
	ds_bpermute_b32 v50, v52, v48
	v_xor_b32_e32 v52, 64, v61
	s_waitcnt lgkmcnt(0)
	v_pk_add_f32 v[48:49], v[48:49], v[50:51]
	ds_bpermute_b32 v51, v52, v49
	ds_bpermute_b32 v50, v52, v48
	v_xor_b32_e32 v52, 0x80, v61
	s_waitcnt lgkmcnt(0)
	v_pk_add_f32 v[48:49], v[48:49], v[50:51]
	ds_bpermute_b32 v51, v52, v49
	ds_bpermute_b32 v50, v52, v48
	v_mov_b32_e32 v52, 0x358637bd
	s_waitcnt lgkmcnt(0)
	v_pk_add_f32 v[48:49], v[48:49], v[50:51]
	s_nop 0
	v_pk_fma_f32 v[48:49], v[48:49], s[2:3], v[52:53] op_sel_hi:[1,0,0]
	s_nop 0
	v_mul_f32_e32 v50, 0x4b800000, v49
	v_cmp_gt_f32_e32 vcc, s1, v49
	v_mul_f32_e32 v51, 0x4b800000, v48
	v_cmp_gt_f32_e64 s[0:1], s1, v48
	v_cndmask_b32_e32 v49, v49, v50, vcc
	v_rsq_f32_e32 v49, v49
	v_cndmask_b32_e64 v48, v48, v51, s[0:1]
	v_rsq_f32_e32 v52, v48
	v_mul_f32_e32 v48, 0x45800000, v49
	v_cndmask_b32_e32 v48, v49, v48, vcc
	v_pk_mul_f32 v[0:1], v[0:1], v[48:49] op_sel_hi:[1,0]
	v_pk_mul_f32 v[2:3], v[2:3], v[48:49] op_sel_hi:[1,0]
	v_pk_mul_f32 v[4:5], v[4:5], v[48:49] op_sel_hi:[1,0]
	v_pk_mul_f32 v[6:7], v[6:7], v[48:49] op_sel_hi:[1,0]
	v_pk_mul_f32 v[12:13], v[12:13], v[48:49] op_sel_hi:[1,0]
	v_pk_mul_f32 v[14:15], v[14:15], v[48:49] op_sel_hi:[1,0]
	s_waitcnt vmcnt(3)
	v_pk_mul_f32 v[2:3], v[34:35], v[2:3]
	v_pk_mul_f32 v[0:1], v[32:33], v[0:1]
	v_pk_mul_f32 v[50:51], v[8:9], v[48:49] op_sel_hi:[1,0]
	v_pk_mul_f32 v[48:49], v[10:11], v[48:49] op_sel_hi:[1,0]
	s_waitcnt vmcnt(2)
	v_pk_mul_f32 v[6:7], v[38:39], v[6:7]
	v_pk_mul_f32 v[4:5], v[36:37], v[4:5]
	s_waitcnt vmcnt(1)
	v_pk_mul_f32 v[10:11], v[42:43], v[14:15]
	v_pk_mul_f32 v[8:9], v[40:41], v[12:13]
	ds_write_b128 v54, v[0:3]
	ds_write_b128 v54, v[4:7] offset:1024
	ds_write_b128 v54, v[8:11] offset:2048
	v_mul_f32_e32 v0, 0x45800000, v52
	v_cndmask_b32_e64 v4, v52, v0, s[0:1]
	s_lshl_b32 s0, s4, 12
	s_add_i32 s0, s0, 0
	v_pk_mul_f32 v[0:1], v[24:25], v[4:5] op_sel_hi:[1,0]
	v_pk_mul_f32 v[2:3], v[26:27], v[4:5] op_sel_hi:[1,0]
	v_pk_mul_f32 v[0:1], v[32:33], v[0:1]
	v_pk_mul_f32 v[2:3], v[34:35], v[2:3]
	v_add_u32_e32 v5, s0, v53
	s_lshl_b32 s0, s94, 7
	s_mul_i32 s1, s94, 0x120000
	ds_write_b128 v5, v[0:3]
	v_pk_mul_f32 v[0:1], v[20:21], v[4:5] op_sel_hi:[1,0]
	v_pk_mul_f32 v[2:3], v[22:23], v[4:5] op_sel_hi:[1,0]
	s_mul_hi_u32 s0, s0, 0x2400
	s_add_u32 s2, s42, s1
	v_pk_mul_f32 v[2:3], v[38:39], v[2:3]
	v_pk_mul_f32 v[0:1], v[36:37], v[0:1]
	s_addc_u32 s4, s43, s0
	s_lshl_b32 s0, s88, 6
	ds_write_b128 v5, v[0:3] offset:1024
	v_pk_mul_f32 v[0:1], v[28:29], v[4:5] op_sel_hi:[1,0]
	v_pk_mul_f32 v[2:3], v[30:31], v[4:5] op_sel_hi:[1,0]
	s_ashr_i32 s1, s0, 31
	v_pk_mul_f32 v[2:3], v[42:43], v[2:3]
	v_pk_mul_f32 v[0:1], v[40:41], v[0:1]
	s_lshl_b64 s[0:1], s[0:1], 2
	ds_write_b128 v5, v[0:3] offset:2048
	v_pk_mul_f32 v[0:1], v[16:17], v[4:5] op_sel_hi:[1,0]
	v_pk_mul_f32 v[2:3], v[18:19], v[4:5] op_sel_hi:[1,0]
	s_add_u32 s0, s2, s0
	s_waitcnt vmcnt(0)
	v_pk_mul_f32 v[2:3], v[46:47], v[2:3]
	v_pk_mul_f32 v[0:1], v[44:45], v[0:1]
	s_addc_u32 s1, s4, s1
	ds_write_b128 v5, v[0:3] offset:3072
	v_lshl_add_u64 v[4:5], v[62:63], 2, s[0:1]
	s_lshl_b32 s0, s94, 9
	v_mov_b32_e32 v2, 0
	v_pk_mul_f32 v[12:13], v[46:47], v[48:49]
	v_pk_mul_f32 v[10:11], v[44:45], v[50:51]
	s_add_i32 s0, s0, 0
	s_mov_b32 s1, 0
	v_mov_b32_e32 v3, v2
	v_mov_b32_e32 v0, v2
	v_mov_b32_e32 v1, v2
	v_mov_b32_e32 v26, v2
	v_mov_b32_e32 v27, v2
	v_mov_b32_e32 v28, v2
	v_mov_b32_e32 v29, v2
	v_mov_b32_e32 v30, v2
	v_mov_b32_e32 v31, v2
	v_mov_b32_e32 v32, v2
	v_mov_b32_e32 v33, v2
	v_mov_b32_e32 v34, v2
	v_mov_b32_e32 v35, v2
	v_mov_b32_e32 v56, v2
	v_mov_b32_e32 v57, v2
	ds_write_b128 v54, v[10:13] offset:3072
	s_waitcnt lgkmcnt(0)
	s_barrier

; __device__ __forceinline__ void headpost(const P& p, int r, int hc, float* v, const float2* cs64, const float2* cs32) {
;     ...
;         const bool isq = hc < 20; if (isq && meta) return;
;         const float* g = isq ? p.g_q_diff : p.g_k_diff;
;         for (int hf = 0; hf < 2; ++hf) { float* w = v + 32 * hf;
;             float ss = 0.f; for (int d = 0; d < 32; ++d) ss += w[d] * w[d];
;             const float rs = rsqrtf(ss * (1.0f / 32.0f) + EPS);
;             for (int d = 0; d < 32; ++d) w[d] = w[d] * rs * g[d];
.LBB7_66:
	s_and_b64 vcc, exec, s[8:9]
	s_cbranch_vccz .LBB7_81
	s_cmp_lt_u32 s88, 20
	s_cselect_b64 s[72:73], -1, 0
	s_cmp_gt_u32 s88, 19
	s_cselect_b64 s[12:13], -1, 0
	s_and_b64 s[8:9], s[72:73], s[4:5]
	s_mov_b64 s[10:11], -1
	s_xor_b64 s[14:15], s[8:9], -1
	s_and_saveexec_b64 s[8:9], s[14:15]
	s_cbranch_execz .LBB7_80
	v_readlane_b32 s36, v254, 9
	s_and_b64 s[14:15], s[72:73], exec
	v_readlane_b32 s48, v254, 21
	v_readlane_b32 s49, v254, 22
	v_readlane_b32 s50, v254, 23
	v_readlane_b32 s51, v254, 24
	s_cselect_b32 s73, s49, s51
	s_cselect_b32 s72, s48, s50
	v_mov_b32_e32 v100, 0
	global_load_dwordx4 v[8:11], v100, s[72:73] offset:16 nt
	global_load_dwordx4 v[4:7], v100, s[72:73] nt
	global_load_dwordx4 v[0:3], v100, s[72:73] offset:64 nt
	ds_read_b128 v[28:31], v61 offset:64
	ds_read_b128 v[20:23], v61 offset:80
	ds_read_b128 v[40:43], v61
	ds_read_b128 v[36:39], v61 offset:16
	ds_read_b128 v[16:19], v61 offset:96
	ds_read_b128 v[32:35], v61 offset:32
	ds_read_b128 v[24:27], v61 offset:48
	ds_read_b96 v[56:58], v61 offset:128
	ds_read_b128 v[12:15], v61 offset:112
	ds_read2_b32 v[66:67], v61 offset0:35 offset1:36
	s_waitcnt lgkmcnt(7)
	v_mov_b32_e32 v47, v41
	v_mov_b32_e32 v49, v40
	s_waitcnt lgkmcnt(2)
	v_mov_b32_e32 v46, v56
	v_mov_b32_e32 v68, v57
	v_mov_b32_e32 v69, v58
	v_pk_mul_f32 v[46:47], v[46:47], v[46:47]
	v_mov_b32_e32 v48, v57
	v_pk_fma_f32 v[46:47], v[48:49], v[48:49], v[46:47]
	v_pk_mov_b32 v[48:49], v[68:69], v[42:43] op_sel:[1,0]
	s_waitcnt lgkmcnt(0)
	v_pk_mov_b32 v[82:83], v[66:67], v[36:37] op_sel:[1,0]
	v_pk_fma_f32 v[46:47], v[48:49], v[48:49], v[46:47]
	v_mov_b32_e32 v48, v66
	v_mov_b32_e32 v49, v43
	v_pk_fma_f32 v[46:47], v[48:49], v[48:49], v[46:47]
	ds_read2_b32 v[58:59], v61 offset0:53 offset1:54
	ds_read2_b32 v[64:65], v61 offset0:55 offset1:56
	ds_read2_b32 v[76:77], v61 offset0:37 offset1:38
	ds_read2_b32 v[74:75], v61 offset0:39 offset1:40
	ds_read2_b32 v[78:79], v61 offset0:41 offset1:42
	ds_read2_b32 v[80:81], v61 offset0:43 offset1:44
	ds_read2_b32 v[70:71], v61 offset0:57 offset1:58
	ds_read2_b32 v[72:73], v61 offset0:59 offset1:60
	v_pk_fma_f32 v[46:47], v[82:83], v[82:83], v[46:47]
	s_waitcnt lgkmcnt(5)
	v_mov_b32_e32 v48, v76
	v_mov_b32_e32 v49, v37
	v_pk_mov_b32 v[82:83], v[76:77], v[38:39] op_sel:[1,0]
	v_pk_fma_f32 v[46:47], v[48:49], v[48:49], v[46:47]
	s_waitcnt lgkmcnt(4)
	v_mov_b32_e32 v48, v74
	v_pk_fma_f32 v[46:47], v[82:83], v[82:83], v[46:47]
	v_mov_b32_e32 v49, v39
	v_pk_mov_b32 v[82:83], v[74:75], v[32:33] op_sel:[1,0]
	v_pk_fma_f32 v[46:47], v[48:49], v[48:49], v[46:47]
	s_waitcnt lgkmcnt(3)
	v_mov_b32_e32 v48, v78
	v_pk_fma_f32 v[46:47], v[82:83], v[82:83], v[46:47]
	v_mov_b32_e32 v49, v33
	v_pk_mov_b32 v[82:83], v[78:79], v[34:35] op_sel:[1,0]
	v_pk_fma_f32 v[46:47], v[48:49], v[48:49], v[46:47]
	s_waitcnt lgkmcnt(2)
	v_mov_b32_e32 v48, v80
	v_pk_fma_f32 v[46:47], v[82:83], v[82:83], v[46:47]
	ds_read2_b32 v[88:89], v61 offset0:45 offset1:46
	ds_read2_b32 v[84:85], v61 offset0:49 offset1:50
	ds_read2_b32 v[82:83], v61 offset0:51 offset1:52
	ds_read2_b32 v[86:87], v61 offset0:47 offset1:48
	v_mov_b32_e32 v49, v35
	v_pk_mov_b32 v[54:55], v[80:81], v[24:25] op_sel:[1,0]
	v_pk_fma_f32 v[46:47], v[48:49], v[48:49], v[46:47]
	s_waitcnt lgkmcnt(3)
	v_mov_b32_e32 v48, v88
	v_pk_fma_f32 v[46:47], v[54:55], v[54:55], v[46:47]
	v_mov_b32_e32 v49, v25
	v_pk_fma_f32 v[46:47], v[48:49], v[48:49], v[46:47]
	v_pk_mov_b32 v[48:49], v[88:89], v[26:27] op_sel:[1,0]
	v_pk_mov_b32 v[50:51], v[58:59], v[64:65] op_sel:[1,0]
	v_pk_fma_f32 v[46:47], v[48:49], v[48:49], v[46:47]
	s_waitcnt lgkmcnt(0)
	v_mov_b32_e32 v48, v86
	v_mov_b32_e32 v49, v27
	v_pk_fma_f32 v[46:47], v[48:49], v[48:49], v[46:47]
	v_pk_mov_b32 v[48:49], v[86:87], v[28:29] op_sel:[1,0]
	v_pk_mul_f32 v[44:45], v[22:23], v[22:23]
	v_pk_fma_f32 v[46:47], v[48:49], v[48:49], v[46:47]
	v_mov_b32_e32 v48, v84
	v_mov_b32_e32 v49, v29
	v_pk_fma_f32 v[46:47], v[48:49], v[48:49], v[46:47]
	v_pk_mov_b32 v[48:49], v[84:85], v[30:31] op_sel:[1,0]
	v_pk_mul_f32 v[50:51], v[50:51], v[50:51]
	v_pk_fma_f32 v[46:47], v[48:49], v[48:49], v[46:47]
	v_mov_b32_e32 v48, v82
	v_mov_b32_e32 v49, v31
	v_pk_fma_f32 v[46:47], v[48:49], v[48:49], v[46:47]
	v_pk_mov_b32 v[48:49], v[82:83], v[20:21] op_sel:[1,0]
	v_pk_mul_f32 v[52:53], v[16:17], v[16:17]
	v_pk_fma_f32 v[46:47], v[48:49], v[48:49], v[46:47]
	v_mov_b32_e32 v48, v58
	v_mov_b32_e32 v49, v21
	v_pk_fma_f32 v[46:47], v[48:49], v[48:49], v[46:47]
	v_mov_b32_e32 v48, v50
	v_mov_b32_e32 v49, v44
	v_pk_add_f32 v[46:47], v[46:47], v[48:49]
	v_pk_mov_b32 v[48:49], v[64:65], v[70:71] op_sel:[1,0]
	v_mov_b32_e32 v44, v51
	v_pk_mul_f32 v[54:55], v[48:49], v[48:49]
	v_pk_add_f32 v[92:93], v[46:47], v[44:45]
	v_mov_b32_e32 v102, v54
	v_mov_b32_e32 v103, v52
	v_pk_add_f32 v[102:103], v[92:93], v[102:103]
	v_pk_mov_b32 v[92:93], v[70:71], v[72:73] op_sel:[1,0]
	v_pk_mul_f32 v[90:91], v[18:19], v[18:19]
	v_pk_mul_f32 v[104:105], v[92:93], v[92:93]
	ds_read2_b32 v[92:93], v61 offset0:61 offset1:62
	v_mov_b32_e32 v52, v55
	global_load_dwordx4 v[48:51], v100, s[72:73] offset:32 nt
	global_load_dwordx4 v[44:47], v100, s[72:73] offset:48 nt
	v_pk_add_f32 v[102:103], v[102:103], v[52:53]
	global_load_dwordx4 v[52:55], v100, s[72:73] offset:80 nt
	v_mov_b32_e32 v106, v104
	v_mov_b32_e32 v107, v90
	v_mov_b32_e32 v90, v105
	ds_read2_b32 v[104:105], v61 offset0:62 offset1:63
	ds_read_b32 v57, v61 offset:252
	v_pk_add_f32 v[102:103], v[102:103], v[106:107]
	s_waitcnt lgkmcnt(2)
; __device__ __forceinline__ bf16_t f2bf(float f) { unsigned u = __float_as_uint(f); u += 0x7fffu + ((u >> 16) & 1u); return (bf16_t)(u >> 16); }
; __device__ __forceinline__ void headpost(const P& p, int r, int hc, float* v, const float2* cs64, const float2* cs32) {
;     ...
;             float ss = 0.f; for (int d = 0; d < 32; ++d) ss += w[d] * w[d];
;             const float rs = rsqrtf(ss * (1.0f / 32.0f) + EPS);
;             for (int d = 0; d < 32; ++d) w[d] = w[d] * rs * g[d];
;             for (int i = 0; i < 16; ++i) { const float2 cs = cs32[i]; const float a = w[i], c = w[i + 16]; w[i] = a * cs.x - c * cs.y; w[i + 16] = c * cs.x + a * cs.y; } }
;         if (isq) { const int h = hc - 12; bf16_t* q = QB + ((size_t)(b * 8 + h) * SEQ + tok) * 64; for (int d = 0; d < 64; ++d) q[(d & 32) + bslot(d & 31)] = f2bf(v[d] * QSCALE_B); }
	v_pk_mov_b32 v[106:107], v[72:73], v[92:93] op_sel:[1,0]
	v_pk_mul_f32 v[94:95], v[12:13], v[12:13]
	v_pk_mul_f32 v[106:107], v[106:107], v[106:107]
	v_pk_add_f32 v[90:91], v[102:103], v[90:91]
	v_mov_b32_e32 v102, v106
	v_mov_b32_e32 v103, v94
	v_pk_add_f32 v[90:91], v[90:91], v[102:103]
	v_pk_mul_f32 v[102:103], v[14:15], v[14:15]
	s_waitcnt lgkmcnt(1)
	v_pk_mul_f32 v[104:105], v[104:105], v[104:105]
	v_mov_b32_e32 v94, v107
	v_pk_add_f32 v[90:91], v[90:91], v[94:95]
	v_mov_b32_e32 v94, v104
	v_mov_b32_e32 v95, v102
	v_pk_add_f32 v[90:91], v[90:91], v[94:95]
	v_mov_b32_e32 v102, v105
	v_pk_add_f32 v[90:91], v[90:91], v[102:103]
	s_mov_b32 s2, 0x3d000000
	v_mov_b32_e32 v94, 0x358637bd
	v_pk_fma_f32 v[90:91], v[90:91], s[2:3], v[94:95] op_sel_hi:[1,0,0]
	s_mov_b32 s2, 0x800000
	v_mul_f32_e32 v94, 0x4b800000, v91
	v_cmp_gt_f32_e32 vcc, s2, v91
	global_load_dwordx4 v[102:105], v100, s[72:73] offset:96 nt
	v_readlane_b32 s37, v254, 10
	v_cndmask_b32_e32 v91, v91, v94, vcc
	v_rsq_f32_e32 v91, v91
	v_lshl_add_u32 v94, v60, 7, 0
	v_add_u32_e32 v95, 0x11000, v94
	v_readlane_b32 s38, v254, 11
	v_mul_f32_e32 v94, 0x45800000, v91
	v_cndmask_b32_e32 v94, v91, v94, vcc
	v_pk_mul_f32 v[40:41], v[40:41], v[94:95] op_sel_hi:[1,0]
	v_pk_mul_f32 v[42:43], v[42:43], v[94:95] op_sel_hi:[1,0]
	s_waitcnt vmcnt(5)
	v_pk_mul_f32 v[40:41], v[4:5], v[40:41]
	v_pk_mul_f32 v[42:43], v[6:7], v[42:43]
	ds_write_b128 v61, v[40:43]
	ds_read_b128 v[106:109], v95
	v_pk_mul_f32 v[36:37], v[36:37], v[94:95] op_sel_hi:[1,0]
	v_pk_mul_f32 v[38:39], v[38:39], v[94:95] op_sel_hi:[1,0]
	v_pk_mul_f32 v[36:37], v[8:9], v[36:37]
	v_pk_mul_f32 v[38:39], v[38:39], v[10:11]
	ds_write_b128 v61, v[36:39] offset:16
	v_pk_mul_f32 v[28:29], v[28:29], v[94:95] op_sel_hi:[1,0]
	v_pk_mul_f32 v[110:111], v[30:31], v[94:95] op_sel_hi:[1,0]
	s_waitcnt vmcnt(4)
	v_pk_mul_f32 v[114:115], v[28:29], v[0:1]
	ds_read_b128 v[28:31], v95 offset:16
	s_waitcnt lgkmcnt(2)
	v_mov_b32_e32 v117, v108
	v_mov_b32_e32 v108, v107
	v_mov_b32_e32 v116, v106
	v_pk_mul_f32 v[112:113], v[114:115], v[108:109]
	v_pk_mul_f32 v[118:119], v[40:41], v[108:109]
	global_load_dwordx4 v[106:109], v100, s[72:73] offset:112 nt
	v_pk_mul_f32 v[32:33], v[32:33], v[94:95] op_sel_hi:[1,0]
	v_pk_mul_f32 v[34:35], v[34:35], v[94:95] op_sel_hi:[1,0]
	v_pk_mul_f32 v[24:25], v[24:25], v[94:95] op_sel_hi:[1,0]
	v_pk_mul_f32 v[26:27], v[26:27], v[94:95] op_sel_hi:[1,0]
	v_pk_mul_f32 v[120:121], v[110:111], v[2:3]
	s_waitcnt lgkmcnt(0)
	v_mov_b32_e32 v123, v30
	v_mov_b32_e32 v30, v29
	v_mov_b32_e32 v122, v28
	v_pk_mul_f32 v[28:29], v[120:121], v[30:31]
	v_pk_mul_f32 v[20:21], v[20:21], v[94:95] op_sel_hi:[1,0]
	v_pk_fma_f32 v[110:111], v[40:41], v[116:117], v[112:113] neg_lo:[0,0,1] neg_hi:[0,0,1]
	v_pk_fma_f32 v[112:113], v[42:43], v[122:123], v[28:29] neg_lo:[0,0,1] neg_hi:[0,0,1]
	v_pk_mul_f32 v[30:31], v[42:43], v[30:31]
	v_pk_fma_f32 v[28:29], v[114:115], v[116:117], v[118:119]
	v_pk_mul_f32 v[100:101], v[22:23], v[94:95] op_sel_hi:[1,0]
	v_pk_fma_f32 v[30:31], v[120:121], v[122:123], v[30:31]
	v_pk_mul_f32 v[16:17], v[16:17], v[94:95] op_sel_hi:[1,0]
	v_pk_mul_f32 v[12:13], v[12:13], v[94:95] op_sel_hi:[1,0]
	v_pk_mul_f32 v[14:15], v[14:15], v[94:95] op_sel_hi:[1,0]
	s_waitcnt vmcnt(4)
	v_pk_mul_f32 v[32:33], v[32:33], v[48:49]
	v_pk_mul_f32 v[34:35], v[34:35], v[50:51]
	s_waitcnt vmcnt(3)
	v_pk_mul_f32 v[24:25], v[24:25], v[44:45]
	v_pk_mul_f32 v[26:27], v[26:27], v[46:47]
	ds_write_b128 v61, v[32:35] offset:32
	ds_write_b128 v61, v[24:27] offset:48
	ds_read_b128 v[40:43], v95 offset:32
	s_waitcnt vmcnt(2)
	v_pk_mul_f32 v[114:115], v[20:21], v[52:53]
	ds_read_b128 v[20:23], v95 offset:48
	v_pk_mul_f32 v[100:101], v[100:101], v[54:55]
	v_cmp_gt_f32_e32 vcc, s2, v90
	s_waitcnt lgkmcnt(1)
	v_mov_b32_e32 v117, v42
	v_mov_b32_e32 v42, v41
	s_waitcnt lgkmcnt(0)
	v_mov_b32_e32 v121, v22
	v_mov_b32_e32 v22, v21
	v_mov_b32_e32 v116, v40
	v_pk_mul_f32 v[118:119], v[36:37], v[42:43]
	v_mov_b32_e32 v120, v20
	v_pk_mul_f32 v[20:21], v[100:101], v[22:23]
	v_pk_mul_f32 v[22:23], v[38:39], v[22:23]
	v_pk_mul_f32 v[40:41], v[114:115], v[42:43]
	v_pk_fma_f32 v[42:43], v[38:39], v[120:121], v[20:21] neg_lo:[0,0,1] neg_hi:[0,0,1]
	v_pk_fma_f32 v[20:21], v[114:115], v[116:117], v[118:119]
	v_pk_fma_f32 v[22:23], v[100:101], v[120:121], v[22:23]
	ds_write_b128 v61, v[28:31] offset:64
	ds_write_b128 v61, v[20:23] offset:80
	ds_read_b128 v[20:23], v95 offset:64
	v_pk_mul_f32 v[28:29], v[18:19], v[94:95] op_sel_hi:[1,0]
	v_pk_fma_f32 v[40:41], v[36:37], v[116:117], v[40:41] neg_lo:[0,0,1] neg_hi:[0,0,1]
	ds_write_b128 v61, v[110:113]
	v_readlane_b32 s39, v254, 12
	v_readlane_b32 s40, v254, 13
	s_waitcnt vmcnt(1)
	v_pk_mul_f32 v[30:31], v[16:17], v[102:103]
	ds_read_b128 v[16:19], v95 offset:80
	s_waitcnt lgkmcnt(2)
	v_mov_b32_e32 v37, v22
	v_mov_b32_e32 v22, v21
	v_pk_mul_f32 v[28:29], v[28:29], v[104:105]
	v_mov_b32_e32 v36, v20
	s_waitcnt lgkmcnt(0)
	v_mov_b32_e32 v101, v18
	v_mov_b32_e32 v18, v17
	v_pk_mul_f32 v[38:39], v[32:33], v[22:23]
	v_mov_b32_e32 v100, v16
	v_pk_mul_f32 v[16:17], v[28:29], v[18:19]
	v_pk_mul_f32 v[18:19], v[34:35], v[18:19]
	v_pk_mul_f32 v[20:21], v[30:31], v[22:23]
	v_pk_fma_f32 v[22:23], v[34:35], v[100:101], v[16:17] neg_lo:[0,0,1] neg_hi:[0,0,1]
	v_pk_fma_f32 v[16:17], v[30:31], v[36:37], v[38:39]
	v_pk_fma_f32 v[18:19], v[28:29], v[100:101], v[18:19]
	ds_write_b128 v61, v[16:19] offset:96
	v_pk_fma_f32 v[20:21], v[32:33], v[36:37], v[20:21] neg_lo:[0,0,1] neg_hi:[0,0,1]
	v_mov_b32_e32 v29, v8
	v_mov_b32_e32 v30, v9
	v_mov_b32_e32 v31, v10
	v_mov_b32_e32 v32, v11
	ds_read_b128 v[8:11], v95 offset:96
	v_mov_b32_e32 v34, v53
	v_mov_b32_e32 v37, v52
	v_mov_b32_e32 v28, v7
	v_mov_b32_e32 v33, v48
	s_waitcnt lgkmcnt(0)
; __device__ __forceinline__ bf16_t f2bf(float f) { unsigned u = __float_as_uint(f); u += 0x7fffu + ((u >> 16) & 1u); return (bf16_t)(u >> 16); }
; __device__ __forceinline__ void headpost(const P& p, int r, int hc, float* v, const float2* cs64, const float2* cs32) {
;     ...
;             float ss = 0.f; for (int d = 0; d < 32; ++d) ss += w[d] * w[d];
;             const float rs = rsqrtf(ss * (1.0f / 32.0f) + EPS);
;             for (int d = 0; d < 32; ++d) w[d] = w[d] * rs * g[d];
;             for (int i = 0; i < 16; ++i) { const float2 cs = cs32[i]; const float a = w[i], c = w[i + 16]; w[i] = a * cs.x - c * cs.y; w[i + 16] = c * cs.x + a * cs.y; } }
;         if (isq) { const int h = hc - 12; bf16_t* q = QB + ((size_t)(b * 8 + h) * SEQ + tok) * 64; for (int d = 0; d < 64; ++d) q[(d & 32) + bslot(d & 31)] = f2bf(v[d] * QSCALE_B); }
	v_mov_b32_e32 v53, v10
	v_mov_b32_e32 v10, v9
	s_waitcnt vmcnt(0)
	v_pk_mul_f32 v[12:13], v[12:13], v[106:107]
	v_mov_b32_e32 v52, v8
	v_pk_mul_f32 v[8:9], v[24:25], v[10:11]
	v_pk_mul_f32 v[14:15], v[14:15], v[108:109]
	v_pk_fma_f32 v[8:9], v[12:13], v[52:53], v[8:9]
	ds_write_b64 v61, v[8:9] offset:112
	ds_read_b64 v[8:9], v95 offset:112
	v_pk_mul_f32 v[10:11], v[12:13], v[10:11]
	ds_write_b128 v61, v[40:43] offset:16
	ds_write_b128 v61, v[20:23] offset:32
	v_mov_b32_e32 v20, v5
	v_mul_f32_e32 v5, 0x4b800000, v90
	s_waitcnt lgkmcnt(2)
	v_mul_f32_e32 v12, v26, v9
	v_fmac_f32_e32 v12, v14, v8
	ds_write2_b32 v61, v12, v15 offset0:30 offset1:31
	ds_read_b64 v[12:13], v95 offset:120
	v_mov_b32_e32 v22, v8
	v_mov_b32_e32 v8, v9
	v_cndmask_b32_e32 v5, v90, v5, vcc
	v_mov_b32_e32 v21, v6
	s_waitcnt lgkmcnt(0)
	v_mov_b32_e32 v9, v13
	v_mov_b32_e32 v23, v12
	v_pk_mul_f32 v[8:9], v[14:15], v[8:9]
	v_pk_fma_f32 v[10:11], v[24:25], v[52:53], v[10:11] neg_lo:[0,0,1] neg_hi:[0,0,1]
	v_pk_fma_f32 v[8:9], v[26:27], v[22:23], v[8:9] neg_lo:[0,0,1] neg_hi:[0,0,1]
	v_mov_b32_e32 v22, v1
	v_rsq_f32_e32 v1, v5
	v_mov_b32_e32 v23, v2
	v_mov_b32_e32 v48, v49
	v_mov_b32_e32 v49, v50
	v_mul_f32_e32 v2, 0x45800000, v1
	v_cndmask_b32_e32 v2, v1, v2, vcc
	v_pk_mul_f32 v[6:7], v[68:69], v[2:3] op_sel_hi:[1,0]
	v_mul_f32_e32 v1, v56, v2
	v_pk_mul_f32 v[20:21], v[20:21], v[6:7]
	v_mul_f32_e32 v4, v4, v1
	v_mov_b32_e32 v5, v20
	v_mov_b32_e32 v6, v21
	ds_write_b96 v61, v[4:6] offset:128
	v_pk_mul_f32 v[6:7], v[66:67], v[2:3] op_sel_hi:[1,0]
	v_mov_b32_e32 v50, v51
	v_pk_mul_f32 v[24:25], v[28:29], v[6:7]
	v_pk_mul_f32 v[6:7], v[76:77], v[2:3] op_sel_hi:[1,0]
	v_mov_b32_e32 v51, v44
	v_pk_mul_f32 v[28:29], v[6:7], v[30:31]
	v_pk_mul_f32 v[6:7], v[74:75], v[2:3] op_sel_hi:[1,0]
	v_mul_f32_e32 v1, v86, v2
	v_pk_mul_f32 v[30:31], v[6:7], v[32:33]
	v_pk_mul_f32 v[6:7], v[78:79], v[2:3] op_sel_hi:[1,0]
	ds_write2_b64 v61, v[10:11], v[8:9] offset0:6 offset1:7
	v_pk_mul_f32 v[32:33], v[6:7], v[48:49]
	v_pk_mul_f32 v[6:7], v[80:81], v[2:3] op_sel_hi:[1,0]
	v_mov_b32_e32 v8, v45
	v_pk_mul_f32 v[40:41], v[6:7], v[50:51]
	v_pk_mul_f32 v[6:7], v[88:89], v[2:3] op_sel_hi:[1,0]
	v_mov_b32_e32 v9, v46
	v_mul_f32_e32 v48, v1, v47
	v_mul_f32_e32 v1, v87, v2
	v_pk_mul_f32 v[42:43], v[6:7], v[8:9]
	v_mul_f32_e32 v7, v1, v0
	v_pk_mul_f32 v[0:1], v[84:85], v[2:3] op_sel_hi:[1,0]
	v_mov_b32_e32 v36, v3
	v_pk_mul_f32 v[22:23], v[0:1], v[22:23]
	v_pk_mul_f32 v[0:1], v[82:83], v[2:3] op_sel_hi:[1,0]
	v_mov_b32_e32 v35, v54
	v_pk_mul_f32 v[36:37], v[0:1], v[36:37]
	v_pk_mul_f32 v[0:1], v[58:59], v[2:3] op_sel_hi:[1,0]
	v_mov_b32_e32 v38, v55
	v_mov_b32_e32 v39, v102
	v_pk_mul_f32 v[34:35], v[0:1], v[34:35]
	v_pk_mul_f32 v[0:1], v[64:65], v[2:3] op_sel_hi:[1,0]
	v_mov_b32_e32 v16, v103
	v_mov_b32_e32 v17, v104
	v_pk_mul_f32 v[38:39], v[0:1], v[38:39]
	v_pk_mul_f32 v[0:1], v[70:71], v[2:3] op_sel_hi:[1,0]
	v_mov_b32_e32 v18, v105
	v_mov_b32_e32 v19, v106
	v_pk_mul_f32 v[16:17], v[0:1], v[16:17]
	v_pk_mul_f32 v[0:1], v[72:73], v[2:3] op_sel_hi:[1,0]
	v_mov_b32_e32 v8, v107
	v_pk_mul_f32 v[18:19], v[0:1], v[18:19]
	v_pk_mul_f32 v[0:1], v[92:93], v[2:3] op_sel_hi:[1,0]
	v_mov_b32_e32 v9, v108
	v_pk_mul_f32 v[44:45], v[0:1], v[8:9]
	ds_read_b64 v[8:9], v95
	ds_write2_b32 v61, v24, v25 offset0:35 offset1:36
	ds_write2_b32 v61, v28, v29 offset0:37 offset1:38
	v_mul_f32_e32 v0, v57, v2
	v_mul_f32_e32 v49, v0, v109
	ds_read2_b64 v[0:3], v95 offset0:1 offset1:2
	v_mov_b32_e32 v6, v27
	v_mov_b32_e32 v26, v13
	s_waitcnt lgkmcnt(3)
	v_mov_b32_e32 v27, v9
	v_mov_b32_e32 v10, v15
	v_mov_b32_e32 v11, v4
	v_mov_b32_e32 v46, v12
	v_mov_b32_e32 v47, v8
	v_pk_mul_f32 v[26:27], v[6:7], v[26:27]
	ds_write2_b32 v61, v30, v31 offset0:39 offset1:40
	v_pk_fma_f32 v[10:11], v[10:11], v[46:47], v[26:27] neg_lo:[0,0,1] neg_hi:[0,0,1]
	v_pk_fma_f32 v[12:13], v[14:15], v[12:13], v[26:27] op_sel:[1,0,0] op_sel_hi:[0,1,1]
	v_mov_b32_e32 v10, v8
	v_mov_b32_e32 v8, v9
	s_waitcnt lgkmcnt(1)
	v_mov_b32_e32 v9, v1
	ds_write2_b32 v61, v32, v33 offset0:41 offset1:42
	ds_write2_b32 v61, v12, v11 offset0:31 offset1:32
	v_mov_b32_e32 v6, v7
	v_mov_b32_e32 v7, v22
	v_mov_b32_e32 v11, v0
	v_pk_mul_f32 v[4:5], v[4:5], v[8:9]
	ds_write2_b32 v61, v40, v41 offset0:43 offset1:44
	v_pk_fma_f32 v[4:5], v[6:7], v[10:11], v[4:5]
	ds_read2_b64 v[8:11], v95 offset0:3 offset1:4
	ds_write2_b32 v61, v42, v43 offset0:45 offset1:46
	v_mov_b32_e32 v6, v0
	v_mov_b32_e32 v0, v1
	v_mov_b32_e32 v1, v3
	v_mov_b32_e32 v7, v2
	v_pk_mul_f32 v[0:1], v[22:23], v[0:1]
	ds_read2_b64 v[12:15], v95 offset0:5 offset1:6
	v_pk_fma_f32 v[0:1], v[20:21], v[6:7], v[0:1] neg_lo:[0,0,1] neg_hi:[0,0,1]
	v_mov_b32_e32 v6, v2
	v_pk_mov_b32 v[20:21], v[20:21], v[24:25] op_sel:[1,0]
	v_mov_b32_e32 v2, v3
	s_waitcnt lgkmcnt(2)
; __device__ __forceinline__ bf16_t f2bf(float f) { unsigned u = __float_as_uint(f); u += 0x7fffu + ((u >> 16) & 1u); return (bf16_t)(u >> 16); }
; __host__ __device__ __forceinline__ int ktile_off(int tok, int d) { return (tok >> 6) * TILE_EL + (d >> 3) * 512 + (tok & 63) * 8 + (d & 7); }
; __device__ __forceinline__ void headpost(const P& p, int r, int hc, float* v, const float2* cs64, const float2* cs32) {
;     ...
;             for (int i = 0; i < 16; ++i) { const float2 cs = cs32[i]; const float a = w[i], c = w[i + 16]; w[i] = a * cs.x - c * cs.y; w[i + 16] = c * cs.x + a * cs.y; } }
;         if (isq) { const int h = hc - 12; bf16_t* q = QB + ((size_t)(b * 8 + h) * SEQ + tok) * 64; for (int d = 0; d < 64; ++d) q[(d & 32) + bslot(d & 31)] = f2bf(v[d] * QSCALE_B); }
;         else { const int h = hc - 20; bf16_t* k = meta ? MT + (4 + h) * TILE_EL : KB + (size_t)(b * 8 + h) * HEAD_EL; const int tk = meta ? pos : tok; for (int d = 0; d < 64; ++d) k[ktile_off(tk, (d & 32) + bslot(d & 31))] = f2bf(v[d]); }
	v_mov_b32_e32 v3, v9
	ds_write2_b32 v61, v0, v1 offset0:33 offset1:34
	v_pk_mov_b32 v[0:1], v[22:23], v[36:37] op_sel:[1,0]
	v_mov_b32_e32 v7, v8
	v_pk_mul_f32 v[2:3], v[20:21], v[2:3]
	ds_write_b32 v61, v48 offset:188
	v_pk_fma_f32 v[6:7], v[0:1], v[6:7], v[2:3]
	v_mov_b32_e32 v2, v9
	v_mov_b32_e32 v3, v11
	v_mov_b32_e32 v0, v8
	v_mov_b32_e32 v1, v10
	v_pk_mul_f32 v[2:3], v[36:37], v[2:3]
	ds_write_b128 v61, v[4:7] offset:192
	v_pk_fma_f32 v[0:1], v[24:25], v[0:1], v[2:3] neg_lo:[0,0,1] neg_hi:[0,0,1]
	v_pk_mov_b32 v[4:5], v[24:25], v[28:29] op_sel:[1,0]
	v_mov_b32_e32 v6, v11
	s_waitcnt lgkmcnt(3)
	v_mov_b32_e32 v7, v13
	ds_write2_b32 v61, v0, v1 offset0:35 offset1:36
	v_pk_mov_b32 v[0:1], v[36:37], v[34:35] op_sel:[1,0]
	v_mov_b32_e32 v2, v10
	v_mov_b32_e32 v3, v12
	v_pk_mul_f32 v[4:5], v[4:5], v[6:7]
	v_mov_b32_e32 v10, v14
	v_pk_fma_f32 v[0:1], v[0:1], v[2:3], v[4:5]
	v_mov_b32_e32 v2, v13
	v_mov_b32_e32 v3, v15
	ds_write_b64 v61, v[0:1] offset:208
	v_mov_b32_e32 v0, v12
	v_mov_b32_e32 v1, v14
	v_pk_mul_f32 v[2:3], v[34:35], v[2:3]
	v_pk_mov_b32 v[12:13], v[28:29], v[30:31] op_sel:[1,0]
	v_pk_fma_f32 v[4:5], v[28:29], v[0:1], v[2:3] neg_lo:[0,0,1] neg_hi:[0,0,1]
	ds_read2_b64 v[0:3], v95 offset0:7 offset1:8
	ds_write2_b32 v61, v4, v5 offset0:37 offset1:38
	ds_read2_b64 v[4:7], v95 offset0:9 offset1:10
	v_mov_b32_e32 v14, v15
	v_pk_mov_b32 v[8:9], v[34:35], v[38:39] op_sel:[1,0]
	s_waitcnt lgkmcnt(2)
	v_mov_b32_e32 v15, v1
	v_mov_b32_e32 v11, v0
	v_pk_mul_f32 v[12:13], v[12:13], v[14:15]
	s_and_b64 vcc, exec, s[12:13]
	v_pk_fma_f32 v[8:9], v[8:9], v[10:11], v[12:13]
	v_mov_b32_e32 v10, v0
	v_mov_b32_e32 v0, v1
	v_mov_b32_e32 v1, v3
	v_mov_b32_e32 v11, v2
	v_pk_mul_f32 v[0:1], v[38:39], v[0:1]
	v_pk_mov_b32 v[12:13], v[30:31], v[32:33] op_sel:[1,0]
	v_pk_fma_f32 v[0:1], v[30:31], v[10:11], v[0:1] neg_lo:[0,0,1] neg_hi:[0,0,1]
	v_mov_b32_e32 v10, v2
	v_mov_b32_e32 v2, v3
	s_waitcnt lgkmcnt(0)
	v_mov_b32_e32 v3, v5
	ds_write2_b32 v61, v0, v1 offset0:39 offset1:40
	v_pk_mov_b32 v[0:1], v[38:39], v[16:17] op_sel:[1,0]
	v_mov_b32_e32 v11, v4
	v_pk_mul_f32 v[2:3], v[12:13], v[2:3]
	v_pk_mov_b32 v[12:13], v[40:41], v[42:43] op_sel:[1,0]
	v_pk_fma_f32 v[0:1], v[0:1], v[10:11], v[2:3]
	ds_write2_b64 v61, v[8:9], v[0:1] offset0:27 offset1:28
	v_mov_b32_e32 v0, v5
	v_mov_b32_e32 v1, v7
	v_mov_b32_e32 v8, v4
	v_pk_mul_f32 v[4:5], v[16:17], v[0:1]
	ds_read2_b64 v[0:3], v95 offset0:11 offset1:12
	v_mov_b32_e32 v9, v6
	v_pk_fma_f32 v[4:5], v[32:33], v[8:9], v[4:5] neg_lo:[0,0,1] neg_hi:[0,0,1]
	v_mov_b32_e32 v8, v6
	v_pk_mov_b32 v[10:11], v[32:33], v[40:41] op_sel:[1,0]
	v_mov_b32_e32 v6, v7
	s_waitcnt lgkmcnt(0)
	v_mov_b32_e32 v7, v1
	ds_write2_b32 v61, v4, v5 offset0:41 offset1:42
	v_pk_mov_b32 v[4:5], v[16:17], v[18:19] op_sel:[1,0]
	v_mov_b32_e32 v9, v0
	v_pk_mul_f32 v[6:7], v[10:11], v[6:7]
	v_mov_b32_e32 v10, v2
	v_pk_fma_f32 v[4:5], v[4:5], v[8:9], v[6:7]
	ds_write_b64 v61, v[4:5] offset:232
	ds_read_b64 v[6:7], v95 offset:104
	v_mov_b32_e32 v4, v0
	v_mov_b32_e32 v5, v2
	v_mov_b32_e32 v0, v1
	v_mov_b32_e32 v1, v3
	v_mov_b32_e32 v2, v3
	s_waitcnt lgkmcnt(0)
	v_mov_b32_e32 v3, v7
	v_pk_mov_b32 v[8:9], v[18:19], v[44:45] op_sel:[1,0]
	v_mov_b32_e32 v11, v6
	v_pk_mul_f32 v[2:3], v[12:13], v[2:3]
	v_pk_mul_f32 v[0:1], v[18:19], v[0:1]
	v_pk_fma_f32 v[2:3], v[8:9], v[10:11], v[2:3]
	ds_write_b64 v61, v[2:3] offset:240
	ds_read_b64 v[2:3], v95 offset:112
	v_pk_fma_f32 v[0:1], v[40:41], v[4:5], v[0:1] neg_lo:[0,0,1] neg_hi:[0,0,1]
	ds_write2_b32 v61, v0, v1 offset0:43 offset1:44
	v_mov_b32_e32 v0, v6
	v_mov_b32_e32 v4, v7
	s_waitcnt lgkmcnt(1)
	v_mov_b32_e32 v1, v2
	v_mul_f32_e32 v2, v45, v2
	v_fmac_f32_e32 v2, v43, v3
	ds_write2_b32 v61, v2, v49 offset0:62 offset1:63
	ds_read_b64 v[6:7], v95 offset:120
	v_mov_b32_e32 v5, v3
	v_pk_mul_f32 v[2:3], v[44:45], v[4:5]
	v_readlane_b32 s41, v254, 14
	v_pk_fma_f32 v[0:1], v[42:43], v[0:1], v[2:3] neg_lo:[0,0,1] neg_hi:[0,0,1]
	ds_write2_b32 v61, v0, v1 offset0:45 offset1:46
	s_waitcnt lgkmcnt(1)
	v_mul_f32_e32 v0, v49, v7
	v_fma_f32 v0, v48, v6, -v0
	ds_write_b32 v61, v0 offset:188
	v_mul_f32_e32 v0, v48, v7
	v_fmac_f32_e32 v0, v49, v6
	v_readlane_b32 s42, v254, 15
	v_readlane_b32 s43, v254, 16
	v_readlane_b32 s44, v254, 17
	v_readlane_b32 s45, v254, 18
	v_readlane_b32 s46, v254, 19
	v_readlane_b32 s47, v254, 20
	ds_write_b32 v61, v0 offset:252
	s_cbranch_vccz .LBB7_76
	s_and_saveexec_b64 s[10:11], s[0:1]
	s_xor_b64 s[10:11], exec, s[10:11]
	s_sub_i32 s2, s88, 20
	v_lshl_add_u32 v0, v98, 3, s2
	v_ashrrev_i32_e32 v1, 31, v0
	v_lshlrev_b64 v[0:1], 19, v[0:1]
	v_lshl_add_u64 v[0:1], s[30:31], 0, v[0:1]
	s_mov_b64 s[12:13], 0x10000000
	v_lshl_add_u64 v[0:1], v[0:1], 0, s[12:13]
	v_lshlrev_b32_e32 v2, 6, v97
	v_lshlrev_b32_e32 v3, 3, v97
	s_andn2_saveexec_b64 s[10:11], s[10:11]
	s_cbranch_execz .LBB7_73
	s_lshl_b32 s2, s88, 13
	v_readlane_b32 s12, v254, 43
	s_add_u32 s2, s12, s2
	v_readlane_b32 s12, v254, 42
	s_addc_u32 s13, s12, 0
	s_add_u32 s12, s2, 0xfffe0000
	s_addc_u32 s13, s13, -1
	v_mov_b64_e32 v[0:1], s[12:13]
	v_mov_b32_e32 v3, v63
	v_mov_b32_e32 v2, v99

; __device__ __forceinline__ void headpost(const P& p, int r, int hc, float* v, const float2* cs64, const float2* cs32) {
;     ...
;         if (hc < 8 && meta) return;
;         const float* g = hc < 8 ? p.g_q_swa : p.g_k_swa;
;         float ss = 0.f; for (int d = 0; d < 64; ++d) ss += v[d] * v[d];
;         const float rs = rsqrtf(ss * (1.0f / 64.0f) + EPS);
;         for (int d = 0; d < 64; ++d) v[d] = v[d] * rs * g[d];
.LBB7_89:
	s_andn2_b64 vcc, exec, s[8:9]
	s_cbranch_vccnz .LBB7_99
	s_cmp_lt_i32 s88, 8
	s_cselect_b64 s[10:11], -1, 0
	s_cmp_gt_i32 s88, 7
	s_cselect_b64 s[8:9], -1, 0
	s_and_b64 s[12:13], s[10:11], s[4:5]
	s_mov_b64 s[4:5], -1
	s_xor_b64 s[12:13], s[12:13], -1
	s_and_b64 exec, exec, s[12:13]
	s_cbranch_execz .LBB7_99
	ds_read2_b32 v[4:5], v61 offset0:1 offset1:2
	ds_read_b32 v12, v61
	ds_read2_b32 v[6:7], v61 offset0:3 offset1:4
	ds_read2_b32 v[8:9], v61 offset0:5 offset1:6
	ds_read2_b32 v[10:11], v61 offset0:7 offset1:8
	s_waitcnt lgkmcnt(4)
	v_mul_f32_e32 v32, v4, v4
	s_waitcnt lgkmcnt(3)
	v_fmac_f32_e32 v32, v12, v12
	v_fmac_f32_e32 v32, v5, v5
	s_waitcnt lgkmcnt(2)
	v_fmac_f32_e32 v32, v6, v6
	ds_read2_b64 v[0:3], v61 offset1:1
	ds_read2_b32 v[4:5], v61 offset0:9 offset1:10
	v_fmac_f32_e32 v32, v7, v7
	s_waitcnt lgkmcnt(3)
	v_fmac_f32_e32 v32, v8, v8
	v_fmac_f32_e32 v32, v9, v9
	s_waitcnt lgkmcnt(2)
	v_fmac_f32_e32 v32, v10, v10
	v_fmac_f32_e32 v32, v11, v11
	ds_read2_b32 v[6:7], v61 offset0:11 offset1:12
	ds_read2_b32 v[8:9], v61 offset0:13 offset1:14
	ds_read2_b32 v[10:11], v61 offset0:15 offset1:16
	s_waitcnt lgkmcnt(3)
	v_fmac_f32_e32 v32, v4, v4
	v_fmac_f32_e32 v32, v5, v5
	s_waitcnt lgkmcnt(2)
	v_fmac_f32_e32 v32, v6, v6
	v_fmac_f32_e32 v32, v7, v7
	ds_read2_b32 v[4:5], v61 offset0:17 offset1:18
	s_waitcnt lgkmcnt(2)
	v_fmac_f32_e32 v32, v8, v8
	v_fmac_f32_e32 v32, v9, v9
	s_waitcnt lgkmcnt(1)
	v_fmac_f32_e32 v32, v10, v10
	v_fmac_f32_e32 v32, v11, v11
	ds_read2_b32 v[6:7], v61 offset0:19 offset1:20
	ds_read2_b32 v[8:9], v61 offset0:21 offset1:22
	ds_read2_b32 v[10:11], v61 offset0:23 offset1:24
	s_waitcnt lgkmcnt(3)
	v_fmac_f32_e32 v32, v4, v4
	v_fmac_f32_e32 v32, v5, v5
	s_waitcnt lgkmcnt(2)
	v_fmac_f32_e32 v32, v6, v6
	v_fmac_f32_e32 v32, v7, v7
	s_waitcnt lgkmcnt(1)
	v_fmac_f32_e32 v32, v8, v8
	v_readlane_b32 s36, v254, 9
	v_fmac_f32_e32 v32, v9, v9
	s_and_b64 s[10:11], s[10:11], exec
	v_readlane_b32 s44, v254, 17
	v_readlane_b32 s45, v254, 18
	v_readlane_b32 s46, v254, 19
	v_readlane_b32 s47, v254, 20
	s_waitcnt lgkmcnt(0)
	v_fmac_f32_e32 v32, v10, v10
	s_cselect_b32 s11, s45, s47
	s_cselect_b32 s10, s44, s46
	v_mov_b32_e32 v60, 0
	ds_read2_b32 v[4:5], v61 offset0:25 offset1:26
	v_fmac_f32_e32 v32, v11, v11
	ds_read2_b32 v[6:7], v61 offset0:27 offset1:28
	ds_read2_b32 v[8:9], v61 offset0:29 offset1:30
	ds_read2_b32 v[10:11], v61 offset0:31 offset1:32
	global_load_dwordx4 v[12:15], v60, s[10:11] offset:16 nt
	global_load_dwordx4 v[16:19], v60, s[10:11] nt
	ds_read2_b32 v[20:21], v61 offset0:37 offset1:38
	s_waitcnt lgkmcnt(4)
	v_fmac_f32_e32 v32, v4, v4
	v_fmac_f32_e32 v32, v5, v5
	s_waitcnt lgkmcnt(3)
	v_fmac_f32_e32 v32, v6, v6
	v_fmac_f32_e32 v32, v7, v7
	ds_read2_b32 v[4:5], v61 offset0:33 offset1:34
	ds_read2_b32 v[6:7], v61 offset0:35 offset1:36
	s_waitcnt lgkmcnt(4)
	v_fmac_f32_e32 v32, v8, v8
	v_fmac_f32_e32 v32, v9, v9
	s_waitcnt lgkmcnt(3)
	v_fmac_f32_e32 v32, v10, v10
	v_fmac_f32_e32 v32, v11, v11
	s_waitcnt lgkmcnt(1)
	v_fmac_f32_e32 v32, v4, v4
	v_fmac_f32_e32 v32, v5, v5
	s_waitcnt lgkmcnt(0)
	v_fmac_f32_e32 v32, v6, v6
	v_fmac_f32_e32 v32, v7, v7
	global_load_dwordx4 v[4:7], v60, s[10:11] offset:48 nt
	global_load_dwordx4 v[8:11], v60, s[10:11] offset:32 nt
	ds_read2_b64 v[24:27], v61 offset0:18 offset1:19
	ds_read2_b32 v[22:23], v61 offset0:39 offset1:40
	v_fmac_f32_e32 v32, v20, v20
	v_fmac_f32_e32 v32, v21, v21
	ds_read2_b32 v[20:21], v61 offset0:41 offset1:42
	ds_read2_b32 v[28:29], v61 offset0:43 offset1:44
	ds_read2_b32 v[30:31], v61 offset0:45 offset1:46
	global_load_dwordx4 v[44:47], v60, s[10:11] offset:80 nt
	global_load_dwordx4 v[52:55], v60, s[10:11] offset:64 nt
	s_waitcnt lgkmcnt(3)
	v_fmac_f32_e32 v32, v22, v22
	v_fmac_f32_e32 v32, v23, v23
	s_waitcnt lgkmcnt(2)
	v_fmac_f32_e32 v32, v20, v20
	v_fmac_f32_e32 v32, v21, v21
	ds_read2_b32 v[20:21], v61 offset0:47 offset1:48
	s_waitcnt lgkmcnt(2)
	v_fmac_f32_e32 v32, v28, v28
	v_fmac_f32_e32 v32, v29, v29
	s_waitcnt lgkmcnt(1)
	v_fmac_f32_e32 v32, v30, v30
	v_fmac_f32_e32 v32, v31, v31
	ds_read2_b32 v[22:23], v61 offset0:49 offset1:50
	ds_read2_b32 v[28:29], v61 offset0:51 offset1:52
	ds_read_b32 v30, v61 offset:212
	s_waitcnt lgkmcnt(3)
	v_fmac_f32_e32 v32, v20, v20
	v_fmac_f32_e32 v32, v21, v21
	s_waitcnt lgkmcnt(2)
	v_fmac_f32_e32 v32, v22, v22
	v_fmac_f32_e32 v32, v23, v23
	global_load_dwordx4 v[40:43], v60, s[10:11] offset:112 nt
	global_load_dwordx4 v[48:51], v60, s[10:11] offset:96 nt
	ds_read2_b64 v[20:23], v61 offset0:27 offset1:31
	s_waitcnt lgkmcnt(2)
	v_fmac_f32_e32 v32, v28, v28
	ds_read2_b64 v[34:37], v61 offset0:27 offset1:28
	v_fmac_f32_e32 v32, v29, v29
	s_waitcnt lgkmcnt(2)
	v_fmac_f32_e32 v32, v30, v30
	ds_read_b128 v[28:31], v61 offset:224
	s_waitcnt lgkmcnt(2)
	v_pk_mul_f32 v[20:21], v[20:21], v[20:21]
	global_load_dwordx4 v[56:59], v60, s[10:11] offset:128 nt
	global_load_dwordx4 v[64:67], v60, s[10:11] offset:144 nt
	v_add_f32_e32 v20, v32, v20
	v_add_f32_e32 v32, v20, v21
	s_waitcnt lgkmcnt(1)
	v_pk_mul_f32 v[20:21], v[36:37], v[36:37]
	ds_read2_b64 v[36:39], v61 offset0:29 offset1:30
	v_add_f32_e32 v20, v32, v20
	v_add_f32_e32 v32, v20, v21
	s_waitcnt lgkmcnt(1)
	v_pk_mul_f32 v[20:21], v[30:31], v[30:31]
	s_mov_b32 s2, 0x800000
	v_add_f32_e32 v20, v32, v20
	ds_read_b128 v[30:33], v61 offset:240
	v_add_f32_e32 v62, v20, v21
	s_waitcnt lgkmcnt(1)
	v_pk_mul_f32 v[20:21], v[38:39], v[38:39]
	global_load_dwordx4 v[68:71], v60, s[10:11] offset:160 nt
	global_load_dwordx4 v[72:75], v60, s[10:11] offset:176 nt
	v_add_f32_e32 v20, v62, v20
	v_add_f32_e32 v38, v20, v21
	s_waitcnt lgkmcnt(0)
; __device__ __forceinline__ void headpost(const P& p, int r, int hc, float* v, const float2* cs64, const float2* cs32) {
;     ...
;         const float rs = rsqrtf(ss * (1.0f / 64.0f) + EPS);
;         for (int d = 0; d < 64; ++d) v[d] = v[d] * rs * g[d];
;         for (int i = 0; i < 32; ++i) { const float2 cs = cs64[i]; const float a = v[i], c = v[i + 32]; v[i] = a * cs.x - c * cs.y; v[i + 32] = c * cs.x + a * cs.y; }
	v_pk_mul_f32 v[20:21], v[32:33], v[32:33]
	global_load_dwordx4 v[84:87], v60, s[10:11] offset:208 nt
	v_add_f32_e32 v20, v38, v20
	v_add_f32_e32 v20, v20, v21
	v_mov_b32_e32 v21, 0x358637bd
	v_fmac_f32_e32 v21, 0x3c800000, v20
	v_mul_f32_e32 v20, 0x4b800000, v21
	v_cmp_gt_f32_e32 vcc, s2, v21
	global_load_dwordx4 v[88:91], v60, s[10:11] offset:224 nt
	global_load_dwordx4 v[92:95], v60, s[10:11] offset:240 nt
	v_cndmask_b32_e32 v20, v21, v20, vcc
	v_rsq_f32_e32 v20, v20
	ds_read2_b64 v[76:79], v61 offset0:2 offset1:3
	v_readlane_b32 s37, v254, 10
	v_readlane_b32 s38, v254, 11
	v_mul_f32_e32 v21, 0x45800000, v20
	v_cndmask_b32_e32 v62, v20, v21, vcc
	v_pk_mul_f32 v[0:1], v[62:63], v[0:1] op_sel_hi:[0,1]
	v_pk_mul_f32 v[2:3], v[62:63], v[2:3] op_sel_hi:[0,1]
	s_waitcnt vmcnt(13)
	v_pk_mul_f32 v[0:1], v[0:1], v[16:17]
	v_pk_mul_f32 v[2:3], v[2:3], v[18:19]
	global_load_dwordx4 v[16:19], v60, s[10:11] offset:192 nt
	ds_write_b128 v61, v[0:3]
	ds_read2_b64 v[0:3], v61 offset0:4 offset1:5
	ds_read_b128 v[80:83], v61
	s_waitcnt lgkmcnt(3)
	v_pk_mul_f32 v[20:21], v[62:63], v[76:77] op_sel_hi:[0,1]
	v_pk_mul_f32 v[32:33], v[62:63], v[78:79] op_sel_hi:[0,1]
	v_pk_mul_f32 v[12:13], v[20:21], v[12:13]
	v_pk_mul_f32 v[14:15], v[32:33], v[14:15]
	ds_read2_b64 v[76:79], v61 offset0:6 offset1:7
	ds_write_b128 v61, v[12:15] offset:16
	ds_read_b128 v[12:15], v61 offset:16
	s_waitcnt lgkmcnt(4)
	v_pk_mul_f32 v[0:1], v[62:63], v[0:1] op_sel_hi:[0,1]
	v_pk_mul_f32 v[2:3], v[62:63], v[2:3] op_sel_hi:[0,1]
	s_waitcnt vmcnt(12)
	v_pk_mul_f32 v[0:1], v[0:1], v[8:9]
	v_pk_mul_f32 v[2:3], v[2:3], v[10:11]
	ds_read2_b64 v[8:11], v61 offset0:8 offset1:9
	ds_write_b128 v61, v[0:3] offset:32
	ds_read_b128 v[0:3], v61 offset:32
	s_waitcnt lgkmcnt(5)
	v_pk_mul_f32 v[20:21], v[62:63], v[76:77] op_sel_hi:[0,1]
	v_pk_mul_f32 v[32:33], v[62:63], v[78:79] op_sel_hi:[0,1]
	v_pk_mul_f32 v[4:5], v[20:21], v[4:5]
	v_pk_mul_f32 v[6:7], v[32:33], v[6:7]
	ds_write_b128 v61, v[4:7] offset:48
	ds_read_b128 v[4:7], v61 offset:48
	s_waitcnt lgkmcnt(4)
	v_pk_mul_f32 v[20:21], v[62:63], v[8:9] op_sel_hi:[0,1]
	v_pk_mul_f32 v[32:33], v[62:63], v[10:11] op_sel_hi:[0,1]
	ds_read2_b64 v[8:11], v61 offset0:10 offset1:11
	s_waitcnt vmcnt(10)
	v_pk_mul_f32 v[52:53], v[20:21], v[52:53]
	v_pk_mul_f32 v[54:55], v[32:33], v[54:55]
	ds_write_b128 v61, v[52:55] offset:64
	ds_read_b128 v[52:55], v61 offset:64
	s_waitcnt lgkmcnt(2)
	v_pk_mul_f32 v[20:21], v[62:63], v[8:9] op_sel_hi:[0,1]
	v_pk_mul_f32 v[32:33], v[62:63], v[10:11] op_sel_hi:[0,1]
	ds_read2_b64 v[8:11], v61 offset0:12 offset1:13
	v_pk_mul_f32 v[44:45], v[20:21], v[44:45]
	v_pk_mul_f32 v[46:47], v[32:33], v[46:47]
	ds_read2_b64 v[76:79], v61 offset0:14 offset1:15
	ds_write_b128 v61, v[44:47] offset:80
	ds_read_b128 v[44:47], v61 offset:80
	s_waitcnt lgkmcnt(3)
	v_pk_mul_f32 v[8:9], v[62:63], v[8:9] op_sel_hi:[0,1]
	v_pk_mul_f32 v[10:11], v[62:63], v[10:11] op_sel_hi:[0,1]
	s_waitcnt vmcnt(8)
	v_pk_mul_f32 v[8:9], v[8:9], v[48:49]
	v_pk_mul_f32 v[10:11], v[10:11], v[50:51]
	ds_read2_b64 v[48:51], v61 offset0:16 offset1:17
	ds_write_b128 v61, v[8:11] offset:96
	ds_read_b128 v[8:11], v61 offset:96
	s_waitcnt lgkmcnt(5)
	v_pk_mul_f32 v[20:21], v[62:63], v[76:77] op_sel_hi:[0,1]
	v_pk_mul_f32 v[32:33], v[62:63], v[78:79] op_sel_hi:[0,1]
	v_pk_mul_f32 v[38:39], v[20:21], v[40:41]
	v_pk_mul_f32 v[40:41], v[32:33], v[42:43]
	ds_write_b128 v61, v[38:41] offset:112
	ds_read_b128 v[38:41], v61 offset:112
	s_waitcnt lgkmcnt(4)
	v_pk_mul_f32 v[20:21], v[62:63], v[48:49] op_sel_hi:[0,1]
	v_pk_mul_f32 v[32:33], v[62:63], v[50:51] op_sel_hi:[0,1]
	s_waitcnt vmcnt(7)
	v_pk_mul_f32 v[48:49], v[20:21], v[56:57]
	v_pk_mul_f32 v[50:51], v[32:33], v[58:59]
	v_pk_mul_f32 v[20:21], v[62:63], v[24:25] op_sel_hi:[0,1]
	v_pk_mul_f32 v[32:33], v[62:63], v[26:27] op_sel_hi:[0,1]
	ds_read2_b64 v[24:27], v61 offset0:20 offset1:21
	s_waitcnt vmcnt(6)
	v_pk_mul_f32 v[56:57], v[20:21], v[64:65]
	v_pk_mul_f32 v[58:59], v[32:33], v[66:67]
	ds_write_b128 v61, v[56:59] offset:144
	ds_read_b128 v[56:59], v61 offset:144
	s_waitcnt lgkmcnt(2)
	v_pk_mul_f32 v[20:21], v[62:63], v[24:25] op_sel_hi:[0,1]
	v_pk_mul_f32 v[32:33], v[62:63], v[26:27] op_sel_hi:[0,1]
	ds_read2_b64 v[24:27], v61 offset0:22 offset1:23
	s_waitcnt vmcnt(5)
	v_pk_mul_f32 v[64:65], v[20:21], v[68:69]
	v_pk_mul_f32 v[66:67], v[32:33], v[70:71]
	ds_write_b128 v61, v[64:67] offset:160
	ds_read_b128 v[64:67], v61 offset:160
	s_waitcnt lgkmcnt(2)
	v_pk_mul_f32 v[20:21], v[62:63], v[24:25] op_sel_hi:[0,1]
	v_pk_mul_f32 v[32:33], v[62:63], v[26:27] op_sel_hi:[0,1]
	ds_read2_b64 v[24:27], v61 offset0:24 offset1:25
	s_waitcnt vmcnt(4)
	v_pk_mul_f32 v[68:69], v[20:21], v[72:73]
	v_pk_mul_f32 v[70:71], v[32:33], v[74:75]
	ds_write_b128 v61, v[68:71] offset:176
	ds_read_b128 v[68:71], v61 offset:176
	s_waitcnt lgkmcnt(2)
	v_pk_mul_f32 v[20:21], v[62:63], v[24:25] op_sel_hi:[0,1]
	v_pk_mul_f32 v[24:25], v[62:63], v[26:27] op_sel_hi:[0,1]
	v_pk_mul_f32 v[26:27], v[62:63], v[34:35] op_sel_hi:[0,1]
	s_waitcnt vmcnt(0)
	v_pk_mul_f32 v[16:17], v[20:21], v[16:17]
	ds_read_b64 v[20:21], v61 offset:208
	v_pk_mul_f32 v[18:19], v[24:25], v[18:19]
	ds_write_b128 v61, v[16:19] offset:192
	ds_read_b128 v[16:19], v61 offset:192
	v_pk_mul_f32 v[26:27], v[26:27], v[86:87]
	s_waitcnt lgkmcnt(2)
; __device__ __forceinline__ void headpost(const P& p, int r, int hc, float* v, const float2* cs64, const float2* cs32) {
;     ...
;         for (int i = 0; i < 32; ++i) { const float2 cs = cs64[i]; const float a = v[i], c = v[i + 32]; v[i] = a * cs.x - c * cs.y; v[i + 32] = c * cs.x + a * cs.y; }
	v_pk_mul_f32 v[20:21], v[62:63], v[20:21] op_sel_hi:[0,1]
	v_pk_mul_f32 v[24:25], v[20:21], v[84:85]
	v_pk_mul_f32 v[20:21], v[62:63], v[28:29] op_sel_hi:[0,1]
	v_pk_mul_f32 v[32:33], v[20:21], v[88:89]
	v_lshl_add_u32 v20, v99, 2, 0
	v_pk_mul_f32 v[28:29], v[62:63], v[36:37] op_sel_hi:[0,1]
	v_add_u32_e32 v42, 0x10000, v20
	v_pk_mul_f32 v[20:21], v[62:63], v[30:31] op_sel_hi:[0,1]
	v_pk_mul_f32 v[22:23], v[62:63], v[22:23] op_sel_hi:[0,1]
	v_pk_mul_f32 v[34:35], v[28:29], v[90:91]
	ds_write_b128 v61, v[24:27] offset:208
	v_pk_mul_f32 v[20:21], v[20:21], v[92:93]
	ds_read_b128 v[24:27], v42
	v_pk_mul_f32 v[22:23], v[22:23], v[94:95]
	ds_write_b128 v61, v[32:35] offset:224
	ds_write_b128 v61, v[20:23] offset:240
	ds_read_b128 v[20:23], v42 offset:16
	ds_read_b128 v[28:31], v61 offset:240
	s_waitcnt lgkmcnt(4)
	v_mov_b32_e32 v37, v26
	v_mov_b32_e32 v26, v25
	v_mov_b32_e32 v36, v24
	s_waitcnt lgkmcnt(1)
	v_mov_b32_e32 v24, v20
	v_mov_b32_e32 v25, v22
	v_mov_b32_e32 v22, v21
	v_pk_mul_f32 v[20:21], v[26:27], v[48:49]
	ds_read_b128 v[32:35], v42 offset:32
	v_pk_fma_f32 v[72:73], v[36:37], v[80:81], v[20:21] neg_lo:[0,0,1] neg_hi:[0,0,1]
	v_pk_mul_f32 v[20:21], v[22:23], v[50:51]
	s_and_b64 vcc, exec, s[8:9]
	v_pk_fma_f32 v[74:75], v[24:25], v[82:83], v[20:21] neg_lo:[0,0,1] neg_hi:[0,0,1]
	v_pk_mul_f32 v[20:21], v[36:37], v[48:49]
	v_pk_mul_f32 v[24:25], v[24:25], v[50:51]
	ds_write_b128 v61, v[72:75]
	ds_write_b128 v61, v[48:51] offset:128
	v_pk_fma_f32 v[20:21], v[26:27], v[80:81], v[20:21]
	v_pk_fma_f32 v[22:23], v[22:23], v[82:83], v[24:25]
	ds_write_b128 v61, v[20:23] offset:128
	ds_read_b128 v[20:23], v42 offset:48
	s_waitcnt lgkmcnt(4)
	v_mov_b32_e32 v27, v34
	v_mov_b32_e32 v34, v33
	v_mov_b32_e32 v26, v32
	v_pk_mul_f32 v[24:25], v[34:35], v[56:57]
	v_readlane_b32 s39, v254, 12
	v_pk_fma_f32 v[24:25], v[26:27], v[12:13], v[24:25] neg_lo:[0,0,1] neg_hi:[0,0,1]
	v_pk_mul_f32 v[26:27], v[26:27], v[56:57]
	v_readlane_b32 s40, v254, 13
	v_pk_fma_f32 v[12:13], v[34:35], v[12:13], v[26:27]
	ds_read_b128 v[32:35], v42 offset:64
	s_waitcnt lgkmcnt(1)
	v_mov_b32_e32 v37, v22
	v_mov_b32_e32 v22, v21
	v_mov_b32_e32 v36, v20
	v_pk_mul_f32 v[20:21], v[22:23], v[58:59]
	v_readlane_b32 s41, v254, 14
	v_pk_fma_f32 v[26:27], v[36:37], v[14:15], v[20:21] neg_lo:[0,0,1] neg_hi:[0,0,1]
	v_pk_mul_f32 v[20:21], v[36:37], v[58:59]
	ds_write_b128 v61, v[24:27] offset:16
	v_pk_fma_f32 v[14:15], v[22:23], v[14:15], v[20:21]
	ds_write_b128 v61, v[12:15] offset:144
	ds_read_b128 v[12:15], v42 offset:80
	ds_read_b128 v[24:27], v42 offset:96
	s_waitcnt lgkmcnt(4)
	v_mov_b32_e32 v23, v34
	v_mov_b32_e32 v34, v33
	v_mov_b32_e32 v22, v32
	v_pk_mul_f32 v[20:21], v[34:35], v[64:65]
	s_waitcnt lgkmcnt(1)
	v_mov_b32_e32 v33, v14
	v_mov_b32_e32 v14, v13
	v_pk_fma_f32 v[20:21], v[22:23], v[0:1], v[20:21] neg_lo:[0,0,1] neg_hi:[0,0,1]
	v_pk_mul_f32 v[22:23], v[22:23], v[64:65]
	v_mov_b32_e32 v32, v12
	v_pk_mul_f32 v[12:13], v[14:15], v[66:67]
	v_pk_fma_f32 v[0:1], v[34:35], v[0:1], v[22:23]
	v_pk_fma_f32 v[22:23], v[32:33], v[2:3], v[12:13] neg_lo:[0,0,1] neg_hi:[0,0,1]
	v_pk_mul_f32 v[12:13], v[32:33], v[66:67]
	ds_write_b128 v61, v[20:23] offset:32
	v_pk_fma_f32 v[2:3], v[14:15], v[2:3], v[12:13]
	ds_write_b128 v61, v[0:3] offset:160
	ds_read_b128 v[0:3], v42 offset:112
	ds_read_b128 v[20:23], v42 offset:128
	s_waitcnt lgkmcnt(4)
	v_mov_b32_e32 v15, v26
	v_mov_b32_e32 v26, v25
	v_mov_b32_e32 v14, v24
	v_pk_mul_f32 v[12:13], v[26:27], v[68:69]
	s_waitcnt lgkmcnt(1)
	v_mov_b32_e32 v25, v2
	v_mov_b32_e32 v2, v1
	v_pk_fma_f32 v[12:13], v[14:15], v[4:5], v[12:13] neg_lo:[0,0,1] neg_hi:[0,0,1]
	v_pk_mul_f32 v[14:15], v[14:15], v[68:69]
	v_mov_b32_e32 v24, v0
	v_pk_mul_f32 v[0:1], v[2:3], v[70:71]
	v_pk_fma_f32 v[4:5], v[26:27], v[4:5], v[14:15]
	v_pk_fma_f32 v[14:15], v[24:25], v[6:7], v[0:1] neg_lo:[0,0,1] neg_hi:[0,0,1]
	v_pk_mul_f32 v[0:1], v[24:25], v[70:71]
	ds_write_b128 v61, v[12:15] offset:48
	v_pk_fma_f32 v[6:7], v[2:3], v[6:7], v[0:1]
	ds_read_b128 v[0:3], v42 offset:144
	ds_write_b128 v61, v[4:7] offset:176
	s_waitcnt lgkmcnt(3)
; __device__ __forceinline__ bf16_t f2bf(float f) { unsigned u = __float_as_uint(f); u += 0x7fffu + ((u >> 16) & 1u); return (bf16_t)(u >> 16); }
; __host__ __device__ __forceinline__ int ktile_off(int tok, int d) { return (tok >> 6) * TILE_EL + (d >> 3) * 512 + (tok & 63) * 8 + (d & 7); }
; __device__ __forceinline__ void headpost(const P& p, int r, int hc, float* v, const float2* cs64, const float2* cs32) {
;     ...
;         for (int i = 0; i < 32; ++i) { const float2 cs = cs64[i]; const float a = v[i], c = v[i + 32]; v[i] = a * cs.x - c * cs.y; v[i + 32] = c * cs.x + a * cs.y; }
;         if (hc < 8) { bf16_t* q = QA + ((size_t)(b * 8 + hc) * SEQ + tok) * 64; for (int d = 0; d < 64; ++d) q[d] = f2bf(v[d] * QSCALE_A); }
;         else { const int kvh = hc - 8; bf16_t* k = meta ? MT + kvh * TILE_EL : KA + (size_t)(b * 2 + kvh) * HEAD_EL; const int tk = meta ? pos : tok; for (int d = 0; d < 64; ++d) k[ktile_off(tk, d)] = f2bf(v[d]); }
	v_mov_b32_e32 v7, v22
	v_mov_b32_e32 v22, v21
	v_mov_b32_e32 v6, v20
	v_pk_mul_f32 v[4:5], v[22:23], v[16:17]
	v_readlane_b32 s42, v254, 15
	v_pk_fma_f32 v[4:5], v[6:7], v[52:53], v[4:5] neg_lo:[0,0,1] neg_hi:[0,0,1]
	v_pk_mul_f32 v[6:7], v[6:7], v[16:17]
	v_readlane_b32 s43, v254, 16
	v_pk_fma_f32 v[12:13], v[22:23], v[52:53], v[6:7]
	ds_read_b128 v[20:23], v42 offset:160
	s_waitcnt lgkmcnt(2)
	v_mov_b32_e32 v15, v2
	v_mov_b32_e32 v2, v1
	v_mov_b32_e32 v14, v0
	v_pk_mul_f32 v[0:1], v[2:3], v[18:19]
	v_readlane_b32 s48, v254, 21
	v_pk_fma_f32 v[6:7], v[14:15], v[54:55], v[0:1] neg_lo:[0,0,1] neg_hi:[0,0,1]
	v_pk_mul_f32 v[0:1], v[14:15], v[18:19]
	ds_write_b128 v61, v[4:7] offset:64
	v_pk_fma_f32 v[14:15], v[2:3], v[54:55], v[0:1]
	ds_write_b128 v61, v[12:15] offset:192
	ds_read_b128 v[0:3], v61 offset:208
	ds_read_b128 v[4:7], v42 offset:176
	s_waitcnt lgkmcnt(4)
	v_mov_b32_e32 v18, v20
	v_mov_b32_e32 v19, v22
	v_mov_b32_e32 v22, v21
	s_waitcnt lgkmcnt(1)
	v_pk_mul_f32 v[16:17], v[22:23], v[0:1]
	v_pk_mul_f32 v[0:1], v[18:19], v[0:1]
	s_waitcnt lgkmcnt(0)
	v_mov_b32_e32 v24, v4
	v_mov_b32_e32 v25, v6
	v_mov_b32_e32 v6, v5
	v_pk_fma_f32 v[0:1], v[22:23], v[44:45], v[0:1]
	ds_read_b128 v[20:23], v42 offset:192
	v_pk_mul_f32 v[4:5], v[6:7], v[2:3]
	v_pk_mul_f32 v[2:3], v[24:25], v[2:3]
	ds_read_b128 v[12:15], v61 offset:224
	v_pk_fma_f32 v[2:3], v[6:7], v[46:47], v[2:3]
	ds_write_b128 v61, v[0:3] offset:208
	ds_read_b128 v[0:3], v42 offset:208
	s_waitcnt lgkmcnt(3)
	v_mov_b32_e32 v7, v22
	v_mov_b32_e32 v22, v21
	v_pk_fma_f32 v[16:17], v[18:19], v[44:45], v[16:17] neg_lo:[0,0,1] neg_hi:[0,0,1]
	v_pk_fma_f32 v[18:19], v[24:25], v[46:47], v[4:5] neg_lo:[0,0,1] neg_hi:[0,0,1]
	v_mov_b32_e32 v6, v20
	s_waitcnt lgkmcnt(2)
	v_pk_mul_f32 v[4:5], v[22:23], v[12:13]
	ds_write_b128 v61, v[16:19] offset:80
	v_pk_fma_f32 v[4:5], v[6:7], v[8:9], v[4:5] neg_lo:[0,0,1] neg_hi:[0,0,1]
	v_pk_mul_f32 v[6:7], v[6:7], v[12:13]
	s_waitcnt lgkmcnt(1)
	v_mov_b32_e32 v13, v2
	v_mov_b32_e32 v2, v1
	v_mov_b32_e32 v12, v0
	v_pk_mul_f32 v[0:1], v[2:3], v[14:15]
	v_pk_fma_f32 v[8:9], v[22:23], v[8:9], v[6:7]
	ds_read_b128 v[16:19], v42 offset:224
	v_pk_fma_f32 v[6:7], v[12:13], v[10:11], v[0:1] neg_lo:[0,0,1] neg_hi:[0,0,1]
	v_pk_mul_f32 v[0:1], v[12:13], v[14:15]
	ds_write_b128 v61, v[4:7] offset:96
	v_pk_fma_f32 v[10:11], v[2:3], v[10:11], v[0:1]
	ds_read_b128 v[0:3], v42 offset:240
	s_waitcnt lgkmcnt(2)
	v_mov_b32_e32 v7, v18
	v_mov_b32_e32 v18, v17
	ds_write_b128 v61, v[8:11] offset:224
	v_mov_b32_e32 v6, v16
	v_pk_mul_f32 v[4:5], v[18:19], v[28:29]
	s_waitcnt lgkmcnt(1)
	v_mov_b32_e32 v11, v2
	v_mov_b32_e32 v2, v1
	v_pk_fma_f32 v[4:5], v[6:7], v[38:39], v[4:5] neg_lo:[0,0,1] neg_hi:[0,0,1]
	v_pk_mul_f32 v[6:7], v[6:7], v[28:29]
	v_mov_b32_e32 v10, v0
	v_pk_mul_f32 v[0:1], v[2:3], v[30:31]
	v_pk_fma_f32 v[8:9], v[18:19], v[38:39], v[6:7]
	v_pk_fma_f32 v[6:7], v[10:11], v[40:41], v[0:1] neg_lo:[0,0,1] neg_hi:[0,0,1]
	v_pk_mul_f32 v[0:1], v[10:11], v[30:31]
	v_readlane_b32 s49, v254, 22
	v_pk_fma_f32 v[10:11], v[2:3], v[40:41], v[0:1]
	v_readlane_b32 s50, v254, 23
	v_readlane_b32 s51, v254, 24
	ds_write_b128 v61, v[4:7] offset:112
	ds_write_b128 v61, v[8:11] offset:240
	s_cbranch_vccz .LBB7_97
	s_add_i32 s2, s88, -8
	s_and_saveexec_b64 s[4:5], s[0:1]
	s_xor_b64 s[0:1], exec, s[4:5]
	v_lshl_add_u32 v0, v98, 1, s2
	v_ashrrev_i32_e32 v1, 31, v0
	v_lshlrev_b64 v[0:1], 19, v[0:1]
	v_lshl_add_u64 v[0:1], s[30:31], 0, v[0:1]
	s_mov_b64 s[4:5], 0xa000000
	v_lshl_add_u64 v[0:1], v[0:1], 0, s[4:5]
	v_lshlrev_b32_e32 v99, 6, v97
	v_lshlrev_b32_e32 v63, 3, v97
	s_andn2_saveexec_b64 s[0:1], s[0:1]
	s_cbranch_execz .LBB7_96
	s_lshl_b32 s2, s2, 13
	v_readlane_b32 s4, v254, 43
	s_add_u32 s4, s4, s2
	v_readlane_b32 s2, v254, 42
	s_addc_u32 s5, s2, 0
	v_mov_b64_e32 v[0:1], s[4:5]

; __device__ __forceinline__ float shx(float v, int m, int lane) { return __int_as_float(__builtin_amdgcn_ds_bpermute((lane ^ m) << 2, __float_as_int(v))); }
; __device__ __forceinline__ unsigned pk2(float lo, float hi) { return (unsigned)f2bf(lo) | ((unsigned)f2bf(hi) << 16); }
; __device__ __forceinline__ void ph0(const Ctx& c) {
;     ...
;     for (int m0 = (G > 42 ? gwx : gw) * 4; m0 < NROWS && (G <= 42 || vcu >= 21); m0 += (G > 42 ? NGWX : NGW) * 4) {
;         f32x4 v[4][4];
; #pragma unroll
;         for (int r = 0; r < 4; ++r) { const int m = m0 + r < NROWS ? m0 + r : NROWS - 1; const float* xr = m < T ? p.x + (size_t)m * DM : p.meta + (size_t)(m - T) * DM;
; #pragma unroll
;             for (int j = 0; j < 4; ++j) v[r][j] = ((const f32x4*)xr)[lane + 64 * j]; }
; #pragma unroll
;         for (int r = 0; r < 4; ++r) { const int m = m0 + r; float s = 0.f;
; #pragma unroll
;             for (int j = 0; j < 4; ++j) s += (v[r][j][0] * v[r][j][0] + v[r][j][1] * v[r][j][1]) + (v[r][j][2] * v[r][j][2] + v[r][j][3] * v[r][j][3]);
; #pragma unroll
;             for (int o = 1; o < 64; o <<= 1) s += shx(s, o, lane);
;             const float rs = rsqrtf(s * (1.0f / DM) + EPS);
;             if (m < NROWS) {
; #pragma unroll
;                 for (int j = 0; j < 4; ++j) { const f32x4 g = ((const f32x4*)p.g_attn)[lane + 64 * j]; const f32x4 y = v[r][j] * rs * g; u32x2 w; w.x = pk2(y[0], y[1]); w.y = pk2(y[2], y[3]); ((u32x2*)(XN + (size_t)m * DM))[lane + 64 * j] = w; } } }
.LBB7_120:
	s_add_i32 s0, s6, 0xffff0000
	s_cmp_lt_i32 s6, 0x10000
	v_readlane_b32 s36, v254, 9
	s_cselect_b32 s1, s7, 0
	s_cselect_b32 s0, s6, s0
	v_readlane_b32 s37, v254, 10
	v_readlane_b32 s38, v254, 11
	v_readlane_b32 s39, v254, 12
	s_cselect_b32 s13, s37, s39
	s_cselect_b32 s14, s36, s38
	s_lshl_b64 s[0:1], s[0:1], 12
	s_add_u32 s0, s14, s0
	s_addc_u32 s1, s13, s1
	v_lshl_add_u64 v[0:1], s[0:1], 0, v[66:67]
	global_load_dwordx4 v[74:77], v[0:1], off nt
	global_load_dwordx4 v[56:59], v[0:1], off offset:1024 nt
	global_load_dwordx4 v[32:35], v[0:1], off offset:3072 nt
	global_load_dwordx4 v[52:55], v[0:1], off offset:2048 nt
	global_load_dwordx4 v[78:81], v[62:63], off nt
	s_add_i32 s1, s6, 1
	s_min_i32 s0, s1, 0x1000f
	s_ashr_i32 s13, s0, 31
	s_add_i32 s14, s0, 0xffff0000
	s_cmp_lt_i32 s1, 0x10000
	s_cselect_b32 s15, s13, 0
	s_cselect_b32 s14, s0, s14
	s_cselect_b32 s0, s37, s39
	s_cselect_b32 s13, s36, s38
	s_lshl_b64 s[14:15], s[14:15], 12
	s_add_u32 s14, s13, s14
	s_addc_u32 s15, s0, s15
	v_lshl_add_u64 v[0:1], s[14:15], 0, v[66:67]
	global_load_dwordx4 v[48:51], v[0:1], off nt
	global_load_dwordx4 v[44:47], v[0:1], off offset:1024 nt
	global_load_dwordx4 v[40:43], v[0:1], off offset:2048 nt
	global_load_dwordx4 v[36:39], v[0:1], off offset:3072 nt
	s_add_i32 s0, s6, 2
	s_min_i32 s13, s0, 0x1000f
	s_ashr_i32 s14, s13, 31
	s_add_i32 s16, s13, 0xffff0000
	s_cmp_lt_i32 s0, 0x10000
	s_cselect_b32 s15, s14, 0
	s_cselect_b32 s14, s13, s16
	s_cselect_b32 s13, s37, s39
	s_cselect_b32 s16, s36, s38
	s_lshl_b64 s[14:15], s[14:15], 12
	s_add_u32 s14, s16, s14
	s_addc_u32 s15, s13, s15
	s_add_i32 s13, s6, 3
	v_readlane_b32 s40, v254, 13
	v_readlane_b32 s41, v254, 14
	v_readlane_b32 s42, v254, 15
	v_readlane_b32 s43, v254, 16
	v_readlane_b32 s44, v254, 17
	v_readlane_b32 s45, v254, 18
	v_readlane_b32 s46, v254, 19
	v_readlane_b32 s47, v254, 20
	v_readlane_b32 s48, v254, 21
	v_readlane_b32 s49, v254, 22
	v_readlane_b32 s50, v254, 23
	v_readlane_b32 s51, v254, 24
	s_waitcnt vmcnt(8)
	v_pk_mul_f32 v[0:1], v[76:77], v[76:77]
	v_pk_mul_f32 v[2:3], v[74:75], v[74:75]
	s_waitcnt vmcnt(7)
	v_pk_mul_f32 v[4:5], v[58:59], v[58:59]
	v_pk_mul_f32 v[6:7], v[56:57], v[56:57]
	v_pk_mov_b32 v[12:13], v[2:3], v[0:1] op_sel:[1,0]
	v_mov_b32_e32 v3, v1
	v_pk_mov_b32 v[0:1], v[6:7], v[4:5] op_sel:[1,0]
	v_mov_b32_e32 v7, v5
	s_waitcnt vmcnt(6)
	v_mul_f32_e32 v11, v32, v32
	s_waitcnt vmcnt(5)
	v_mul_f32_e32 v8, v53, v53
	v_mul_f32_e32 v10, v55, v55
	v_pk_add_f32 v[2:3], v[12:13], v[2:3]
	v_pk_add_f32 v[0:1], v[0:1], v[6:7]
	v_mul_f32_e32 v14, v33, v33
	v_mul_f32_e32 v15, v34, v34
	v_mul_f32_e32 v16, v35, v35
	v_pk_fma_f32 v[4:5], v[52:53], v[52:53], v[8:9] op_sel_hi:[1,1,0]
	v_pk_fma_f32 v[8:9], v[54:55], v[54:55], v[10:11] op_sel_hi:[1,1,0]
	v_pk_add_f32 v[2:3], v[2:3], v[2:3] op_sel:[0,1] op_sel_hi:[1,0]
	v_pk_add_f32 v[0:1], v[0:1], v[0:1] op_sel:[0,1] op_sel_hi:[1,0]
	v_mov_b32_e32 v5, v15
	v_mov_b32_e32 v9, v16
	v_mov_b32_e32 v3, v11
	v_mov_b32_e32 v1, v14
	v_pk_add_f32 v[4:5], v[4:5], v[8:9]
	v_pk_add_f32 v[0:1], v[2:3], v[0:1]
	s_nop 0
	v_pk_add_f32 v[0:1], v[0:1], v[4:5]
	s_nop 0
	v_add_f32_e32 v0, v0, v1
	ds_bpermute_b32 v1, v61, v0
	s_waitcnt lgkmcnt(0)
	v_add_f32_e32 v0, v0, v1
	ds_bpermute_b32 v1, v68, v0
	s_waitcnt lgkmcnt(0)
	v_add_f32_e32 v2, v0, v1
	ds_bpermute_b32 v3, v69, v2
	v_lshl_add_u64 v[0:1], s[14:15], 0, v[66:67]
	global_load_dwordx4 v[28:31], v[0:1], off nt
	global_load_dwordx4 v[24:27], v[0:1], off offset:1024 nt
	global_load_dwordx4 v[20:23], v[0:1], off offset:2048 nt
	global_load_dwordx4 v[16:19], v[0:1], off offset:3072 nt
	s_min_i32 s14, s13, 0x1000f
	s_waitcnt lgkmcnt(0)
	v_add_f32_e32 v2, v2, v3
	ds_bpermute_b32 v3, v70, v2
	s_ashr_i32 s15, s14, 31
	s_add_i32 s16, s14, 0xffff0000
	s_cmp_lt_i32 s13, 0x10000
	s_cselect_b32 s15, s15, 0
	s_waitcnt lgkmcnt(0)
	v_add_f32_e32 v0, v2, v3
	ds_bpermute_b32 v1, v71, v0
	s_cselect_b32 s14, s14, s16
	s_cselect_b32 s16, s37, s39
	s_cselect_b32 s17, s36, s38
	s_lshl_b64 s[14:15], s[14:15], 12
	s_waitcnt lgkmcnt(0)
	v_add_f32_e32 v2, v0, v1
	ds_bpermute_b32 v3, v72, v2
	s_add_u32 s14, s17, s14
	s_addc_u32 s15, s16, s15
	v_lshl_add_u64 v[0:1], s[14:15], 0, v[66:67]
	s_cmp_lt_i32 s1, 0x10010
	s_waitcnt lgkmcnt(0)
	v_add_f32_e32 v2, v2, v3
	v_fmamk_f32 v2, v2, 0x3a800000, v73
	v_mul_f32_e32 v3, 0x4b800000, v2
	v_cmp_gt_f32_e32 vcc, s10, v2
	s_nop 1
	v_cndmask_b32_e32 v2, v2, v3, vcc
	v_rsq_f32_e32 v82, v2
	global_load_dwordx4 v[12:15], v[0:1], off nt
	global_load_dwordx4 v[8:11], v[0:1], off offset:1024 nt
	global_load_dwordx4 v[4:7], v[0:1], off offset:2048 nt
	s_nop 0
	global_load_dwordx4 v[0:3], v[0:1], off offset:3072 nt
	v_mul_f32_e32 v83, 0x45800000, v82
	v_cndmask_b32_e32 v82, v82, v83, vcc
	v_pk_mul_f32 v[74:75], v[74:75], v[82:83] op_sel_hi:[1,0]
	v_pk_mul_f32 v[76:77], v[76:77], v[82:83] op_sel_hi:[1,0]
	s_waitcnt vmcnt(12)
	v_pk_mul_f32 v[74:75], v[78:79], v[74:75]
	v_pk_mul_f32 v[76:77], v[80:81], v[76:77]
	v_bfe_u32 v78, v74, 16, 1
	v_bfe_u32 v80, v76, 16, 1
	v_bfe_u32 v79, v75, 16, 1
	v_bfe_u32 v81, v77, 16, 1
	v_add3_u32 v74, v74, v78, s11
	v_add3_u32 v76, v76, v80, s11
	v_add3_u32 v75, v75, v79, s11
	v_add3_u32 v77, v77, v81, s11
	v_lshrrev_b32_e32 v74, 16, v74
	v_lshrrev_b32_e32 v76, 16, v76
	v_and_or_b32 v74, v75, s2, v74
	v_and_or_b32 v75, v77, s2, v76
	global_store_dwordx2 v[64:65], v[74:75], off
	global_load_dwordx4 v[74:77], v[62:63], off offset:1024 nt
	v_pk_mul_f32 v[56:57], v[56:57], v[82:83] op_sel_hi:[1,0]
	v_pk_mul_f32 v[58:59], v[58:59], v[82:83] op_sel_hi:[1,0]
	v_pk_mul_f32 v[52:53], v[52:53], v[82:83] op_sel_hi:[1,0]
	v_pk_mul_f32 v[54:55], v[54:55], v[82:83] op_sel_hi:[1,0]
	v_pk_mul_f32 v[32:33], v[32:33], v[82:83] op_sel_hi:[1,0]
	v_pk_mul_f32 v[34:35], v[34:35], v[82:83] op_sel_hi:[1,0]
	s_waitcnt vmcnt(0)
; __device__ __forceinline__ float shx(float v, int m, int lane) { return __int_as_float(__builtin_amdgcn_ds_bpermute((lane ^ m) << 2, __float_as_int(v))); }
; __device__ __forceinline__ unsigned pk2(float lo, float hi) { return (unsigned)f2bf(lo) | ((unsigned)f2bf(hi) << 16); }
; __device__ __forceinline__ void ph0(const Ctx& c) {
;     ...
;         for (int r = 0; r < 4; ++r) { const int m = m0 + r; float s = 0.f;
; #pragma unroll
;             for (int j = 0; j < 4; ++j) s += (v[r][j][0] * v[r][j][0] + v[r][j][1] * v[r][j][1]) + (v[r][j][2] * v[r][j][2] + v[r][j][3] * v[r][j][3]);
; #pragma unroll
;             for (int o = 1; o < 64; o <<= 1) s += shx(s, o, lane);
;             const float rs = rsqrtf(s * (1.0f / DM) + EPS);
;             if (m < NROWS) {
; #pragma unroll
;                 for (int j = 0; j < 4; ++j) { const f32x4 g = ((const f32x4*)p.g_attn)[lane + 64 * j]; const f32x4 y = v[r][j] * rs * g; u32x2 w; w.x = pk2(y[0], y[1]); w.y = pk2(y[2], y[3]); ((u32x2*)(XN + (size_t)m * DM))[lane + 64 * j] = w; } } }
	v_pk_mul_f32 v[58:59], v[76:77], v[58:59]
	v_pk_mul_f32 v[56:57], v[74:75], v[56:57]
	v_bfe_u32 v76, v58, 16, 1
	v_bfe_u32 v74, v56, 16, 1
	v_bfe_u32 v75, v57, 16, 1
	v_bfe_u32 v77, v59, 16, 1
	v_add3_u32 v56, v56, v74, s11
	v_add3_u32 v58, v58, v76, s11
	v_add3_u32 v57, v57, v75, s11
	v_add3_u32 v59, v59, v77, s11
	v_lshrrev_b32_e32 v56, 16, v56
	v_lshrrev_b32_e32 v58, 16, v58
	v_and_or_b32 v56, v57, s2, v56
	v_and_or_b32 v57, v59, s2, v58
	global_store_dwordx2 v[64:65], v[56:57], off offset:512
	global_load_dwordx4 v[56:59], v[62:63], off offset:2048 nt
	v_mul_f32_e32 v74, v41, v41
	v_mul_f32_e32 v75, v43, v43
	v_mul_f32_e32 v76, v37, v37
	v_mul_f32_e32 v77, v39, v39
	v_fmac_f32_e32 v74, v40, v40
	v_fmac_f32_e32 v75, v42, v42
	v_fmac_f32_e32 v76, v36, v36
	v_fmac_f32_e32 v77, v38, v38
	s_waitcnt vmcnt(0)
	v_pk_mul_f32 v[54:55], v[58:59], v[54:55]
	v_pk_mul_f32 v[52:53], v[56:57], v[52:53]
	v_bfe_u32 v58, v54, 16, 1
	v_bfe_u32 v56, v52, 16, 1
	v_bfe_u32 v57, v53, 16, 1
	v_bfe_u32 v59, v55, 16, 1
	v_add3_u32 v52, v52, v56, s11
	v_add3_u32 v54, v54, v58, s11
	v_add3_u32 v53, v53, v57, s11
	v_add3_u32 v55, v55, v59, s11
	v_lshrrev_b32_e32 v52, 16, v52
	v_lshrrev_b32_e32 v54, 16, v54
	v_and_or_b32 v52, v53, s2, v52
	v_and_or_b32 v53, v55, s2, v54
	global_store_dwordx2 v[64:65], v[52:53], off offset:1024
	global_load_dwordx4 v[54:57], v[62:63], off offset:3072 nt
	v_mul_f32_e32 v52, v49, v49
	v_mul_f32_e32 v53, v51, v51
	v_mul_f32_e32 v58, v45, v45
	v_mul_f32_e32 v59, v47, v47
	v_fmac_f32_e32 v52, v48, v48
	v_fmac_f32_e32 v53, v50, v50
	v_fmac_f32_e32 v58, v44, v44
	v_fmac_f32_e32 v59, v46, v46
	v_add_f32_e32 v52, v52, v53
	v_add_f32_e32 v53, v58, v59
	v_add_f32_e32 v58, v74, v75
	v_add_f32_e32 v52, v52, v53
	v_add_f32_e32 v59, v76, v77
	v_add_f32_e32 v52, v52, v58
	v_add_f32_e32 v52, v52, v59
	ds_bpermute_b32 v53, v61, v52
	s_waitcnt lgkmcnt(0)
	v_add_f32_e32 v52, v52, v53
	ds_bpermute_b32 v53, v68, v52
	s_waitcnt lgkmcnt(0)
	v_add_f32_e32 v52, v52, v53
	ds_bpermute_b32 v53, v69, v52
	s_waitcnt lgkmcnt(0)
	v_add_f32_e32 v52, v52, v53
	ds_bpermute_b32 v53, v70, v52
	s_waitcnt lgkmcnt(0)
	v_add_f32_e32 v52, v52, v53
	ds_bpermute_b32 v53, v71, v52
	s_waitcnt lgkmcnt(0)
	v_add_f32_e32 v52, v52, v53
	ds_bpermute_b32 v53, v72, v52
	s_waitcnt vmcnt(0)
	v_pk_mul_f32 v[34:35], v[56:57], v[34:35]
	v_pk_mul_f32 v[32:33], v[54:55], v[32:33]
	v_bfe_u32 v56, v34, 16, 1
	v_bfe_u32 v54, v32, 16, 1
	v_bfe_u32 v55, v33, 16, 1
	v_bfe_u32 v57, v35, 16, 1
	v_add3_u32 v32, v32, v54, s11
	v_add3_u32 v34, v34, v56, s11
	v_add3_u32 v33, v33, v55, s11
	v_add3_u32 v35, v35, v57, s11
	v_lshrrev_b32_e32 v32, 16, v32
	v_lshrrev_b32_e32 v34, 16, v34
	v_and_or_b32 v32, v33, s2, v32
	v_and_or_b32 v33, v35, s2, v34
	global_store_dwordx2 v[64:65], v[32:33], off offset:1536
	s_cbranch_scc0 .LBB7_122
	global_load_dwordx4 v[32:35], v[62:63], off nt
	s_waitcnt lgkmcnt(0)
	v_add_f32_e32 v52, v52, v53
	v_fmamk_f32 v52, v52, 0x3a800000, v73
	v_mul_f32_e32 v53, 0x4b800000, v52
	v_cmp_gt_f32_e32 vcc, s10, v52
	s_nop 1
	v_cndmask_b32_e32 v52, v52, v53, vcc
	v_rsq_f32_e32 v52, v52
	s_nop 0
	v_mul_f32_e32 v53, 0x45800000, v52
	v_cndmask_b32_e32 v52, v52, v53, vcc
	v_pk_mul_f32 v[48:49], v[48:49], v[52:53] op_sel_hi:[1,0]
	v_pk_mul_f32 v[50:51], v[50:51], v[52:53] op_sel_hi:[1,0]
	v_pk_mul_f32 v[44:45], v[44:45], v[52:53] op_sel_hi:[1,0]
	v_pk_mul_f32 v[46:47], v[46:47], v[52:53] op_sel_hi:[1,0]
	v_pk_mul_f32 v[40:41], v[40:41], v[52:53] op_sel_hi:[1,0]
	v_pk_mul_f32 v[42:43], v[42:43], v[52:53] op_sel_hi:[1,0]
	v_pk_mul_f32 v[36:37], v[36:37], v[52:53] op_sel_hi:[1,0]
	v_pk_mul_f32 v[38:39], v[38:39], v[52:53] op_sel_hi:[1,0]
	s_waitcnt vmcnt(0)
	v_pk_mul_f32 v[34:35], v[50:51], v[34:35]
	v_pk_mul_f32 v[32:33], v[48:49], v[32:33]
	v_bfe_u32 v50, v34, 16, 1
	v_bfe_u32 v48, v32, 16, 1
	v_bfe_u32 v49, v33, 16, 1
	v_bfe_u32 v51, v35, 16, 1
	v_add3_u32 v32, v32, v48, s11
	v_add3_u32 v34, v34, v50, s11
	v_add3_u32 v33, v33, v49, s11
	v_add3_u32 v35, v35, v51, s11
	v_lshrrev_b32_e32 v32, 16, v32
	v_lshrrev_b32_e32 v34, 16, v34
	v_and_or_b32 v32, v33, s2, v32
	v_and_or_b32 v33, v35, s2, v34
	global_store_dwordx2 v[64:65], v[32:33], off offset:2048
	global_load_dwordx4 v[32:35], v[62:63], off offset:1024 nt
	s_waitcnt vmcnt(0)
	v_pk_mul_f32 v[34:35], v[46:47], v[34:35]
	v_pk_mul_f32 v[32:33], v[44:45], v[32:33]
	v_bfe_u32 v46, v34, 16, 1
	v_bfe_u32 v44, v32, 16, 1
	v_bfe_u32 v45, v33, 16, 1
	v_bfe_u32 v47, v35, 16, 1
	v_add3_u32 v32, v32, v44, s11
	v_add3_u32 v34, v34, v46, s11
	v_add3_u32 v33, v33, v45, s11
	v_add3_u32 v35, v35, v47, s11
	v_lshrrev_b32_e32 v32, 16, v32
	v_lshrrev_b32_e32 v34, 16, v34
	v_and_or_b32 v32, v33, s2, v32
	v_and_or_b32 v33, v35, s2, v34
	global_store_dwordx2 v[64:65], v[32:33], off offset:2560
	global_load_dwordx4 v[32:35], v[62:63], off offset:2048 nt
	s_waitcnt vmcnt(0)
	v_pk_mul_f32 v[34:35], v[42:43], v[34:35]
	v_pk_mul_f32 v[32:33], v[40:41], v[32:33]
	v_bfe_u32 v42, v34, 16, 1
	v_bfe_u32 v40, v32, 16, 1
	v_bfe_u32 v41, v33, 16, 1
	v_bfe_u32 v43, v35, 16, 1
	v_add3_u32 v32, v32, v40, s11
	v_add3_u32 v34, v34, v42, s11
	v_add3_u32 v33, v33, v41, s11
	v_add3_u32 v35, v35, v43, s11
	v_lshrrev_b32_e32 v32, 16, v32
	v_lshrrev_b32_e32 v34, 16, v34
	v_and_or_b32 v32, v33, s2, v32
	v_and_or_b32 v33, v35, s2, v34
	global_store_dwordx2 v[64:65], v[32:33], off offset:3072
	global_load_dwordx4 v[32:35], v[62:63], off offset:3072 nt
	s_waitcnt vmcnt(0)
	v_pk_mul_f32 v[34:35], v[38:39], v[34:35]
	v_pk_mul_f32 v[32:33], v[36:37], v[32:33]
	v_bfe_u32 v38, v34, 16, 1
	v_bfe_u32 v36, v32, 16, 1
	v_bfe_u32 v37, v33, 16, 1
	v_bfe_u32 v39, v35, 16, 1
	v_add3_u32 v32, v32, v36, s11
	v_add3_u32 v34, v34, v38, s11
	v_add3_u32 v33, v33, v37, s11
	v_add3_u32 v35, v35, v39, s11
	v_lshrrev_b32_e32 v32, 16, v32
	v_lshrrev_b32_e32 v34, 16, v34
	v_and_or_b32 v32, v33, s2, v32
	v_and_or_b32 v33, v35, s2, v34
	global_store_dwordx2 v[64:65], v[32:33], off offset:3584
; __device__ __forceinline__ float shx(float v, int m, int lane) { return __int_as_float(__builtin_amdgcn_ds_bpermute((lane ^ m) << 2, __float_as_int(v))); }
; __device__ __forceinline__ unsigned pk2(float lo, float hi) { return (unsigned)f2bf(lo) | ((unsigned)f2bf(hi) << 16); }
; __device__ __forceinline__ void ph0(const Ctx& c) {
;     ...
;         for (int r = 0; r < 4; ++r) { const int m = m0 + r; float s = 0.f;
; #pragma unroll
;             for (int j = 0; j < 4; ++j) s += (v[r][j][0] * v[r][j][0] + v[r][j][1] * v[r][j][1]) + (v[r][j][2] * v[r][j][2] + v[r][j][3] * v[r][j][3]);
; #pragma unroll
;             for (int o = 1; o < 64; o <<= 1) s += shx(s, o, lane);
;             const float rs = rsqrtf(s * (1.0f / DM) + EPS);
;             if (m < NROWS) {
; #pragma unroll
;                 for (int j = 0; j < 4; ++j) { const f32x4 g = ((const f32x4*)p.g_attn)[lane + 64 * j]; const f32x4 y = v[r][j] * rs * g; u32x2 w; w.x = pk2(y[0], y[1]); w.y = pk2(y[2], y[3]); ((u32x2*)(XN + (size_t)m * DM))[lane + 64 * j] = w; } } }
.LBB7_122:
	v_mul_f32_e32 v32, v29, v29
	v_mul_f32_e32 v33, v31, v31
	v_fmac_f32_e32 v32, v28, v28
	v_fmac_f32_e32 v33, v30, v30
	v_add_f32_e32 v32, v32, v33
	v_mul_f32_e32 v33, v25, v25
	v_mul_f32_e32 v34, v27, v27
	v_fmac_f32_e32 v33, v24, v24
	v_fmac_f32_e32 v34, v26, v26
	v_add_f32_e32 v33, v33, v34
	v_add_f32_e32 v32, v32, v33
	v_mul_f32_e32 v33, v21, v21
	v_mul_f32_e32 v34, v23, v23
	v_fmac_f32_e32 v33, v20, v20
	v_fmac_f32_e32 v34, v22, v22
	v_add_f32_e32 v33, v33, v34
	v_add_f32_e32 v32, v32, v33
	v_mul_f32_e32 v33, v17, v17
	v_mul_f32_e32 v34, v19, v19
	v_fmac_f32_e32 v33, v16, v16
	v_fmac_f32_e32 v34, v18, v18
	v_add_f32_e32 v33, v33, v34
	v_add_f32_e32 v32, v32, v33
	ds_bpermute_b32 v33, v61, v32
	s_cmp_gt_i32 s0, 0x1000f
	s_waitcnt lgkmcnt(0)
	v_add_f32_e32 v32, v32, v33
	ds_bpermute_b32 v33, v68, v32
	s_waitcnt lgkmcnt(0)
	v_add_f32_e32 v32, v32, v33
	ds_bpermute_b32 v33, v69, v32
	s_waitcnt lgkmcnt(0)
	v_add_f32_e32 v32, v32, v33
	ds_bpermute_b32 v33, v70, v32
	s_waitcnt lgkmcnt(0)
	v_add_f32_e32 v32, v32, v33
	ds_bpermute_b32 v33, v71, v32
	s_waitcnt lgkmcnt(0)
	v_add_f32_e32 v32, v32, v33
	ds_bpermute_b32 v33, v72, v32
	s_cbranch_scc1 .LBB7_124
	global_load_dwordx4 v[34:37], v[62:63], off nt
	s_waitcnt lgkmcnt(0)
	v_add_f32_e32 v32, v32, v33
	v_fmamk_f32 v32, v32, 0x3a800000, v73
	v_mul_f32_e32 v33, 0x4b800000, v32
	v_cmp_gt_f32_e32 vcc, s10, v32
	s_nop 1
	v_cndmask_b32_e32 v32, v32, v33, vcc
	v_rsq_f32_e32 v38, v32
	v_add_co_u32_e64 v32, s[0:1], s12, v64
	v_mul_f32_e32 v39, 0x45800000, v38
	v_cndmask_b32_e32 v38, v38, v39, vcc
	v_pk_mul_f32 v[28:29], v[28:29], v[38:39] op_sel_hi:[1,0]
	v_pk_mul_f32 v[30:31], v[30:31], v[38:39] op_sel_hi:[1,0]
	v_addc_co_u32_e64 v33, s[0:1], 0, v65, s[0:1]
	v_pk_mul_f32 v[24:25], v[24:25], v[38:39] op_sel_hi:[1,0]
	v_pk_mul_f32 v[26:27], v[26:27], v[38:39] op_sel_hi:[1,0]
	v_pk_mul_f32 v[20:21], v[20:21], v[38:39] op_sel_hi:[1,0]
	v_pk_mul_f32 v[22:23], v[22:23], v[38:39] op_sel_hi:[1,0]
	v_pk_mul_f32 v[16:17], v[16:17], v[38:39] op_sel_hi:[1,0]
	v_pk_mul_f32 v[18:19], v[18:19], v[38:39] op_sel_hi:[1,0]
	s_waitcnt vmcnt(0)
	v_pk_mul_f32 v[30:31], v[30:31], v[36:37]
	v_pk_mul_f32 v[28:29], v[28:29], v[34:35]
	v_bfe_u32 v36, v30, 16, 1
	v_bfe_u32 v34, v28, 16, 1
	v_bfe_u32 v35, v29, 16, 1
	v_bfe_u32 v37, v31, 16, 1
	v_add3_u32 v28, v28, v34, s11
	v_add3_u32 v30, v30, v36, s11
	v_add3_u32 v29, v29, v35, s11
	v_add3_u32 v31, v31, v37, s11
	v_lshrrev_b32_e32 v28, 16, v28
	v_lshrrev_b32_e32 v30, 16, v30
	v_and_or_b32 v28, v29, s2, v28
	v_and_or_b32 v29, v31, s2, v30
	global_store_dwordx2 v[32:33], v[28:29], off
	global_load_dwordx4 v[28:31], v[62:63], off offset:1024 nt
	s_waitcnt vmcnt(0)
	v_pk_mul_f32 v[26:27], v[26:27], v[30:31]
	v_pk_mul_f32 v[24:25], v[24:25], v[28:29]
	v_bfe_u32 v30, v26, 16, 1
	v_bfe_u32 v28, v24, 16, 1
	v_bfe_u32 v29, v25, 16, 1
	v_bfe_u32 v31, v27, 16, 1
	v_add3_u32 v24, v24, v28, s11
	v_add3_u32 v26, v26, v30, s11
	v_add3_u32 v25, v25, v29, s11
	v_add3_u32 v27, v27, v31, s11
	v_lshrrev_b32_e32 v24, 16, v24
	v_lshrrev_b32_e32 v26, 16, v26
	v_and_or_b32 v24, v25, s2, v24
	v_and_or_b32 v25, v27, s2, v26
	global_store_dwordx2 v[32:33], v[24:25], off offset:512
	global_load_dwordx4 v[24:27], v[62:63], off offset:2048 nt
	s_waitcnt vmcnt(0)
	v_pk_mul_f32 v[22:23], v[22:23], v[26:27]
	v_pk_mul_f32 v[20:21], v[20:21], v[24:25]
	v_bfe_u32 v26, v22, 16, 1
	v_bfe_u32 v24, v20, 16, 1
	v_bfe_u32 v25, v21, 16, 1
	v_bfe_u32 v27, v23, 16, 1
	v_add3_u32 v20, v20, v24, s11
	v_add3_u32 v22, v22, v26, s11
	v_add3_u32 v21, v21, v25, s11
	v_add3_u32 v23, v23, v27, s11
	v_lshrrev_b32_e32 v20, 16, v20
	v_lshrrev_b32_e32 v22, 16, v22
	v_and_or_b32 v20, v21, s2, v20
	v_and_or_b32 v21, v23, s2, v22
	global_store_dwordx2 v[32:33], v[20:21], off offset:1024
	global_load_dwordx4 v[20:23], v[62:63], off offset:3072 nt
	s_waitcnt vmcnt(0)
	v_pk_mul_f32 v[18:19], v[18:19], v[22:23]
	v_pk_mul_f32 v[16:17], v[16:17], v[20:21]
	v_bfe_u32 v22, v18, 16, 1
	v_bfe_u32 v20, v16, 16, 1
	v_bfe_u32 v21, v17, 16, 1
	v_bfe_u32 v23, v19, 16, 1
	v_add3_u32 v16, v16, v20, s11
	v_add3_u32 v18, v18, v22, s11
	v_add3_u32 v17, v17, v21, s11
	v_add3_u32 v19, v19, v23, s11
	v_lshrrev_b32_e32 v16, 16, v16
	v_lshrrev_b32_e32 v18, 16, v18
	v_and_or_b32 v16, v17, s2, v16
	v_and_or_b32 v17, v19, s2, v18
	global_store_dwordx2 v[32:33], v[16:17], off offset:1536
; __device__ __forceinline__ float shx(float v, int m, int lane) { return __int_as_float(__builtin_amdgcn_ds_bpermute((lane ^ m) << 2, __float_as_int(v))); }
; __device__ __forceinline__ unsigned pk2(float lo, float hi) { return (unsigned)f2bf(lo) | ((unsigned)f2bf(hi) << 16); }
; __device__ __forceinline__ void ph0(const Ctx& c) {
;     ...
;         for (int r = 0; r < 4; ++r) { const int m = m0 + r; float s = 0.f;
; #pragma unroll
;             for (int j = 0; j < 4; ++j) s += (v[r][j][0] * v[r][j][0] + v[r][j][1] * v[r][j][1]) + (v[r][j][2] * v[r][j][2] + v[r][j][3] * v[r][j][3]);
; #pragma unroll
;             for (int o = 1; o < 64; o <<= 1) s += shx(s, o, lane);
;             const float rs = rsqrtf(s * (1.0f / DM) + EPS);
;             if (m < NROWS) {
; #pragma unroll
;                 for (int j = 0; j < 4; ++j) { const f32x4 g = ((const f32x4*)p.g_attn)[lane + 64 * j]; const f32x4 y = v[r][j] * rs * g; u32x2 w; w.x = pk2(y[0], y[1]); w.y = pk2(y[2], y[3]); ((u32x2*)(XN + (size_t)m * DM))[lane + 64 * j] = w; } } }
.LBB7_124:
	v_mul_f32_e32 v16, v13, v13
	v_mul_f32_e32 v17, v15, v15
	v_fmac_f32_e32 v16, v12, v12
	v_fmac_f32_e32 v17, v14, v14
	v_add_f32_e32 v16, v16, v17
	v_mul_f32_e32 v17, v9, v9
	v_mul_f32_e32 v18, v11, v11
	v_fmac_f32_e32 v17, v8, v8
	v_fmac_f32_e32 v18, v10, v10
	v_add_f32_e32 v17, v17, v18
	v_add_f32_e32 v16, v16, v17
	v_mul_f32_e32 v17, v5, v5
	v_mul_f32_e32 v18, v7, v7
	v_fmac_f32_e32 v17, v4, v4
	v_fmac_f32_e32 v18, v6, v6
	v_add_f32_e32 v17, v17, v18
	v_add_f32_e32 v16, v16, v17
	v_mul_f32_e32 v17, v1, v1
	v_mul_f32_e32 v18, v3, v3
	v_fmac_f32_e32 v17, v0, v0
	v_fmac_f32_e32 v18, v2, v2
	v_add_f32_e32 v17, v17, v18
	v_add_f32_e32 v16, v16, v17
	ds_bpermute_b32 v17, v61, v16
	s_cmp_gt_i32 s13, 0x1000f
	s_waitcnt lgkmcnt(0)
	v_add_f32_e32 v16, v16, v17
	ds_bpermute_b32 v17, v68, v16
	s_waitcnt lgkmcnt(0)
	v_add_f32_e32 v16, v16, v17
	ds_bpermute_b32 v17, v69, v16
	s_waitcnt lgkmcnt(0)
	v_add_f32_e32 v16, v16, v17
	ds_bpermute_b32 v17, v70, v16
	s_waitcnt lgkmcnt(0)
	v_add_f32_e32 v16, v16, v17
	ds_bpermute_b32 v17, v71, v16
	s_waitcnt lgkmcnt(0)
	v_add_f32_e32 v16, v16, v17
	ds_bpermute_b32 v17, v72, v16
	s_cbranch_scc1 .LBB7_119
	global_load_dwordx4 v[18:21], v[62:63], off nt
	s_waitcnt lgkmcnt(0)
	v_add_f32_e32 v16, v16, v17
	v_fmamk_f32 v16, v16, 0x3a800000, v73
	v_mul_f32_e32 v17, 0x4b800000, v16
	v_cmp_gt_f32_e32 vcc, s10, v16
	s_nop 1
	v_cndmask_b32_e32 v16, v16, v17, vcc
	v_rsq_f32_e32 v22, v16
	v_add_co_u32_e64 v16, s[0:1], s12, v64
	v_mul_f32_e32 v23, 0x45800000, v22
	v_cndmask_b32_e32 v22, v22, v23, vcc
	v_pk_mul_f32 v[12:13], v[12:13], v[22:23] op_sel_hi:[1,0]
	v_pk_mul_f32 v[14:15], v[14:15], v[22:23] op_sel_hi:[1,0]
	v_addc_co_u32_e64 v17, s[0:1], 0, v65, s[0:1]
	v_pk_mul_f32 v[8:9], v[8:9], v[22:23] op_sel_hi:[1,0]
	v_pk_mul_f32 v[10:11], v[10:11], v[22:23] op_sel_hi:[1,0]
	v_pk_mul_f32 v[4:5], v[4:5], v[22:23] op_sel_hi:[1,0]
	v_pk_mul_f32 v[6:7], v[6:7], v[22:23] op_sel_hi:[1,0]
	v_pk_mul_f32 v[0:1], v[0:1], v[22:23] op_sel_hi:[1,0]
	v_pk_mul_f32 v[2:3], v[2:3], v[22:23] op_sel_hi:[1,0]
	s_waitcnt vmcnt(0)
	v_pk_mul_f32 v[14:15], v[14:15], v[20:21]
	v_pk_mul_f32 v[12:13], v[12:13], v[18:19]
	v_bfe_u32 v20, v14, 16, 1
	v_bfe_u32 v18, v12, 16, 1
	v_bfe_u32 v19, v13, 16, 1
	v_bfe_u32 v21, v15, 16, 1
	v_add3_u32 v12, v12, v18, s11
	v_add3_u32 v14, v14, v20, s11
	v_add3_u32 v13, v13, v19, s11
	v_add3_u32 v15, v15, v21, s11
	v_lshrrev_b32_e32 v12, 16, v12
	v_lshrrev_b32_e32 v14, 16, v14
	v_and_or_b32 v12, v13, s2, v12
	v_and_or_b32 v13, v15, s2, v14
	global_store_dwordx2 v[16:17], v[12:13], off offset:2048
	global_load_dwordx4 v[12:15], v[62:63], off offset:1024 nt
	s_waitcnt vmcnt(0)
	v_pk_mul_f32 v[10:11], v[10:11], v[14:15]
	v_pk_mul_f32 v[8:9], v[8:9], v[12:13]
	v_bfe_u32 v14, v10, 16, 1
	v_bfe_u32 v12, v8, 16, 1
	v_bfe_u32 v13, v9, 16, 1
	v_bfe_u32 v15, v11, 16, 1
	v_add3_u32 v8, v8, v12, s11
	v_add3_u32 v10, v10, v14, s11
	v_add3_u32 v9, v9, v13, s11
	v_add3_u32 v11, v11, v15, s11
	v_lshrrev_b32_e32 v8, 16, v8
	v_lshrrev_b32_e32 v10, 16, v10
	v_and_or_b32 v8, v9, s2, v8
	v_and_or_b32 v9, v11, s2, v10
	global_store_dwordx2 v[16:17], v[8:9], off offset:2560
	global_load_dwordx4 v[8:11], v[62:63], off offset:2048 nt
	s_waitcnt vmcnt(0)
	v_pk_mul_f32 v[6:7], v[6:7], v[10:11]
	v_pk_mul_f32 v[4:5], v[4:5], v[8:9]
	v_bfe_u32 v10, v6, 16, 1
	v_bfe_u32 v8, v4, 16, 1
	v_bfe_u32 v9, v5, 16, 1
	v_bfe_u32 v11, v7, 16, 1
	v_add3_u32 v4, v4, v8, s11
	v_add3_u32 v6, v6, v10, s11
	v_add3_u32 v5, v5, v9, s11
	v_add3_u32 v7, v7, v11, s11
	v_lshrrev_b32_e32 v4, 16, v4
	v_lshrrev_b32_e32 v6, 16, v6
	v_and_or_b32 v4, v5, s2, v4
	v_and_or_b32 v5, v7, s2, v6
	global_store_dwordx2 v[16:17], v[4:5], off offset:3072
	global_load_dwordx4 v[4:7], v[62:63], off offset:3072 nt
	s_waitcnt vmcnt(0)
	v_pk_mul_f32 v[2:3], v[2:3], v[6:7]
	v_pk_mul_f32 v[0:1], v[0:1], v[4:5]
	v_bfe_u32 v6, v2, 16, 1
	v_bfe_u32 v4, v0, 16, 1
	v_bfe_u32 v5, v1, 16, 1
	v_bfe_u32 v7, v3, 16, 1
	v_add3_u32 v0, v0, v4, s11
	v_add3_u32 v2, v2, v6, s11
	v_add3_u32 v1, v1, v5, s11
	v_add3_u32 v3, v3, v7, s11
	v_lshrrev_b32_e32 v0, 16, v0
	v_lshrrev_b32_e32 v2, 16, v2
	v_and_or_b32 v0, v1, s2, v0
	v_and_or_b32 v1, v3, s2, v2
	global_store_dwordx2 v[16:17], v[0:1], off offset:3584
	s_branch .LBB7_119

; #define LAS __attribute__((address_space(3)))
; __device__ __forceinline__ int fresh_lane() { unsigned z = 0u; asm volatile("" : "+v"(z)); return (int)__builtin_amdgcn_mbcnt_hi(~0u, __builtin_amdgcn_mbcnt_lo(~0u, z)); }
; __device__ __forceinline__ void ph4(const Ctx& c) {
;     const P& p = *c.pp; const int wave = c.wave, lane = fresh_lane(), tid = wave * 64 + lane; LAS unsigned char* L = c.lds + RING_OFF;
;     LAS int* lhist = (LAS int*)(L + R_HIST); LAS int* lbase = lhist + 32; LAS int* lsel = (LAS int*)(L + R_SEL); LAS float* lgate = (LAS float*)(L + R_GATE);
;     unsigned* counts = c.ctl + CW_COUNT;
;     bf16x8 bh[4][2], bl[4][2]; f32x4 gq[4];
;     { const bf16_t* wh = (const bf16_t*)(p.ws + WS_WRT); const bf16_t* wl = wh + NE * DM;
; #pragma unroll
;       for (int s = 0; s < 4; ++s)
; #pragma unroll
;           for (int eb = 0; eb < 2; ++eb) { const size_t o = (size_t)(16 * eb + (lane & 15)) * DM + 128 * wave + 32 * s + 8 * (lane >> 4); bh[s][eb] = *(const bf16x8*)(wh + o); bl[s][eb] = *(const bf16x8*)(wl + o); }
; #pragma unroll
;       for (int j = 0; j < 4; ++j) gq[j] = ((const f32x4*)p.g_ffn)[lane + 64 * j]; }
;     const float bias = p.b_router[lane & 31];
;     for (int ch = c.bx; ch < T / 256; ch += c.G) {
.LBB7_686:
	v_readlane_b32 s4, v254, 2
	s_cmp_lt_i32 s4, 5
	s_cselect_b64 s[10:11], -1, 0
	s_and_b64 s[0:1], s[10:11], s[0:1]
	s_andn2_b64 vcc, exec, s[0:1]
	v_readlane_b32 s5, v254, 3
	s_cbranch_vccnz .LBB7_705
	v_mov_b32_e32 v145, 0
	s_waitcnt vmcnt(0)
	v_mov_b32_e32 v0, 0
	s_cmpk_gt_i32 s92, 0xff
	s_cbranch_scc1 .LBB7_705
	v_mbcnt_lo_u32_b32 v0, -1, v0
	v_mbcnt_hi_u32_b32 v80, -1, v0
	s_add_u32 s0, s30, 0xb80000
	v_lshlrev_b32_e32 v0, 10, v80
	s_addc_u32 s1, s31, 0
	v_and_b32_e32 v144, 0x3c00, v0
	v_ashrrev_i32_e32 v0, 1, v80
	s_add_u32 s4, s30, 0xb90000
	v_and_b32_e32 v0, -8, v0
	s_addc_u32 s5, s31, 0
	s_lshl_b32 s6, s94, 7
	s_mov_b32 s7, 0
	v_ashrrev_i32_e32 v1, 31, v0
	v_lshl_add_u64 v[48:49], v[0:1], 0, s[6:7]
	v_lshl_add_u64 v[0:1], v[48:49], 0, v[144:145]
	v_lshlrev_b64 v[0:1], 1, v[0:1]
	v_lshl_add_u64 v[8:9], s[0:1], 0, v[0:1]
	v_or_b32_e32 v56, 0x4000, v144
	v_mov_b32_e32 v57, v145
	v_lshl_add_u64 v[10:11], s[4:5], 0, v[0:1]
	global_load_dwordx4 v[0:3], v[8:9], off nt
	s_waitcnt lgkmcnt(0)
	global_load_dwordx4 v[4:7], v[10:11], off nt
	v_lshl_add_u64 v[8:9], v[48:49], 0, v[56:57]
	v_lshlrev_b64 v[8:9], 1, v[8:9]
	v_lshl_add_u64 v[16:17], s[0:1], 0, v[8:9]
	v_lshl_add_u64 v[24:25], v[48:49], 0, 32
	v_lshl_add_u64 v[18:19], s[4:5], 0, v[8:9]
	global_load_dwordx4 v[8:11], v[16:17], off nt
	global_load_dwordx4 v[12:15], v[18:19], off nt
	v_lshl_add_u64 v[16:17], v[24:25], 0, v[144:145]
	v_lshl_add_u64 v[24:25], v[24:25], 0, v[56:57]
	v_lshlrev_b64 v[16:17], 1, v[16:17]
	v_lshlrev_b64 v[24:25], 1, v[24:25]
	s_mov_b64 s[6:7], 0x60
	v_lshl_add_u64 v[26:27], s[0:1], 0, v[16:17]
	v_lshl_add_u64 v[28:29], s[4:5], 0, v[16:17]
	v_lshl_add_u64 v[32:33], s[0:1], 0, v[24:25]
	v_lshl_add_u64 v[40:41], v[48:49], 0, 64
	v_lshl_add_u64 v[58:59], v[48:49], 0, s[6:7]
	global_load_dwordx4 v[16:19], v[26:27], off nt
	global_load_dwordx4 v[20:23], v[28:29], off nt
	v_lshl_add_u64 v[34:35], s[4:5], 0, v[24:25]
	global_load_dwordx4 v[24:27], v[32:33], off nt
	global_load_dwordx4 v[28:31], v[34:35], off nt
	v_lshl_add_u64 v[32:33], v[40:41], 0, v[144:145]
	v_lshl_add_u64 v[40:41], v[40:41], 0, v[56:57]
	v_lshl_add_u64 v[48:49], v[58:59], 0, v[144:145]
	v_lshl_add_u64 v[56:57], v[58:59], 0, v[56:57]
	v_ashrrev_i32_e32 v81, 31, v80
	v_readlane_b32 s36, v254, 25
	v_lshlrev_b64 v[32:33], 1, v[32:33]
	v_lshlrev_b64 v[40:41], 1, v[40:41]
	v_lshlrev_b64 v[48:49], 1, v[48:49]
	v_lshlrev_b64 v[56:57], 1, v[56:57]
	v_lshlrev_b64 v[82:83], 4, v[80:81]
	v_readlane_b32 s50, v254, 39
	v_readlane_b32 s51, v254, 40
	v_lshl_add_u64 v[42:43], s[0:1], 0, v[32:33]
	v_lshl_add_u64 v[44:45], s[4:5], 0, v[32:33]
	v_lshl_add_u64 v[50:51], s[0:1], 0, v[40:41]
	v_lshl_add_u64 v[52:53], s[4:5], 0, v[40:41]
	v_lshl_add_u64 v[60:61], s[0:1], 0, v[48:49]
	v_lshl_add_u64 v[62:63], s[4:5], 0, v[48:49]
	v_lshl_add_u64 v[64:65], s[0:1], 0, v[56:57]
	v_lshl_add_u64 v[66:67], s[4:5], 0, v[56:57]
	v_lshl_add_u64 v[84:85], s[50:51], 0, v[82:83]
	global_load_dwordx4 v[32:35], v[42:43], off nt
	global_load_dwordx4 v[36:39], v[44:45], off nt
	s_nop 0
	global_load_dwordx4 v[40:43], v[50:51], off nt
	global_load_dwordx4 v[44:47], v[52:53], off nt
	s_nop 0
	global_load_dwordx4 v[48:51], v[60:61], off nt
	global_load_dwordx4 v[52:55], v[62:63], off nt
	global_load_dwordx4 v[56:59], v[64:65], off nt
	s_nop 0
	global_load_dwordx4 v[60:63], v[66:67], off nt
	s_nop 0
	global_load_dwordx4 v[64:67], v[84:85], off nt
	global_load_dwordx4 v[68:71], v[84:85], off offset:1024 nt
	global_load_dwordx4 v[72:75], v[84:85], off offset:2048 nt
	global_load_dwordx4 v[76:79], v[84:85], off offset:3072 nt
	v_and_b32_e32 v84, 31, v80
	v_lshlrev_b32_e32 v84, 2, v84
	global_load_dword v144, v84, s[18:19]
	v_readlane_b32 s0, v254, 5
	s_add_i32 s2, 0, 0x14200
	s_add_i32 s4, 0, 0x14280
	v_add_u32_e32 v146, s0, v80
	v_lshlrev_b32_e32 v84, 2, v146
	v_add_u32_e32 v196, s2, v84
	s_lshl_b32 s2, s94, 1
	s_add_u32 s14, s30, 0x2f000000
	s_mul_i32 s6, s94, 0x1020
	s_addc_u32 s15, s31, 0
	s_add_i32 s33, s6, 0
	s_lshl_b32 s34, s94, 8
	s_lshl_b32 s35, s94, 11
	s_add_u32 s16, s30, 0xc00000
	v_readlane_b32 s37, v254, 26
	v_readlane_b32 s38, v254, 27
	v_readlane_b32 s39, v254, 28
	v_readlane_b32 s40, v254, 29
	v_readlane_b32 s41, v254, 30
	v_readlane_b32 s42, v254, 31
	v_readlane_b32 s43, v254, 32
	v_readlane_b32 s44, v254, 33
	v_readlane_b32 s45, v254, 34
	v_readlane_b32 s46, v254, 35
	v_readlane_b32 s47, v254, 36
	v_readlane_b32 s48, v254, 37
	v_readlane_b32 s49, v254, 38
	s_addc_u32 s17, s31, 0
	s_add_u32 s18, s30, 0x1400000
	v_readlane_b32 s36, v254, 9
	s_addc_u32 s19, s31, 0
	v_readlane_b32 s37, v254, 10
	s_add_i32 s6, s34, 0
	v_add_u32_e32 v197, s4, v84
	v_ashrrev_i32_e32 v147, 31, v146
	s_movk_i32 s4, 0x400
	v_readlane_b32 s44, v254, 17
	v_readlane_b32 s45, v254, 18
	v_readlane_b32 s46, v254, 19
	v_readlane_b32 s47, v254, 20
	v_readlane_b32 s48, v254, 21
	v_readlane_b32 s49, v254, 22
	v_readlane_b32 s50, v254, 23
	v_readlane_b32 s51, v254, 24
	v_lshl_add_u64 v[150:151], s[36:37], 0, v[82:83]
	v_lshl_add_u32 v82, v80, 2, s6
	s_mov_b32 s13, 1
	v_cmp_gt_i32_e64 s[0:1], 32, v146
	v_lshl_add_u64 v[148:149], v[146:147], 2, s[30:31]
	v_cmp_gt_i32_e64 s[4:5], s4, v146
	v_lshl_add_u64 v[152:153], v[80:81], 3, s[28:29]
	s_lshl_b32 s44, s92, 8
	s_lshl_b32 s45, s3, 8
	v_add_u32_e32 v147, 0x15300, v82
	s_lshl_b32 s46, s92, 10
	s_lshl_b32 s47, s3, 10
	v_lshlrev_b64 v[154:155], 3, v[80:81]
	v_mov_b32_e32 v198, 0x358637bd
	s_mov_b32 s48, 0x800000
	s_add_i32 s49, 0, 0x10200
	v_mov_b32_e32 v199, 1
	s_movk_i32 s50, 0x1ff
	v_mov_b32_e32 v200, 0xff800000
	s_mov_b32 s51, s92
	v_readlane_b32 s38, v254, 11
	v_readlane_b32 s39, v254, 12
	v_readlane_b32 s40, v254, 13
	v_readlane_b32 s41, v254, 14
	v_readlane_b32 s42, v254, 15
	v_readlane_b32 s43, v254, 16
	s_branch .LBB7_690

; __device__ __forceinline__ void r_load(const P& p, RRows& r, int tok0, int lane) {
; #pragma unroll
;     for (int rr = 0; rr < 2; ++rr) { const f32x4* xr = (const f32x4*)(p.x + (size_t)(tok0 + rr) * DM); const u32x2* orow = (const u32x2*)((const bf16_t*)p.out + (size_t)(tok0 + rr) * 2048);
; #pragma unroll
;         for (int j = 0; j < 4; ++j) { r.x[rr][j] = xr[lane + 64 * j]; r.o[rr][j] = orow[lane + 64 * j]; } }
; }
; __device__ __forceinline__ void ph4(const Ctx& c) {
;     ...
;     for (int ch = c.bx; ch < T / 256; ch += c.G) {
;         const int t0 = ch * 256;
;         if (tid < NE) lhist[tid] = 0;
;         RRows ra, rb; r_load(p, ra, t0 + 2 * wave, lane);
.LBB7_690:
	s_and_saveexec_b64 s[6:7], s[0:1]
	ds_write_b32 v196, v145
	s_or_b64 exec, exec, s[6:7]
	s_lshl_b32 s6, s51, 8
	s_add_i32 s6, s6, s2
	s_ashr_i32 s7, s6, 31
	s_lshl_b64 s[8:9], s[6:7], 12
	s_or_b32 s6, s6, 1
	s_ashr_i32 s7, s6, 31
	s_lshl_b64 s[6:7], s[6:7], 12
	s_waitcnt vmcnt(23)
	v_lshl_add_u64 v[96:97], v[150:151], 0, s[8:9]
	v_lshl_add_u64 v[98:99], v[152:153], 0, s[8:9]
	s_waitcnt vmcnt(20)
	v_lshl_add_u64 v[108:109], v[150:151], 0, s[6:7]
	global_load_dwordx4 v[80:83], v[96:97], off nt
	global_load_dwordx4 v[84:87], v[96:97], off offset:1024 nt
	global_load_dwordx4 v[88:91], v[96:97], off offset:2048 nt
	global_load_dwordx4 v[92:95], v[96:97], off offset:3072 nt
	global_load_dwordx2 v[156:157], v[98:99], off nt
	global_load_dwordx2 v[158:159], v[98:99], off offset:512 nt
	global_load_dwordx2 v[160:161], v[98:99], off offset:1024 nt
	global_load_dwordx2 v[162:163], v[98:99], off offset:1536 nt
	v_lshl_add_u64 v[112:113], v[152:153], 0, s[6:7]
	global_load_dwordx4 v[96:99], v[108:109], off nt
	global_load_dwordx4 v[100:103], v[108:109], off offset:1024 nt
	global_load_dwordx4 v[104:107], v[108:109], off offset:2048 nt
	s_nop 0
	global_load_dwordx4 v[108:111], v[108:109], off offset:3072 nt
	s_nop 0
	global_load_dwordx2 v[164:165], v[112:113], off nt
	global_load_dwordx2 v[166:167], v[112:113], off offset:512 nt
	global_load_dwordx2 v[168:169], v[112:113], off offset:1024 nt
	global_load_dwordx2 v[170:171], v[112:113], off offset:1536 nt
	s_mov_b32 s52, 0
	s_mov_b32 s53, s2
	s_branch .LBB7_694

; __device__ __forceinline__ unsigned cvt_pk_bf16(float lo, float hi) { unsigned r; asm volatile("v_cvt_pk_bf16_f32 %0, %1, %2" : "=v"(r) : "v"(lo), "v"(hi)); return r; }
; __device__ __forceinline__ void r_tile(const Ctx& c, const RRows& r, int tokw  , int slot0  , const f32x4 (&gq)[4], const bf16x8 (&bh)[4][2], const bf16x8 (&bl)[4][2], float bias) {
;     ...
;     for (int rr = 0; rr < 2; ++rr) { f32x4 h[4]; float s = 0.f;
; #pragma unroll
;         for (int j = 0; j < 4; ++j) { const u32x2 w = r.o[rr][j]; h[j] = r.x[rr][j] + (f32x4){__uint_as_float(w.x << 16), __uint_as_float(w.x & 0xffff0000u), __uint_as_float(w.y << 16), __uint_as_float(w.y & 0xffff0000u)};
;             s += (h[j][0] * h[j][0] + h[j][1] * h[j][1]) + (h[j][2] * h[j][2] + h[j][3] * h[j][3]); }
;         s = allsum64(s);
;         const float rs = rsqrtf(s * (1.0f / DM) + EPS);
; #pragma unroll
;         for (int j = 0; j < 4; ++j) { u32x2 hb; hb.x = pg8::cvt_pk_bf16(h[j][0], h[j][1]); hb.y = pg8::cvt_pk_bf16(h[j][2], h[j][3]); ((u32x2*)((bf16_t*)p.out + (size_t)(tokw + rr) * 2048))[lane + 64 * j] = hb; }
; #pragma unroll
; __device__ __forceinline__ void ph4(const Ctx& c) {
;     ...
;             r_load(p, rb, t0 + 16 * (tile + 1) + 2 * wave, lane);
.LBB7_694:
	s_waitcnt vmcnt(11)
	v_lshlrev_b32_e32 v188, 16, v156
	v_and_b32_e32 v189, 0xffff0000, v156
	v_lshlrev_b32_e32 v190, 16, v157
	v_and_b32_e32 v191, 0xffff0000, v157
	v_pk_add_f32 v[192:193], v[82:83], v[190:191]
	v_pk_add_f32 v[194:195], v[80:81], v[188:189]
	v_mul_f32_e32 v189, v193, v193
	v_mul_f32_e32 v188, v195, v195
	v_fmac_f32_e32 v188, v194, v194
	v_fmac_f32_e32 v189, v192, v192
	v_add_f32_e32 v206, v188, v189
	s_waitcnt vmcnt(10)
	v_lshlrev_b32_e32 v188, 16, v158
	v_and_b32_e32 v189, 0xffff0000, v158
	v_lshlrev_b32_e32 v190, 16, v159
	v_and_b32_e32 v191, 0xffff0000, v159
	v_pk_add_f32 v[202:203], v[86:87], v[190:191]
	v_pk_add_f32 v[204:205], v[84:85], v[188:189]
	v_mul_f32_e32 v189, v203, v203
	v_mul_f32_e32 v188, v205, v205
	v_fmac_f32_e32 v188, v204, v204
	v_fmac_f32_e32 v189, v202, v202
	v_add_f32_e32 v188, v188, v189
	v_add_f32_e32 v210, v188, v206
	s_waitcnt vmcnt(9)
	v_lshlrev_b32_e32 v188, 16, v160
	v_and_b32_e32 v189, 0xffff0000, v160
	v_lshlrev_b32_e32 v190, 16, v161
	v_and_b32_e32 v191, 0xffff0000, v161
	v_pk_add_f32 v[206:207], v[90:91], v[190:191]
	v_pk_add_f32 v[208:209], v[88:89], v[188:189]
	v_mul_f32_e32 v189, v207, v207
	v_mul_f32_e32 v188, v209, v209
	v_fmac_f32_e32 v188, v208, v208
	v_fmac_f32_e32 v189, v206, v206
	v_add_f32_e32 v188, v188, v189
	v_add_f32_e32 v214, v188, v210
	s_waitcnt vmcnt(8)
	v_lshlrev_b32_e32 v188, 16, v162
	v_and_b32_e32 v189, 0xffff0000, v162
	v_lshlrev_b32_e32 v190, 16, v163
	v_and_b32_e32 v191, 0xffff0000, v163
	v_pk_add_f32 v[210:211], v[94:95], v[190:191]
	v_pk_add_f32 v[212:213], v[92:93], v[188:189]
	v_mul_f32_e32 v189, v211, v211
	v_mul_f32_e32 v188, v213, v213
	v_fmac_f32_e32 v188, v212, v212
	v_fmac_f32_e32 v189, v210, v210
	v_add_f32_e32 v188, v188, v189
	v_add_f32_e32 v188, v188, v214
	s_add_i32 s40, s44, s53
	s_add_i32 s36, s40, 16
	v_add_f32_dpp v188, v188, v188 quad_perm:[1,0,3,2] row_mask:0xf bank_mask:0xf bound_ctrl:1
	s_ashr_i32 s37, s36, 31
	s_lshl_b64 s[6:7], s[36:37], 12
	v_add_f32_dpp v188, v188, v188 quad_perm:[2,3,0,1] row_mask:0xf bank_mask:0xf bound_ctrl:1
	s_add_u32 s38, s28, s6
	s_addc_u32 s39, s29, s7
	v_add_f32_dpp v188, v188, v188 row_half_mirror row_mask:0xf bank_mask:0xf bound_ctrl:1
	s_add_i32 s20, s40, 17
	s_ashr_i32 s21, s20, 31
	v_add_f32_dpp v188, v188, v188 row_mirror row_mask:0xf bank_mask:0xf bound_ctrl:1
	v_mov_b32_e32 v189, v188
	s_nop 1
	v_permlane16_swap_b32_e32 v188, v189
	v_add_f32_e32 v188, v188, v189
	v_mov_b32_e32 v189, v188
	s_nop 1
	v_permlane32_swap_b32_e32 v188, v189
	v_lshl_add_u64 v[112:113], v[150:151], 0, s[6:7]
	s_lshl_b64 s[6:7], s[20:21], 12
	v_add_f32_e32 v188, v188, v189
	s_add_u32 s24, s28, s6
	v_fmamk_f32 v188, v188, 0x3a800000, v198
	s_addc_u32 s25, s29, s7
	v_mul_f32_e32 v189, 0x4b800000, v188
	v_cmp_gt_f32_e32 vcc, s48, v188
	v_lshl_add_u64 v[114:115], s[38:39], 0, v[154:155]
	global_load_dwordx4 v[140:143], v[112:113], off nt
	global_load_dwordx4 v[136:139], v[112:113], off offset:1024 nt
	global_load_dwordx4 v[132:135], v[112:113], off offset:2048 nt
	global_load_dwordx4 v[128:131], v[112:113], off offset:3072 nt
	global_load_dwordx2 v[186:187], v[114:115], off nt
	global_load_dwordx2 v[184:185], v[114:115], off offset:512 nt
	global_load_dwordx2 v[182:183], v[114:115], off offset:1024 nt
	global_load_dwordx2 v[180:181], v[114:115], off offset:1536 nt
	v_lshl_add_u64 v[112:113], v[150:151], 0, s[6:7]
	v_lshl_add_u64 v[172:173], s[24:25], 0, v[154:155]
	v_mov_b32_e32 v201, 0
	v_cndmask_b32_e32 v188, v188, v189, vcc
	global_load_dwordx4 v[124:127], v[112:113], off nt
	global_load_dwordx4 v[120:123], v[112:113], off offset:1024 nt
	global_load_dwordx4 v[116:119], v[112:113], off offset:2048 nt
	s_nop 0
	global_load_dwordx4 v[112:115], v[112:113], off offset:3072 nt
	s_nop 0
	global_load_dwordx2 v[178:179], v[172:173], off nt
	global_load_dwordx2 v[176:177], v[172:173], off offset:512 nt
	global_load_dwordx2 v[174:175], v[172:173], off offset:1024 nt
	s_nop 0
	global_load_dwordx2 v[172:173], v[172:173], off offset:1536 nt
	v_rsq_f32_e32 v218, v188
	s_ashr_i32 s41, s40, 31
	v_mbcnt_lo_u32_b32 v188, -1, v201
	v_mbcnt_hi_u32_b32 v188, -1, v188
	s_lshl_b64 s[6:7], s[40:41], 12
	s_add_u32 s6, s28, s6
	v_ashrrev_i32_e32 v189, 31, v188
	s_addc_u32 s7, s29, s7
	v_lshlrev_b64 v[190:191], 3, v[188:189]
	v_cvt_pk_bf16_f32 v214, v194, v195
	v_lshl_add_u64 v[216:217], s[6:7], 0, v[190:191]
	v_cvt_pk_bf16_f32 v215, v192, v193
	global_store_dwordx2 v[216:217], v[214:215], off
	v_cvt_pk_bf16_f32 v214, v204, v205
	v_cvt_pk_bf16_f32 v215, v202, v203
	global_store_dwordx2 v[216:217], v[214:215], off offset:512
	v_cvt_pk_bf16_f32 v214, v208, v209
	v_mul_f32_e32 v201, 0x45800000, v218
	v_cvt_pk_bf16_f32 v215, v206, v207
	global_store_dwordx2 v[216:217], v[214:215], off offset:1024
	v_cvt_pk_bf16_f32 v214, v212, v213
	v_cvt_pk_bf16_f32 v215, v210, v211
	global_store_dwordx2 v[216:217], v[214:215], off offset:1536
	v_cndmask_b32_e32 v214, v218, v201, vcc
	v_pk_mul_f32 v[194:195], v[194:195], v[214:215] op_sel_hi:[1,0]
	v_pk_mul_f32 v[192:193], v[192:193], v[214:215] op_sel_hi:[1,0]
	v_pk_mul_f32 v[218:219], v[64:65], v[194:195]
	v_pk_mul_f32 v[216:217], v[66:67], v[192:193]
	v_cvt_pk_bf16_f32 v220, v218, v219
	s_lshl_b64 s[6:7], s[40:41], 10
	v_cvt_pk_bf16_f32 v221, v216, v217
	v_lshlrev_b32_e32 v201, 16, v220
	v_lshlrev_b32_e32 v222, 16, v221
	v_and_b32_e32 v223, 0xffff0000, v221
	v_and_b32_e32 v215, 0xffff0000, v220
	v_xor_b32_e32 v223, 0x80000000, v223
	v_xor_b32_e32 v222, 0x80000000, v222
	v_pk_fma_f32 v[192:193], v[66:67], v[192:193], v[222:223]
	v_xor_b32_e32 v223, 0x80000000, v215
	v_xor_b32_e32 v222, 0x80000000, v201
; #define LAS __attribute__((address_space(3)))
; __device__ __forceinline__ unsigned cvt_pk_bf16(float lo, float hi) { unsigned r; asm volatile("v_cvt_pk_bf16_f32 %0, %1, %2" : "=v"(r) : "v"(lo), "v"(hi)); return r; }
; __device__ __forceinline__ void r_tile(const Ctx& c, const RRows& r, int tokw  , int slot0  , const f32x4 (&gq)[4], const bf16x8 (&bh)[4][2], const bf16x8 (&bl)[4][2], float bias) {
;     ...
;         for (int j = 0; j < 4; ++j) { u32x2 hb; hb.x = pg8::cvt_pk_bf16(h[j][0], h[j][1]); hb.y = pg8::cvt_pk_bf16(h[j][2], h[j][3]); ((u32x2*)((bf16_t*)p.out + (size_t)(tokw + rr) * 2048))[lane + 64 * j] = hb; }
; #pragma unroll
;         for (int j = 0; j < 4; ++j) { const f32x4 v = h[j] * rs * gq[j]; u32x2 wh, wl; wh.x = pg8::cvt_pk_bf16(v[0], v[1]); wh.y = pg8::cvt_pk_bf16(v[2], v[3]);
;             const f32x4 d = v - (f32x4){__uint_as_float(wh.x << 16), __uint_as_float(wh.x & 0xffff0000u), __uint_as_float(wh.y << 16), __uint_as_float(wh.y & 0xffff0000u)};
;             wl.x = pg8::cvt_pk_bf16(d[0], d[1]); wl.y = pg8::cvt_pk_bf16(d[2], d[3]);
;             ((unsigned*)(V + (size_t)(tokw + rr) * DM))[lane + 64 * j] = pg8::pk4_fp8(8.0f * v[0], 8.0f * v[1], 8.0f * v[2], 8.0f * v[3]);
;             *(LAS u32x2*)(L + R_AH + (2 * wave + rr) * R_AP + (lane + 64 * j) * 8) = wh; *(LAS u32x2*)(L + R_AL + (2 * wave + rr) * R_AP + (lane + 64 * j) * 8) = wl; } }
	v_pk_fma_f32 v[194:195], v[64:65], v[194:195], v[222:223]
	v_mul_f32_e32 v215, 0x41000000, v218
	v_mul_f32_e32 v218, 0x41000000, v219
	s_add_u32 s6, s14, s6
	v_mov_b32_e32 v222, v201
	v_cvt_pk_fp8_f32 v222, v215, v218
	v_cvt_pk_bf16_f32 v218, v194, v195
	v_mul_f32_e32 v194, 0x41000000, v216
	v_mul_f32_e32 v195, 0x41000000, v217
	v_cvt_pk_fp8_f32 v222, v194, v195 op_sel:[0,0,1]
	s_addc_u32 s7, s15, s7
	v_cvt_pk_bf16_f32 v219, v192, v193
	v_lshlrev_b64 v[192:193], 2, v[188:189]
	v_lshl_add_u64 v[194:195], s[6:7], 0, v[192:193]
	v_lshl_add_u32 v189, v188, 3, s33
	v_pk_mul_f32 v[204:205], v[204:205], v[214:215] op_sel_hi:[1,0]
	v_pk_mul_f32 v[202:203], v[202:203], v[214:215] op_sel_hi:[1,0]
	global_store_dword v[194:195], v222, off
	ds_write_b64 v189, v[220:221]
	ds_write_b64 v189, v[218:219] offset:33024
	v_pk_mul_f32 v[216:217], v[70:71], v[202:203]
	v_pk_mul_f32 v[218:219], v[68:69], v[204:205]
	s_add_i32 s6, s40, 1
	v_cvt_pk_bf16_f32 v220, v218, v219
	v_cvt_pk_bf16_f32 v221, v216, v217
	v_mul_f32_e32 v218, 0x41000000, v218
	v_lshlrev_b32_e32 v222, 16, v221
	v_and_b32_e32 v223, 0xffff0000, v221
	v_and_b32_e32 v224, 0xffff0000, v220
	v_xor_b32_e32 v223, 0x80000000, v223
	v_xor_b32_e32 v222, 0x80000000, v222
	v_pk_fma_f32 v[202:203], v[70:71], v[202:203], v[222:223]
	v_xor_b32_e32 v223, 0x80000000, v224
	v_mul_f32_e32 v219, 0x41000000, v219
	v_mov_b32_e32 v224, v201
	v_cvt_pk_fp8_f32 v224, v218, v219
	v_lshlrev_b32_e32 v215, 16, v220
	v_xor_b32_e32 v222, 0x80000000, v215
	v_mul_f32_e32 v215, 0x41000000, v216
	v_mul_f32_e32 v216, 0x41000000, v217
	v_cvt_pk_fp8_f32 v224, v215, v216 op_sel:[0,0,1]
	v_pk_fma_f32 v[204:205], v[68:69], v[204:205], v[222:223]
	v_mov_b32_e32 v222, v201
	v_cvt_pk_bf16_f32 v204, v204, v205
	v_cvt_pk_bf16_f32 v205, v202, v203
	global_store_dword v[194:195], v224, off offset:256
	ds_write_b64 v189, v[220:221] offset:512
	ds_write_b64 v189, v[204:205] offset:33536
	v_pk_mul_f32 v[202:203], v[208:209], v[214:215] op_sel_hi:[1,0]
	v_pk_mul_f32 v[204:205], v[206:207], v[214:215] op_sel_hi:[1,0]
	v_pk_mul_f32 v[208:209], v[72:73], v[202:203]
	v_pk_mul_f32 v[206:207], v[74:75], v[204:205]
	v_cvt_pk_bf16_f32 v216, v208, v209
	v_mul_f32_e32 v208, 0x41000000, v208
	v_cvt_pk_bf16_f32 v217, v206, v207
	v_and_b32_e32 v220, 0xffff0000, v216
	v_lshlrev_b32_e32 v218, 16, v217
	v_and_b32_e32 v219, 0xffff0000, v217
	v_xor_b32_e32 v219, 0x80000000, v219
	v_xor_b32_e32 v218, 0x80000000, v218
	v_pk_fma_f32 v[204:205], v[74:75], v[204:205], v[218:219]
	v_xor_b32_e32 v219, 0x80000000, v220
	v_mul_f32_e32 v209, 0x41000000, v209
	v_mov_b32_e32 v220, v201
	v_cvt_pk_fp8_f32 v220, v208, v209
	v_mul_f32_e32 v206, 0x41000000, v206
	v_mul_f32_e32 v207, 0x41000000, v207
	v_lshlrev_b32_e32 v215, 16, v216
	v_cvt_pk_fp8_f32 v220, v206, v207 op_sel:[0,0,1]
	v_xor_b32_e32 v218, 0x80000000, v215
	v_pk_fma_f32 v[202:203], v[72:73], v[202:203], v[218:219]
	s_waitcnt vmcnt(22)
	v_and_b32_e32 v221, 0xffff0000, v171
	v_cvt_pk_bf16_f32 v202, v202, v203
	v_cvt_pk_bf16_f32 v203, v204, v205
	global_store_dword v[194:195], v220, off offset:512
	ds_write_b64 v189, v[216:217] offset:1024
	ds_write_b64 v189, v[202:203] offset:34048
	v_pk_mul_f32 v[202:203], v[212:213], v[214:215] op_sel_hi:[1,0]
	v_pk_mul_f32 v[204:205], v[210:211], v[214:215] op_sel_hi:[1,0]
	v_pk_mul_f32 v[208:209], v[76:77], v[202:203]
	v_pk_mul_f32 v[206:207], v[78:79], v[204:205]
	v_cvt_pk_bf16_f32 v210, v208, v209
	v_and_b32_e32 v217, 0xffff0000, v169
	v_cvt_pk_bf16_f32 v211, v206, v207
	v_lshlrev_b32_e32 v214, 16, v210
	v_lshlrev_b32_e32 v212, 16, v211
	v_and_b32_e32 v213, 0xffff0000, v211
	v_and_b32_e32 v215, 0xffff0000, v210
	v_xor_b32_e32 v213, 0x80000000, v213
	v_xor_b32_e32 v212, 0x80000000, v212
	v_pk_fma_f32 v[204:205], v[78:79], v[204:205], v[212:213]
	v_xor_b32_e32 v213, 0x80000000, v215
	v_xor_b32_e32 v212, 0x80000000, v214
	v_pk_fma_f32 v[202:203], v[76:77], v[202:203], v[212:213]
	v_lshlrev_b32_e32 v212, 16, v167
	v_cvt_pk_bf16_f32 v202, v202, v203
	v_mul_f32_e32 v203, 0x41000000, v208
	v_mul_f32_e32 v208, 0x41000000, v209
	v_cvt_pk_fp8_f32 v222, v203, v208
	v_cvt_pk_bf16_f32 v203, v204, v205
	v_mul_f32_e32 v204, 0x41000000, v206
	v_mul_f32_e32 v205, 0x41000000, v207
	v_cvt_pk_fp8_f32 v222, v204, v205 op_sel:[0,0,1]
	v_lshlrev_b32_e32 v204, 16, v164
	v_and_b32_e32 v205, 0xffff0000, v164
	v_lshlrev_b32_e32 v206, 16, v165
	v_and_b32_e32 v207, 0xffff0000, v165
	v_pk_add_f32 v[206:207], v[98:99], v[206:207]
	v_pk_add_f32 v[204:205], v[96:97], v[204:205]
	v_mul_f32_e32 v209, v207, v207
	v_mul_f32_e32 v208, v205, v205
	v_fmac_f32_e32 v208, v204, v204
	v_fmac_f32_e32 v209, v206, v206
	v_add_f32_e32 v214, v208, v209
	v_lshlrev_b32_e32 v208, 16, v166
	v_and_b32_e32 v209, 0xffff0000, v166
	v_and_b32_e32 v213, 0xffff0000, v167
	v_pk_add_f32 v[212:213], v[102:103], v[212:213]
	v_pk_add_f32 v[208:209], v[100:101], v[208:209]
	v_mul_f32_e32 v216, v213, v213
	v_mul_f32_e32 v215, v209, v209
	v_fmac_f32_e32 v215, v208, v208
	v_fmac_f32_e32 v216, v212, v212
	v_add_f32_e32 v215, v215, v216
	v_add_f32_e32 v218, v215, v214
	v_lshlrev_b32_e32 v214, 16, v168
	v_and_b32_e32 v215, 0xffff0000, v168
	v_lshlrev_b32_e32 v216, 16, v169
	v_pk_add_f32 v[216:217], v[106:107], v[216:217]
	v_pk_add_f32 v[214:215], v[104:105], v[214:215]
	v_mul_f32_e32 v220, v217, v217
	v_mul_f32_e32 v219, v215, v215
	v_fmac_f32_e32 v219, v214, v214
	v_fmac_f32_e32 v220, v216, v216
	v_add_f32_e32 v219, v219, v220
	v_add_f32_e32 v223, v219, v218
	v_lshlrev_b32_e32 v218, 16, v170
	v_and_b32_e32 v219, 0xffff0000, v170
	v_lshlrev_b32_e32 v220, 16, v171
	v_pk_add_f32 v[220:221], v[110:111], v[220:221]
	v_pk_add_f32 v[218:219], v[108:109], v[218:219]
; #define LAS __attribute__((address_space(3)))
; __device__ __forceinline__ unsigned cvt_pk_bf16(float lo, float hi) { unsigned r; asm volatile("v_cvt_pk_bf16_f32 %0, %1, %2" : "=v"(r) : "v"(lo), "v"(hi)); return r; }
; __device__ __forceinline__ void r_tile(const Ctx& c, const RRows& r, int tokw  , int slot0  , const f32x4 (&gq)[4], const bf16x8 (&bh)[4][2], const bf16x8 (&bl)[4][2], float bias) {
;     ...
;     for (int rr = 0; rr < 2; ++rr) { f32x4 h[4]; float s = 0.f;
; #pragma unroll
;         for (int j = 0; j < 4; ++j) { const u32x2 w = r.o[rr][j]; h[j] = r.x[rr][j] + (f32x4){__uint_as_float(w.x << 16), __uint_as_float(w.x & 0xffff0000u), __uint_as_float(w.y << 16), __uint_as_float(w.y & 0xffff0000u)};
;             s += (h[j][0] * h[j][0] + h[j][1] * h[j][1]) + (h[j][2] * h[j][2] + h[j][3] * h[j][3]); }
;         s = allsum64(s);
;         const float rs = rsqrtf(s * (1.0f / DM) + EPS);
; #pragma unroll
;         for (int j = 0; j < 4; ++j) { u32x2 hb; hb.x = pg8::cvt_pk_bf16(h[j][0], h[j][1]); hb.y = pg8::cvt_pk_bf16(h[j][2], h[j][3]); ((u32x2*)((bf16_t*)p.out + (size_t)(tokw + rr) * 2048))[lane + 64 * j] = hb; }
; #pragma unroll
;         for (int j = 0; j < 4; ++j) { const f32x4 v = h[j] * rs * gq[j]; u32x2 wh, wl; wh.x = pg8::cvt_pk_bf16(v[0], v[1]); wh.y = pg8::cvt_pk_bf16(v[2], v[3]);
;             const f32x4 d = v - (f32x4){__uint_as_float(wh.x << 16), __uint_as_float(wh.x & 0xffff0000u), __uint_as_float(wh.y << 16), __uint_as_float(wh.y & 0xffff0000u)};
;             wl.x = pg8::cvt_pk_bf16(d[0], d[1]); wl.y = pg8::cvt_pk_bf16(d[2], d[3]);
;             ((unsigned*)(V + (size_t)(tokw + rr) * DM))[lane + 64 * j] = pg8::pk4_fp8(8.0f * v[0], 8.0f * v[1], 8.0f * v[2], 8.0f * v[3]);
;             *(LAS u32x2*)(L + R_AH + (2 * wave + rr) * R_AP + (lane + 64 * j) * 8) = wh; *(LAS u32x2*)(L + R_AL + (2 * wave + rr) * R_AP + (lane + 64 * j) * 8) = wl; } }
;     __syncthreads();
	v_mul_f32_e32 v225, v221, v221
	v_mul_f32_e32 v224, v219, v219
	v_fmac_f32_e32 v224, v218, v218
	v_fmac_f32_e32 v225, v220, v220
	v_add_f32_e32 v224, v224, v225
	v_add_f32_e32 v223, v224, v223
	s_ashr_i32 s7, s6, 31
	s_lshl_b64 s[8:9], s[6:7], 12
	v_add_f32_dpp v223, v223, v223 quad_perm:[1,0,3,2] row_mask:0xf bank_mask:0xf bound_ctrl:1
	s_add_u32 s8, s28, s8
	s_addc_u32 s9, s29, s9
	v_add_f32_dpp v223, v223, v223 quad_perm:[2,3,0,1] row_mask:0xf bank_mask:0xf bound_ctrl:1
	global_store_dword v[194:195], v222, off offset:768
	ds_write_b64 v189, v[210:211] offset:1536
	ds_write_b64 v189, v[202:203] offset:34560
	v_add_f32_dpp v223, v223, v223 row_half_mirror row_mask:0xf bank_mask:0xf bound_ctrl:1
	v_cvt_pk_bf16_f32 v194, v204, v205
	v_cvt_pk_bf16_f32 v195, v206, v207
	v_lshl_add_u64 v[190:191], s[8:9], 0, v[190:191]
	global_store_dwordx2 v[190:191], v[194:195], off
	v_add_f32_dpp v223, v223, v223 row_mirror row_mask:0xf bank_mask:0xf bound_ctrl:1
	v_mov_b32_e32 v224, v223
	s_nop 1
	v_permlane16_swap_b32_e32 v223, v224
	v_add_f32_e32 v223, v223, v224
	v_mov_b32_e32 v224, v223
	s_nop 1
	v_permlane32_swap_b32_e32 v223, v224
	v_add_f32_e32 v223, v223, v224
	v_fmamk_f32 v223, v223, 0x3a800000, v198
	v_mul_f32_e32 v224, 0x4b800000, v223
	v_cmp_gt_f32_e32 vcc, s48, v223
	v_cvt_pk_bf16_f32 v194, v208, v209
	v_cvt_pk_bf16_f32 v195, v212, v213
	global_store_dwordx2 v[190:191], v[194:195], off offset:512
	v_cvt_pk_bf16_f32 v194, v214, v215
	v_cvt_pk_bf16_f32 v195, v216, v217
	s_nop 0
	v_cndmask_b32_e32 v223, v223, v224, vcc
	v_rsq_f32_e32 v223, v223
	global_store_dwordx2 v[190:191], v[194:195], off offset:1024
	v_cvt_pk_bf16_f32 v194, v218, v219
	v_cvt_pk_bf16_f32 v195, v220, v221
	v_mul_f32_e32 v202, 0x45800000, v223
	global_store_dwordx2 v[190:191], v[194:195], off offset:1536
	v_cndmask_b32_e32 v190, v223, v202, vcc
	v_pk_mul_f32 v[194:195], v[204:205], v[190:191] op_sel_hi:[1,0]
	v_pk_mul_f32 v[202:203], v[206:207], v[190:191] op_sel_hi:[1,0]
	v_pk_mul_f32 v[206:207], v[64:65], v[194:195]
	v_pk_mul_f32 v[204:205], v[66:67], v[202:203]
	v_cvt_pk_bf16_f32 v210, v206, v207
	s_lshl_b64 s[6:7], s[6:7], 10
	v_cvt_pk_bf16_f32 v211, v204, v205
	v_lshlrev_b32_e32 v191, 16, v210
	v_lshlrev_b32_e32 v222, 16, v211
	v_and_b32_e32 v223, 0xffff0000, v211
	v_xor_b32_e32 v223, 0x80000000, v223
	v_xor_b32_e32 v222, 0x80000000, v222
	v_pk_fma_f32 v[202:203], v[66:67], v[202:203], v[222:223]
	v_xor_b32_e32 v222, 0x80000000, v191
	v_mul_f32_e32 v191, 0x41000000, v206
	v_mul_f32_e32 v206, 0x41000000, v207
	v_mov_b32_e32 v207, v201
	v_cvt_pk_fp8_f32 v207, v191, v206
	v_mul_f32_e32 v191, 0x41000000, v204
	v_mul_f32_e32 v204, 0x41000000, v205
	v_and_b32_e32 v224, 0xffff0000, v210
	v_cvt_pk_fp8_f32 v207, v191, v204 op_sel:[0,0,1]
	s_add_u32 s6, s14, s6
	v_xor_b32_e32 v223, 0x80000000, v224
	s_addc_u32 s7, s15, s7
	v_pk_fma_f32 v[194:195], v[64:65], v[194:195], v[222:223]
	v_lshl_add_u64 v[192:193], s[6:7], 0, v[192:193]
	v_cvt_pk_bf16_f32 v194, v194, v195
	v_cvt_pk_bf16_f32 v195, v202, v203
	global_store_dword v[192:193], v207, off
	ds_write_b64 v189, v[210:211] offset:2064
	ds_write_b64 v189, v[194:195] offset:35088
	v_pk_mul_f32 v[194:195], v[208:209], v[190:191] op_sel_hi:[1,0]
	v_pk_mul_f32 v[202:203], v[212:213], v[190:191] op_sel_hi:[1,0]
	v_pk_mul_f32 v[206:207], v[68:69], v[194:195]
	v_pk_mul_f32 v[204:205], v[70:71], v[202:203]
	v_cvt_pk_bf16_f32 v208, v206, v207
	v_mul_f32_e32 v206, 0x41000000, v206
	v_cvt_pk_bf16_f32 v209, v204, v205
	v_and_b32_e32 v212, 0xffff0000, v208
	v_lshlrev_b32_e32 v210, 16, v209
	v_and_b32_e32 v211, 0xffff0000, v209
	v_xor_b32_e32 v211, 0x80000000, v211
	v_xor_b32_e32 v210, 0x80000000, v210
	v_pk_fma_f32 v[202:203], v[70:71], v[202:203], v[210:211]
	v_xor_b32_e32 v211, 0x80000000, v212
	v_mul_f32_e32 v207, 0x41000000, v207
	v_mov_b32_e32 v212, v201
	v_cvt_pk_fp8_f32 v212, v206, v207
	v_lshlrev_b32_e32 v191, 16, v208
	v_xor_b32_e32 v210, 0x80000000, v191
	v_mul_f32_e32 v191, 0x41000000, v204
	v_mul_f32_e32 v204, 0x41000000, v205
	v_cvt_pk_fp8_f32 v212, v191, v204 op_sel:[0,0,1]
	v_pk_fma_f32 v[194:195], v[68:69], v[194:195], v[210:211]
	v_cmp_gt_u32_e32 vcc, 32, v188
	v_cvt_pk_bf16_f32 v194, v194, v195
	v_cvt_pk_bf16_f32 v195, v202, v203
	global_store_dword v[192:193], v212, off offset:256
	ds_write_b64 v189, v[208:209] offset:2576
	ds_write_b64 v189, v[194:195] offset:35600
	v_pk_mul_f32 v[194:195], v[214:215], v[190:191] op_sel_hi:[1,0]
	v_pk_mul_f32 v[202:203], v[216:217], v[190:191] op_sel_hi:[1,0]
	v_pk_mul_f32 v[206:207], v[72:73], v[194:195]
	v_pk_mul_f32 v[204:205], v[74:75], v[202:203]
	v_cvt_pk_bf16_f32 v208, v206, v207
	v_mul_f32_e32 v206, 0x41000000, v206
	v_cvt_pk_bf16_f32 v209, v204, v205
	v_and_b32_e32 v212, 0xffff0000, v208
	v_lshlrev_b32_e32 v210, 16, v209
	v_and_b32_e32 v211, 0xffff0000, v209
	v_xor_b32_e32 v211, 0x80000000, v211
	v_xor_b32_e32 v210, 0x80000000, v210
	v_pk_fma_f32 v[202:203], v[74:75], v[202:203], v[210:211]
	v_xor_b32_e32 v211, 0x80000000, v212
	v_mul_f32_e32 v207, 0x41000000, v207
	v_mov_b32_e32 v212, v201
	v_cvt_pk_fp8_f32 v212, v206, v207
	v_lshlrev_b32_e32 v191, 16, v208
	v_xor_b32_e32 v210, 0x80000000, v191
	v_mul_f32_e32 v191, 0x41000000, v204
	v_mul_f32_e32 v204, 0x41000000, v205
	v_cvt_pk_fp8_f32 v212, v191, v204 op_sel:[0,0,1]
	v_pk_fma_f32 v[194:195], v[72:73], v[194:195], v[210:211]
	s_nop 0
	v_cvt_pk_bf16_f32 v194, v194, v195
	v_cvt_pk_bf16_f32 v195, v202, v203
	global_store_dword v[192:193], v212, off offset:512
	ds_write_b64 v189, v[208:209] offset:3088
	ds_write_b64 v189, v[194:195] offset:36112
	v_pk_mul_f32 v[194:195], v[218:219], v[190:191] op_sel_hi:[1,0]
	v_pk_mul_f32 v[190:191], v[220:221], v[190:191] op_sel_hi:[1,0]
	v_pk_mul_f32 v[204:205], v[76:77], v[194:195]
	v_pk_mul_f32 v[202:203], v[78:79], v[190:191]
	v_cvt_pk_bf16_f32 v206, v204, v205
	v_mul_f32_e32 v204, 0x41000000, v204
	v_mul_f32_e32 v205, 0x41000000, v205
	v_cvt_pk_fp8_f32 v201, v204, v205
	v_cvt_pk_bf16_f32 v207, v202, v203
	v_mul_f32_e32 v202, 0x41000000, v202
	v_mul_f32_e32 v203, 0x41000000, v203
	v_lshlrev_b32_e32 v208, 16, v207
	v_and_b32_e32 v209, 0xffff0000, v207
	v_cvt_pk_fp8_f32 v201, v202, v203 op_sel:[0,0,1]
	v_lshlrev_b32_e32 v210, 16, v206
	v_and_b32_e32 v211, 0xffff0000, v206
	v_xor_b32_e32 v209, 0x80000000, v209
	v_xor_b32_e32 v208, 0x80000000, v208
	v_pk_fma_f32 v[190:191], v[78:79], v[190:191], v[208:209]
	v_xor_b32_e32 v209, 0x80000000, v211
	v_xor_b32_e32 v208, 0x80000000, v210
	v_pk_fma_f32 v[194:195], v[76:77], v[194:195], v[208:209]
	s_nop 0
	v_cvt_pk_bf16_f32 v194, v194, v195
	v_cvt_pk_bf16_f32 v195, v190, v191
	global_store_dword v[192:193], v201, off offset:768
	ds_write_b64 v189, v[206:207] offset:3600
	ds_write_b64 v189, v[194:195] offset:36624
	v_and_b32_e32 v189, 15, v188
	v_and_b32_e32 v191, -16, v188
	v_mul_u32_u24_e32 v190, 0x810, v189
	v_add_u32_e32 v191, s34, v191
	v_add3_u32 v194, v191, v190, 0
	s_waitcnt lgkmcnt(0)
	s_barrier
; #define LAS __attribute__((address_space(3)))
; __device__ __forceinline__ void r_tile(const Ctx& c, const RRows& r, int tokw  , int slot0  , const f32x4 (&gq)[4], const bf16x8 (&bh)[4][2], const bf16x8 (&bl)[4][2], float bias) {
;     ...
;     f32x4 acc[2], ahh[2], ahl[2], alh[2];
; #pragma unroll
;     for (int eb = 0; eb < 2; ++eb) { ahh[eb] = (f32x4){0.f, 0.f, 0.f, 0.f}; ahl[eb] = ahh[eb]; alh[eb] = ahh[eb]; }
; #pragma unroll
;     for (int s = 0; s < 4; ++s) { const int off = (lane & 15) * R_AP + (128 * wave + 32 * s + 8 * (lane >> 4)) * 2;
;         const bf16x8 ah = *(const LAS bf16x8*)(L + R_AH + off), al = *(const LAS bf16x8*)(L + R_AL + off);
; #pragma unroll
;         for (int eb = 0; eb < 2; ++eb) { ahh[eb] = __builtin_amdgcn_mfma_f32_16x16x32_bf16(ah, bh[s][eb], ahh[eb], 0, 0, 0); ahl[eb] = __builtin_amdgcn_mfma_f32_16x16x32_bf16(ah, bl[s][eb], ahl[eb], 0, 0, 0);
;             alh[eb] = __builtin_amdgcn_mfma_f32_16x16x32_bf16(al, bh[s][eb], alh[eb], 0, 0, 0); } }
; #pragma unroll
;     for (int eb = 0; eb < 2; ++eb) acc[eb] = ahh[eb] + (ahl[eb] + alh[eb]);
;     LAS float* part = (LAS float*)(L + R_PART);
; #pragma unroll
;     for (int eb = 0; eb < 2; ++eb)
; #pragma unroll
;         for (int q = 0; q < 4; ++q) part[(wave * 16 + (lane >> 4) * 4 + q) * 32 + 16 * eb + (lane & 15)] = acc[eb][q];
;     __syncthreads();
;     const int tl = 2 * wave + (lane >> 5), e = lane & 31; float lg = bias;
; #pragma unroll
;     for (int w = 0; w < 8; ++w) lg += part[(w * 16 + tl) * 32 + e];
;     float cur = lg, tv0 = 0.f, tv1 = 0.f, tv2 = 0.f, tv3 = 0.f; int ti0 = 0, ti1 = 0, ti2 = 0, ti3 = 0;
; #pragma unroll
;     for (int k = 0; k < TOPK; ++k) {
;         const float bv = allmax32(cur); const unsigned long long mk = __builtin_amdgcn_ballot_w64(cur == bv);
;         const int i0 = (int)__builtin_ctzll(mk | (1ull << 32)), i1 = (int)__builtin_ctzll((mk >> 32) | (1ull << 32)); const int bi = (lane >> 5) ? i1 : i0;
;         if (k == 0) { tv0 = bv; ti0 = bi; } if (k == 1) { tv1 = bv; ti1 = bi; } if (k == 2) { tv2 = bv; ti2 = bi; } if (k == 3) { tv3 = bv; ti3 = bi; }
;         if (e == bi) cur = -INFINITY; }
	ds_read_b128 v[190:193], v194
	ds_read_b128 v[202:205], v194 offset:64
	ds_read_b128 v[214:217], v194 offset:33024
	ds_read_b128 v[218:221], v194 offset:33088
	s_waitcnt lgkmcnt(3)
	v_mfma_f32_16x16x32_bf16 v[206:209], v[190:193], v[0:3], 0
	v_lshlrev_b32_e32 v201, 5, v188
	v_and_b32_e32 v201, 0xfffffe00, v201
	v_lshlrev_b32_e32 v189, 2, v189
	v_mfma_f32_16x16x32_bf16 v[210:213], v[190:193], v[4:7], 0
	v_add_u32_e32 v201, s35, v201
	v_add3_u32 v189, s49, v189, v201
	s_waitcnt lgkmcnt(1)
	v_mfma_f32_16x16x32_bf16 v[222:225], v[214:217], v[0:3], 0
	v_mfma_f32_16x16x32_bf16 v[226:229], v[190:193], v[8:11], 0
	v_mfma_f32_16x16x32_bf16 v[190:193], v[190:193], v[12:15], 0
	v_mfma_f32_16x16x32_bf16 v[214:217], v[214:217], v[8:11], 0
	v_mfma_f32_16x16x32_bf16 v[206:209], v[202:205], v[16:19], v[206:209]
	v_mfma_f32_16x16x32_bf16 v[210:213], v[202:205], v[20:23], v[210:213]
	s_waitcnt lgkmcnt(0)
	v_mfma_f32_16x16x32_bf16 v[222:225], v[218:221], v[16:19], v[222:225]
	v_mfma_f32_16x16x32_bf16 v[226:229], v[202:205], v[24:27], v[226:229]
	v_mfma_f32_16x16x32_bf16 v[190:193], v[202:205], v[28:31], v[190:193]
	v_mfma_f32_16x16x32_bf16 v[202:205], v[218:221], v[24:27], v[214:217]
	s_nop 2
	ds_read_b128 v[214:217], v194 offset:128
	ds_read_b128 v[218:221], v194 offset:192
	ds_read_b128 v[230:233], v194 offset:33152
	ds_read_b128 v[234:237], v194 offset:33216
	s_waitcnt lgkmcnt(3)
	v_mfma_f32_16x16x32_bf16 v[210:213], v[214:217], v[36:39], v[210:213]
	s_waitcnt lgkmcnt(1)
	v_mfma_f32_16x16x32_bf16 v[222:225], v[230:233], v[32:35], v[222:225]
	v_mfma_f32_16x16x32_bf16 v[190:193], v[214:217], v[44:47], v[190:193]
	v_mfma_f32_16x16x32_bf16 v[202:205], v[230:233], v[40:43], v[202:205]
	v_mfma_f32_16x16x32_bf16 v[206:209], v[214:217], v[32:35], v[206:209]
	v_mfma_f32_16x16x32_bf16 v[226:229], v[214:217], v[40:43], v[226:229]
	v_mfma_f32_16x16x32_bf16 v[210:213], v[218:221], v[52:55], v[210:213]
	s_waitcnt lgkmcnt(0)
	v_mfma_f32_16x16x32_bf16 v[214:217], v[234:237], v[48:51], v[222:225]
	v_mfma_f32_16x16x32_bf16 v[190:193], v[218:221], v[60:63], v[190:193]
	v_mfma_f32_16x16x32_bf16 v[202:205], v[234:237], v[56:59], v[202:205]
	s_nop 5
	v_add_f32_e64 v210, v210, v214
	v_add_f32_e64 v211, v211, v215
	v_pk_add_f32 v[194:195], v[212:213], v[216:217]
	v_mfma_f32_16x16x32_bf16 v[206:209], v[218:221], v[48:51], v[206:209]
	v_mfma_f32_16x16x32_bf16 v[222:225], v[218:221], v[56:59], v[226:229]
	v_add_f32_e64 v190, v190, v202
	v_add_f32_e64 v191, v191, v203
	s_nop 4
	v_pk_add_f32 v[206:207], v[206:207], v[210:211]
	v_pk_add_f32 v[192:193], v[192:193], v[204:205]
	v_pk_add_f32 v[194:195], v[208:209], v[194:195]
	v_pk_add_f32 v[190:191], v[222:223], v[190:191]
	v_pk_add_f32 v[192:193], v[224:225], v[192:193]
	ds_write2_b32 v189, v206, v190 offset1:16
	ds_write2_b32 v189, v207, v191 offset0:32 offset1:48
	ds_write2_b32 v189, v194, v192 offset0:64 offset1:80
	ds_write2_b32 v189, v195, v193 offset0:96 offset1:112
	v_ashrrev_i32_e32 v189, 5, v188
	v_and_b32_e32 v191, 31, v188
	v_add_lshl_u32 v192, v189, s2, 7
	v_lshlrev_b32_e32 v190, 2, v191
	v_add3_u32 v201, s49, v192, v190
	s_waitcnt lgkmcnt(0)
	s_barrier
	ds_read2st64_b32 v[192:193], v201 offset1:8
	ds_read2st64_b32 v[194:195], v201 offset0:16 offset1:24
	ds_read2st64_b32 v[202:203], v201 offset0:32 offset1:40
	s_waitcnt lgkmcnt(2)
	v_add_f32_e32 v192, v144, v192
	v_add_f32_e32 v204, v192, v193
	ds_read2st64_b32 v[192:193], v201 offset0:48 offset1:56
	s_waitcnt lgkmcnt(2)
	v_add_f32_e32 v194, v204, v194
	v_add_f32_e32 v194, v194, v195
	s_waitcnt lgkmcnt(1)
	v_add_f32_e32 v194, v194, v202
	v_add_f32_e32 v194, v194, v203
	s_waitcnt lgkmcnt(0)
	v_add_f32_e32 v192, v194, v192
	v_add_f32_e32 v193, v192, v193
	s_nop 1
	v_mov_b32_dpp v192, v193 quad_perm:[1,0,3,2] row_mask:0xf bank_mask:0xf bound_ctrl:1
	v_max_f32_e32 v192, v192, v192
	v_max_f32_e32 v192, v193, v192
	s_nop 1
	v_mov_b32_dpp v194, v192 quad_perm:[2,3,0,1] row_mask:0xf bank_mask:0xf bound_ctrl:1
	v_max_f32_e32 v194, v194, v194
	v_max_f32_e32 v192, v192, v194
	s_nop 1
	v_mov_b32_dpp v194, v192 row_half_mirror row_mask:0xf bank_mask:0xf bound_ctrl:1
	v_max_f32_e32 v194, v194, v194
	v_max_f32_e32 v192, v192, v194
	s_nop 1
	v_mov_b32_dpp v194, v192 row_mirror row_mask:0xf bank_mask:0xf bound_ctrl:1
	v_max_f32_e32 v194, v194, v194
	v_max_f32_e32 v192, v192, v194
	v_mov_b32_e32 v194, v192
	s_nop 1
	v_permlane16_swap_b32_e32 v192, v194
	v_max_f32_e32 v194, v194, v194
	v_max_f32_e32 v192, v192, v192
	v_max_f32_e32 v192, v192, v194
	v_cmp_eq_f32_e64 s[6:7], v193, v192
	s_or_b32 s9, s7, 1
	s_mov_b32 s8, s6
	s_mov_b32 s12, s7
	s_ff1_i32_b64 s6, s[8:9]
	s_ff1_i32_b64 s7, s[12:13]
	v_mov_b32_e32 v194, s7
	v_mov_b32_e32 v195, s6
	v_cndmask_b32_e32 v188, v194, v195, vcc
	v_cmp_ne_u32_e64 s[6:7], v191, v188
	s_nop 1
	v_cndmask_b32_e64 v195, v200, v193, s[6:7]
	s_nop 1
	v_mov_b32_dpp v193, v195 quad_perm:[1,0,3,2] row_mask:0xf bank_mask:0xf bound_ctrl:1
	v_max_f32_e32 v193, v193, v193
	v_max_f32_e32 v193, v195, v193
	s_nop 1
	v_mov_b32_dpp v194, v193 quad_perm:[2,3,0,1] row_mask:0xf bank_mask:0xf bound_ctrl:1
	v_max_f32_e32 v194, v194, v194
	v_max_f32_e32 v193, v193, v194
	s_nop 1
	v_mov_b32_dpp v194, v193 row_half_mirror row_mask:0xf bank_mask:0xf bound_ctrl:1
	v_max_f32_e32 v194, v194, v194
	v_max_f32_e32 v193, v193, v194
	s_nop 1
	v_mov_b32_dpp v194, v193 row_mirror row_mask:0xf bank_mask:0xf bound_ctrl:1
	v_max_f32_e32 v194, v194, v194
	v_max_f32_e32 v193, v193, v194
	v_mov_b32_e32 v194, v193
	s_nop 1
	v_permlane16_swap_b32_e32 v193, v194
	v_max_f32_e32 v194, v194, v194
	v_max_f32_e32 v193, v193, v193
; #define LAS __attribute__((address_space(3)))
; __device__ __forceinline__ void r_tile(const Ctx& c, const RRows& r, int tokw  , int slot0  , const f32x4 (&gq)[4], const bf16x8 (&bh)[4][2], const bf16x8 (&bl)[4][2], float bias) {
;     ...
;     for (int k = 0; k < TOPK; ++k) {
;         const float bv = allmax32(cur); const unsigned long long mk = __builtin_amdgcn_ballot_w64(cur == bv);
;         const int i0 = (int)__builtin_ctzll(mk | (1ull << 32)), i1 = (int)__builtin_ctzll((mk >> 32) | (1ull << 32)); const int bi = (lane >> 5) ? i1 : i0;
;         if (k == 0) { tv0 = bv; ti0 = bi; } if (k == 1) { tv1 = bv; ti1 = bi; } if (k == 2) { tv2 = bv; ti2 = bi; } if (k == 3) { tv3 = bv; ti3 = bi; }
;         if (e == bi) cur = -INFINITY; }
;     const float e1 = __expf(tv1 - tv0), e2 = __expf(tv2 - tv0), e3 = __expf(tv3 - tv0); const float inv = 1.0f / (1.0f + e1 + e2 + e3);
;     if (e < 4) { const int sel = e == 0 ? ti0 : e == 1 ? ti1 : e == 2 ? ti2 : ti3; const float gg = (e == 0 ? 1.0f : e == 1 ? e1 : e == 2 ? e2 : e3) * inv;
;         LAS int* lsel = (LAS int*)(L + R_SEL); LAS float* lgate = (LAS float*)(L + R_GATE); LAS int* lhist = (LAS int*)(L + R_HIST);
;         lsel[(slot0 + tl) * 4 + e] = sel; lgate[(slot0 + tl) * 4 + e] = gg; atomicAdd((int*)(lhist + sel), 1); }
; __device__ __forceinline__ void ph4(const Ctx& c) {
;     ...
;             if (tile + 2 < 16) r_load(p, ra, t0 + 16 * (tile + 2) + 2 * wave, lane);
	v_max_f32_e32 v194, v193, v194
	v_cmp_eq_f32_e64 s[6:7], v195, v194
	s_or_b32 s9, s7, 1
	s_mov_b32 s8, s6
	s_mov_b32 s12, s7
	s_ff1_i32_b64 s6, s[8:9]
	s_ff1_i32_b64 s7, s[12:13]
	v_mov_b32_e32 v193, s7
	v_mov_b32_e32 v201, s6
	v_cndmask_b32_e32 v193, v193, v201, vcc
	v_cmp_ne_u32_e64 s[6:7], v191, v193
	s_nop 1
	v_cndmask_b32_e64 v202, v200, v195, s[6:7]
	s_nop 1
	v_mov_b32_dpp v195, v202 quad_perm:[1,0,3,2] row_mask:0xf bank_mask:0xf bound_ctrl:1
	v_max_f32_e32 v195, v195, v195
	v_max_f32_e32 v195, v202, v195
	s_nop 1
	v_mov_b32_dpp v201, v195 quad_perm:[2,3,0,1] row_mask:0xf bank_mask:0xf bound_ctrl:1
	v_max_f32_e32 v201, v201, v201
	v_max_f32_e32 v195, v195, v201
	s_nop 1
	v_mov_b32_dpp v201, v195 row_half_mirror row_mask:0xf bank_mask:0xf bound_ctrl:1
	v_max_f32_e32 v201, v201, v201
	v_max_f32_e32 v195, v195, v201
	s_nop 1
	v_mov_b32_dpp v201, v195 row_mirror row_mask:0xf bank_mask:0xf bound_ctrl:1
	v_max_f32_e32 v201, v201, v201
	v_max_f32_e32 v195, v195, v201
	v_mov_b32_e32 v201, v195
	s_nop 1
	v_permlane16_swap_b32_e32 v195, v201
	v_max_f32_e32 v201, v201, v201
	v_max_f32_e32 v195, v195, v195
	v_max_f32_e32 v201, v195, v201
	v_cmp_eq_f32_e64 s[6:7], v202, v201
	s_or_b32 s9, s7, 1
	s_mov_b32 s8, s6
	s_mov_b32 s12, s7
	s_ff1_i32_b64 s6, s[8:9]
	s_ff1_i32_b64 s7, s[12:13]
	v_mov_b32_e32 v195, s7
	v_mov_b32_e32 v203, s6
	v_cndmask_b32_e32 v195, v195, v203, vcc
	v_cmp_ne_u32_e64 s[6:7], v191, v195
	s_nop 1
	v_cndmask_b32_e64 v203, v200, v202, s[6:7]
	v_cmp_gt_u32_e64 s[6:7], 4, v191
	s_nop 0
	v_mov_b32_dpp v202, v203 quad_perm:[1,0,3,2] row_mask:0xf bank_mask:0xf bound_ctrl:1
	v_max_f32_e32 v202, v202, v202
	v_max_f32_e32 v202, v203, v202
	s_nop 1
	v_mov_b32_dpp v204, v202 quad_perm:[2,3,0,1] row_mask:0xf bank_mask:0xf bound_ctrl:1
	v_max_f32_e32 v204, v204, v204
	v_max_f32_e32 v202, v202, v204
	s_nop 1
	v_mov_b32_dpp v204, v202 row_half_mirror row_mask:0xf bank_mask:0xf bound_ctrl:1
	v_max_f32_e32 v204, v204, v204
	v_max_f32_e32 v202, v202, v204
	s_nop 1
	v_mov_b32_dpp v204, v202 row_mirror row_mask:0xf bank_mask:0xf bound_ctrl:1
	v_max_f32_e32 v204, v204, v204
	v_max_f32_e32 v202, v202, v204
	v_mov_b32_e32 v204, v202
	s_nop 1
	v_permlane16_swap_b32_e32 v202, v204
	v_max_f32_e32 v204, v204, v204
	v_max_f32_e32 v202, v202, v202
	v_max_f32_e32 v202, v202, v204
	v_cmp_eq_f32_e64 s[8:9], v203, v202
	s_and_saveexec_b64 s[42:43], s[6:7]
	s_cbranch_execz .LBB7_696
	v_sub_f32_e32 v194, v194, v192
	v_mul_f32_e32 v194, 0x3fb8aa3b, v194
	v_sub_f32_e32 v201, v201, v192
	v_exp_f32_e32 v194, v194
	v_mul_f32_e32 v201, 0x3fb8aa3b, v201
	v_sub_f32_e32 v192, v202, v192
	v_exp_f32_e32 v201, v201
	v_mul_f32_e32 v192, 0x3fb8aa3b, v192
	v_exp_f32_e32 v192, v192
	v_add_f32_e32 v202, 1.0, v194
	v_add_f32_e32 v202, v202, v201
	s_or_b32 s7, s9, 1
	s_mov_b32 s6, s8
	v_add_f32_e32 v202, v202, v192
	s_ff1_i32_b64 s8, s[6:7]
	v_div_scale_f32 v203, s[6:7], v202, v202, 1.0
	v_rcp_f32_e32 v204, v203
	s_mov_b32 s12, s9
	s_ff1_i32_b64 s9, s[12:13]
	v_mov_b32_e32 v205, s9
	v_mov_b32_e32 v206, s8
	v_cndmask_b32_e32 v205, v205, v206, vcc
	v_fma_f32 v206, -v203, v204, 1.0
	v_fmac_f32_e32 v204, v206, v204
	v_div_scale_f32 v206, vcc, 1.0, v202, 1.0
	v_mul_f32_e32 v207, v206, v204
	v_fma_f32 v208, -v203, v207, v206
	v_fmac_f32_e32 v207, v208, v204
	v_fma_f32 v203, -v203, v207, v206
	v_div_fmas_f32 v203, v203, v204, v207
	v_cmp_eq_u32_e32 vcc, 2, v191
	v_add_u32_e32 v189, s53, v189
	v_cmp_eq_u32_e64 s[6:7], 1, v191
	v_cndmask_b32_e32 v195, v205, v195, vcc
	v_cmp_eq_u32_e64 s[8:9], 0, v191
	v_cndmask_b32_e32 v191, v192, v201, vcc
	v_lshl_or_b32 v189, v189, 4, v190
	v_cndmask_b32_e64 v193, v195, v193, s[6:7]
	v_cndmask_b32_e64 v191, v191, v194, s[6:7]
	v_add_u32_e32 v189, 0, v189
	v_div_fixup_f32 v202, v203, v202, 1.0
	v_cndmask_b32_e64 v188, v193, v188, s[8:9]
	v_cndmask_b32_e64 v191, v191, 1.0, s[8:9]
	v_add_u32_e32 v190, 0x14300, v189
	v_mul_f32_e32 v191, v202, v191
	ds_write_b32 v190, v188
	v_add_u32_e32 v189, 0x15300, v189
	v_lshl_add_u32 v188, v188, 2, 0
	ds_write_b32 v189, v191
	v_add_u32_e32 v188, 0x14200, v188
	ds_add_u32 v188, v199
.LBB7_696:
	s_or_b64 exec, exec, s[42:43]
	s_cmp_gt_u32 s52, 13
	s_cselect_b64 s[42:43], -1, 0
	s_and_b64 vcc, exec, s[42:43]
	s_cbranch_vccnz .LBB7_698
	s_add_i32 s6, s40, 32
	s_ashr_i32 s7, s6, 31
	s_lshl_b64 s[6:7], s[6:7], 12
	v_lshl_add_u64 v[92:93], v[150:151], 0, s[6:7]
	v_lshl_add_u64 v[96:97], v[152:153], 0, s[6:7]
	s_add_i32 s6, s40, 33
	s_ashr_i32 s7, s6, 31
	s_lshl_b64 s[6:7], s[6:7], 12
	v_lshl_add_u64 v[108:109], v[150:151], 0, s[6:7]
	v_lshl_add_u64 v[170:171], v[152:153], 0, s[6:7]
	global_load_dwordx4 v[80:83], v[92:93], off nt
	global_load_dwordx4 v[84:87], v[92:93], off offset:1024 nt
	global_load_dwordx4 v[88:91], v[92:93], off offset:2048 nt
	s_nop 0
	global_load_dwordx4 v[92:95], v[92:93], off offset:3072 nt
	s_nop 0
	global_load_dwordx2 v[156:157], v[96:97], off nt
	global_load_dwordx2 v[158:159], v[96:97], off offset:512 nt
	global_load_dwordx2 v[160:161], v[96:97], off offset:1024 nt
	global_load_dwordx2 v[162:163], v[96:97], off offset:1536 nt
	s_nop 0
	global_load_dwordx4 v[96:99], v[108:109], off nt
	global_load_dwordx4 v[100:103], v[108:109], off offset:1024 nt
	global_load_dwordx4 v[104:107], v[108:109], off offset:2048 nt
	s_nop 0
	global_load_dwordx4 v[108:111], v[108:109], off offset:3072 nt
	s_nop 0
	global_load_dwordx2 v[164:165], v[170:171], off nt
	global_load_dwordx2 v[166:167], v[170:171], off offset:512 nt
	global_load_dwordx2 v[168:169], v[170:171], off offset:1024 nt
	s_nop 0
	global_load_dwordx2 v[170:171], v[170:171], off offset:1536 nt

; __device__ __forceinline__ int fresh_lane() { unsigned z = 0u; asm volatile("" : "+v"(z)); return (int)__builtin_amdgcn_mbcnt_hi(~0u, __builtin_amdgcn_mbcnt_lo(~0u, z)); }
; __device__ __forceinline__ void p7_load(const P& p, int t, int lane, R7& r) {
;     const unsigned char* row = (const unsigned char*)p.out + (size_t)t * 4096; const unsigned char* ys = p.ws + WS_YS3;
;     r.h0 = *(const u32x4*)(row + 32 * lane); r.h1v = *(const u32x4*)(row + 32 * lane + 16); r.y[0] = *(const u32x4*)(row + 2048 + 16 * lane);
; #pragma unroll
;     for (int k = 0; k < 3; ++k) r.y[k + 1] = *(const u32x4*)(ys + ((size_t)t * 3 + k) * DM + 16 * lane);
; }
; __device__ __forceinline__ void ph7(const Ctx& c) {
;     const P& p = *c.pp; const int gw = c.bx * NWAVES + c.wave, NGW = c.G * NWAVES, lane = fresh_lane();
;     R7 a, b; int t = gw;
;     if (t < T) p7_load(p, t, lane, a);
.LBB7_980:
	v_readlane_b32 s4, v254, 2
	v_readlane_b32 s5, v254, 3
	s_cmp_gt_i32 s4, 7
	s_cselect_b64 s[4:5], -1, 0
	s_xor_b64 s[0:1], s[0:1], -1
	s_or_b64 s[0:1], s[4:5], s[0:1]
	s_and_b64 vcc, exec, s[0:1]
	s_cbranch_vccnz .LBB7_990
	s_lshl_b32 s0, s92, 3
	s_add_i32 s0, s94, s0
	s_waitcnt vmcnt(0)
	v_mov_b32_e32 v0, 0
	s_cmp_gt_i32 s0, 0xffff
	s_cbranch_scc1 .LBB7_990
	v_mbcnt_lo_u32_b32 v0, -1, v0
	s_ashr_i32 s1, s0, 31
	s_lshl_b32 s8, s3, 3
	v_mbcnt_hi_u32_b32 v8, -1, v0
	s_lshl_b64 s[4:5], s[0:1], 12
	s_add_u32 s4, s28, s4
	v_lshlrev_b32_e32 v12, 5, v8
	v_lshlrev_b32_e32 v14, 4, v8
	v_ashrrev_i32_e32 v9, 31, v8
	s_addc_u32 s5, s29, s5
	v_ashrrev_i32_e32 v13, 31, v12
	v_ashrrev_i32_e32 v15, 31, v14
	v_lshlrev_b64 v[8:9], 4, v[8:9]
	v_lshl_add_u64 v[10:11], s[4:5], 0, v[12:13]
	v_sub_co_u32_e32 v48, vcc, 0, v8
	s_waitcnt lgkmcnt(0)
	v_lshl_add_u64 v[16:17], s[30:31], 0, v[14:15]
	s_mov_b64 s[4:5], 0x27000000
	v_subb_co_u32_e32 v49, vcc, 0, v9, vcc
	v_lshl_add_u64 v[50:51], v[16:17], 0, s[4:5]
	v_mov_b32_e32 v56, 0xc00
	v_lshl_add_u64 v[8:9], v[10:11], 0, v[48:49]
	v_mad_i64_i32 v[16:17], s[4:5], s0, v56, v[50:51]
	global_load_dwordx4 v[0:3], v[10:11], off offset:16 nt
	global_load_dwordx4 v[4:7], v[10:11], off nt
	v_lshl_add_u64 v[52:53], v[14:15], 2, s[28:29]
	global_load_dwordx4 v[8:11], v[8:9], off offset:2048 nt
	s_nop 0
	global_load_dwordx4 v[20:23], v[16:17], off nt
	global_load_dwordx4 v[24:27], v[16:17], off offset:1024 nt
	global_load_dwordx4 v[28:31], v[16:17], off offset:2048 nt
	v_lshl_add_u64 v[54:55], s[28:29], 0, v[12:13]
	s_lshl_b32 s3, s3, 4
	s_mov_b32 s2, 0x3c800000
	s_branch .LBB7_985

; __device__ __forceinline__ void p7_finish(const P& p, int t, int lane, const R7& r) {
;     float o[16];
; #pragma unroll
;     for (int q = 0; q < 4; ++q) { o[2 * q] = __uint_as_float(r.h0[q] << 16); o[2 * q + 1] = __uint_as_float(r.h0[q] & 0xffff0000u); o[8 + 2 * q] = __uint_as_float(r.h1v[q] << 16); o[8 + 2 * q + 1] = __uint_as_float(r.h1v[q] & 0xffff0000u); }
; #pragma unroll
;     for (int q = 0; q < 4; ++q) { float s0 = 0.f, s1 = 0.f, s2 = 0.f, s3 = 0.f;
; #pragma unroll
;         for (int k = 0; k < 4; ++k) { const auto lo = __builtin_amdgcn_cvt_pk_f32_fp8((int)r.y[k][q], false), hi = __builtin_amdgcn_cvt_pk_f32_fp8((int)r.y[k][q], true); s0 += lo[0]; s1 += lo[1]; s2 += hi[0]; s3 += hi[1]; }
;         o[4 * q] += s0 * (1.0f / 64.0f); o[4 * q + 1] += s1 * (1.0f / 64.0f); o[4 * q + 2] += s2 * (1.0f / 64.0f); o[4 * q + 3] += s3 * (1.0f / 64.0f); }
;     asm volatile("" ::: "memory");
;     f32x4* dst = (f32x4*)(p.out + (size_t)t * DM + 16 * lane);
; #pragma unroll
;     for (int q = 0; q < 4; ++q) dst[q] = (f32x4){o[4 * q], o[4 * q + 1], o[4 * q + 2], o[4 * q + 3]};
; }
; __device__ __forceinline__ void ph7(const Ctx& c) {
;     ...
;     while (t < T) {
;         const int t1 = t + NGW; if (t1 < T) p7_load(p, t1, lane, b);
;         p7_finish(p, t, lane, a);
;         if (t1 >= T) break;
;         const int t2 = t1 + NGW; if (t2 < T) p7_load(p, t2, lane, a);
;         p7_finish(p, t1, lane, b);
;         t = t2;
;     }
.LBB7_985:
	s_add_i32 s4, s0, s8
	s_cmp_lt_i32 s4, 0x10000
	s_cselect_b64 s[6:7], -1, 0
	s_cmp_gt_i32 s4, 0xffff
	s_cbranch_scc1 .LBB7_987
	s_ashr_i32 s5, s4, 31
	s_lshl_b64 s[10:11], s[4:5], 12
	v_lshl_add_u64 v[32:33], v[54:55], 0, s[10:11]
	global_load_dwordx4 v[12:15], v[32:33], off offset:16 nt
	global_load_dwordx4 v[16:19], v[32:33], off nt
	v_lshl_add_u64 v[32:33], v[32:33], 0, v[48:49]
	v_mad_i64_i32 v[58:59], s[10:11], s4, v56, v[50:51]
	global_load_dwordx4 v[32:35], v[32:33], off offset:2048 nt
	s_nop 0
	global_load_dwordx4 v[36:39], v[58:59], off nt
	global_load_dwordx4 v[40:43], v[58:59], off offset:1024 nt
	global_load_dwordx4 v[44:47], v[58:59], off offset:2048 nt
.LBB7_987:
	s_waitcnt vmcnt(3)
	v_cvt_pk_f32_fp8_sdwa v[60:61], v8 src0_sel:WORD_1
	s_waitcnt vmcnt(2)
	v_cvt_pk_f32_fp8_sdwa v[64:65], v20 src0_sel:WORD_1
	v_cvt_pk_f32_fp8_e32 v[58:59], v8
	s_waitcnt vmcnt(1)
	v_cvt_pk_f32_fp8_sdwa v[68:69], v24 src0_sel:WORD_1
	v_cvt_pk_f32_fp8_e32 v[62:63], v20
	s_waitcnt vmcnt(0)
	v_cvt_pk_f32_fp8_sdwa v[72:73], v28 src0_sel:WORD_1
	v_pk_add_f32 v[60:61], v[60:61], 0 op_sel_hi:[1,0]
	v_cvt_pk_f32_fp8_e32 v[66:67], v24
	v_pk_add_f32 v[60:61], v[60:61], v[64:65]
	v_pk_add_f32 v[58:59], v[58:59], 0 op_sel_hi:[1,0]
	v_pk_add_f32 v[60:61], v[60:61], v[68:69]
	v_cvt_pk_f32_fp8_sdwa v[64:65], v9 src0_sel:WORD_1
	v_cvt_pk_f32_fp8_e32 v[70:71], v28
	v_pk_add_f32 v[58:59], v[58:59], v[62:63]
	v_lshlrev_b32_e32 v62, 16, v5
	v_and_b32_e32 v63, 0xffff0000, v5
	v_pk_add_f32 v[60:61], v[60:61], v[72:73]
	v_cvt_pk_f32_fp8_sdwa v[68:69], v21 src0_sel:WORD_1
	v_pk_fma_f32 v[60:61], v[60:61], s[2:3], v[62:63] op_sel_hi:[1,0,1]
	v_cvt_pk_f32_fp8_e32 v[62:63], v9
	v_cvt_pk_f32_fp8_sdwa v[72:73], v25 src0_sel:WORD_1
	v_pk_add_f32 v[58:59], v[58:59], v[66:67]
	v_cvt_pk_f32_fp8_e32 v[66:67], v21
	v_cvt_pk_f32_fp8_sdwa v[76:77], v29 src0_sel:WORD_1
	v_pk_add_f32 v[64:65], v[64:65], 0 op_sel_hi:[1,0]
	v_pk_add_f32 v[58:59], v[58:59], v[70:71]
	v_cvt_pk_f32_fp8_e32 v[70:71], v25
	v_pk_add_f32 v[64:65], v[64:65], v[68:69]
	v_lshlrev_b32_e32 v74, 16, v4
	v_and_b32_e32 v75, 0xffff0000, v4
	v_pk_add_f32 v[62:63], v[62:63], 0 op_sel_hi:[1,0]
	v_pk_add_f32 v[64:65], v[64:65], v[72:73]
	v_cvt_pk_f32_fp8_sdwa v[68:69], v10 src0_sel:WORD_1
	v_pk_fma_f32 v[58:59], v[58:59], s[2:3], v[74:75] op_sel_hi:[1,0,1]
	v_cvt_pk_f32_fp8_e32 v[74:75], v29
	v_pk_add_f32 v[62:63], v[62:63], v[66:67]
	v_lshlrev_b32_e32 v66, 16, v7
	v_and_b32_e32 v67, 0xffff0000, v7
	v_pk_add_f32 v[64:65], v[64:65], v[76:77]
	v_cvt_pk_f32_fp8_sdwa v[72:73], v22 src0_sel:WORD_1
	v_pk_fma_f32 v[64:65], v[64:65], s[2:3], v[66:67] op_sel_hi:[1,0,1]
	v_cvt_pk_f32_fp8_e32 v[66:67], v10
	v_cvt_pk_f32_fp8_sdwa v[76:77], v26 src0_sel:WORD_1
	v_pk_add_f32 v[62:63], v[62:63], v[70:71]
	v_cvt_pk_f32_fp8_e32 v[70:71], v22
	v_cvt_pk_f32_fp8_sdwa v[80:81], v30 src0_sel:WORD_1
	v_pk_add_f32 v[68:69], v[68:69], 0 op_sel_hi:[1,0]
	v_lshlrev_b32_e32 v78, 16, v6
	v_and_b32_e32 v79, 0xffff0000, v6
	v_pk_add_f32 v[62:63], v[62:63], v[74:75]
	v_cvt_pk_f32_fp8_e32 v[74:75], v26
	v_pk_add_f32 v[68:69], v[68:69], v[72:73]
	v_pk_fma_f32 v[62:63], v[62:63], s[2:3], v[78:79] op_sel_hi:[1,0,1]
	v_cvt_pk_f32_fp8_e32 v[78:79], v30
	v_pk_add_f32 v[66:67], v[66:67], 0 op_sel_hi:[1,0]
	v_pk_add_f32 v[68:69], v[68:69], v[76:77]
	v_pk_add_f32 v[66:67], v[66:67], v[70:71]
	v_lshlrev_b32_e32 v70, 16, v1
	v_and_b32_e32 v71, 0xffff0000, v1
	v_pk_add_f32 v[68:69], v[68:69], v[80:81]
	v_cvt_pk_f32_fp8_sdwa v[72:73], v11 src0_sel:WORD_1
	v_pk_fma_f32 v[68:69], v[68:69], s[2:3], v[70:71] op_sel_hi:[1,0,1]
	v_cvt_pk_f32_fp8_e32 v[70:71], v11
	v_cvt_pk_f32_fp8_sdwa v[76:77], v23 src0_sel:WORD_1
	v_pk_add_f32 v[66:67], v[66:67], v[74:75]
	v_cvt_pk_f32_fp8_e32 v[74:75], v23
	v_cvt_pk_f32_fp8_sdwa v[80:81], v27 src0_sel:WORD_1
	v_lshlrev_b32_e32 v82, 16, v0
	v_and_b32_e32 v83, 0xffff0000, v0
	v_pk_add_f32 v[66:67], v[66:67], v[78:79]
	v_cvt_pk_f32_fp8_e32 v[78:79], v27
	v_cvt_pk_f32_fp8_sdwa v[84:85], v31 src0_sel:WORD_1
	v_pk_fma_f32 v[66:67], v[66:67], s[2:3], v[82:83] op_sel_hi:[1,0,1]
	v_cvt_pk_f32_fp8_e32 v[82:83], v31
	v_pk_add_f32 v[72:73], v[72:73], 0 op_sel_hi:[1,0]
	v_pk_add_f32 v[70:71], v[70:71], 0 op_sel_hi:[1,0]
	v_pk_add_f32 v[72:73], v[72:73], v[76:77]
	v_pk_add_f32 v[70:71], v[70:71], v[74:75]
	v_pk_add_f32 v[72:73], v[72:73], v[80:81]
	s_ashr_i32 s1, s0, 31
	v_pk_add_f32 v[70:71], v[70:71], v[78:79]
	v_lshlrev_b32_e32 v74, 16, v3
	v_and_b32_e32 v75, 0xffff0000, v3
	v_pk_add_f32 v[72:73], v[72:73], v[84:85]
	s_lshl_b64 s[10:11], s[0:1], 12
	v_lshlrev_b32_e32 v86, 16, v2
	v_and_b32_e32 v87, 0xffff0000, v2
	v_pk_add_f32 v[70:71], v[70:71], v[82:83]
	v_pk_fma_f32 v[72:73], v[72:73], s[2:3], v[74:75] op_sel_hi:[1,0,1]
	v_lshl_add_u64 v[74:75], v[52:53], 0, s[10:11]
	s_andn2_b64 vcc, exec, s[6:7]
	s_mov_b64 s[6:7], -1
	v_pk_fma_f32 v[70:71], v[70:71], s[2:3], v[86:87] op_sel_hi:[1,0,1]
	global_store_dwordx4 v[74:75], v[58:61], off
	global_store_dwordx4 v[74:75], v[62:65], off offset:16
	global_store_dwordx4 v[74:75], v[66:69], off offset:32
	global_store_dwordx4 v[74:75], v[70:73], off offset:48
	s_cbranch_vccnz .LBB7_984
	s_add_i32 s0, s3, s0
	s_cmp_gt_i32 s0, 0xffff
	s_cbranch_scc1 .LBB7_983
	s_ashr_i32 s1, s0, 31
	s_lshl_b64 s[6:7], s[0:1], 12
	v_lshl_add_u64 v[8:9], v[54:55], 0, s[6:7]
	global_load_dwordx4 v[0:3], v[8:9], off offset:16 nt
	global_load_dwordx4 v[4:7], v[8:9], off nt
	v_lshl_add_u64 v[8:9], v[8:9], 0, v[48:49]
	v_mad_i64_i32 v[58:59], s[0:1], s0, v56, v[50:51]
	global_load_dwordx4 v[8:11], v[8:9], off offset:2048 nt
	s_nop 0
	global_load_dwordx4 v[20:23], v[58:59], off nt
	global_load_dwordx4 v[24:27], v[58:59], off offset:1024 nt
	global_load_dwordx4 v[28:31], v[58:59], off offset:2048 nt
	s_branch .LBB7_983
